# LayerNorm statistics: ds_bpermute round trips replaced by DPP adds and v_permlane16/32_swap (P5/P10 fused epilogues, P9 wave sums), same additions
# baseline (speedup 1.0000x reference)
.LBB0_701:
	s_lshl_b32 s3, s12, 8
	s_waitcnt vmcnt(0)
	s_barrier
	v_mbcnt_lo_u32_b32 v146, -1, 0
	v_mbcnt_hi_u32_b32 v146, -1, v146
	s_add_i32 s6, s3, s0
	v_and_b32_e32 v162, 15, v146
	s_lshl_b32 s5, s2, 5
	v_or_b32_e32 v168, s6, v162
	s_lshl_b32 s6, s4, 8
	v_ashrrev_i32_e32 v128, 2, v146
	s_or_b32 s5, s6, s5
	v_and_b32_e32 v128, -4, v128
	v_add_u32_e32 v160, s5, v128
	v_ashrrev_i32_e32 v161, 31, v160
	v_ashrrev_i32_e32 v169, 31, v168
	v_lshl_add_u64 v[170:171], v[160:161], 2, s[72:73]
	v_lshlrev_b64 v[128:129], 13, v[168:169]
	v_or_b32_e32 v148, 16, v168
	v_lshl_add_u64 v[140:141], v[170:171], 0, v[128:129]
	v_ashrrev_i32_e32 v149, 31, v148
	global_load_dwordx4 v[128:131], v[140:141], off
	global_load_dwordx4 v[132:135], v[140:141], off offset:64
	global_load_dwordx4 v[136:139], v[140:141], off offset:512
	global_load_dwordx4 v[142:145], v[140:141], off offset:576
	v_lshlrev_b64 v[148:149], 13, v[148:149]
	v_lshl_add_u64 v[164:165], v[170:171], 0, v[148:149]
	global_load_dwordx4 v[148:151], v[164:165], off
	global_load_dwordx4 v[152:155], v[164:165], off offset:64
	global_load_dwordx4 v[156:159], v[164:165], off offset:512
	s_nop 0
	global_load_dwordx4 v[164:167], v[164:165], off offset:576
	s_mov_b32 s14, 0x3f9837f0
	s_mov_b32 s6, 0x39000000
	v_or_b32_e32 v172, 32, v168
	v_ashrrev_i32_e32 v173, 31, v172
	v_lshlrev_b64 v[172:173], 13, v[172:173]
	v_lshl_add_u64 v[172:173], v[170:171], 0, v[172:173]
	s_mov_b32 s5, 0x100000
	s_mov_b64 s[16:17], 0x120000
	s_mov_b64 s[10:11], 0x100000
	s_lshl_b32 s2, s2, 3
	s_add_i32 s2, s2, 0
	s_waitcnt vmcnt(7)
	v_pk_mul_f32 v[130:131], v[130:131], s[14:15] op_sel_hi:[1,0]
	s_waitcnt vmcnt(6)
	v_pk_mul_f32 v[132:133], v[132:133], s[14:15] op_sel_hi:[1,0]
	v_pk_mul_f32 v[128:129], v[128:129], s[14:15] op_sel_hi:[1,0]
	s_waitcnt vmcnt(4)
	v_pk_mul_f32 v[142:143], v[142:143], s[14:15] op_sel_hi:[1,0]
	v_pk_fma_f32 v[132:133], v[120:121], s[6:7], v[132:133] op_sel_hi:[1,0,1]
	v_pk_fma_f32 v[120:121], v[104:105], s[6:7], v[142:143] op_sel_hi:[1,0,1]
	v_or_b32_e32 v142, 48, v168
	v_pk_mul_f32 v[134:135], v[134:135], s[14:15] op_sel_hi:[1,0]
	v_pk_mul_f32 v[174:175], v[138:139], s[14:15] op_sel_hi:[1,0]
	v_pk_mul_f32 v[176:177], v[136:137], s[14:15] op_sel_hi:[1,0]
	v_pk_mul_f32 v[144:145], v[144:145], s[14:15] op_sel_hi:[1,0]
	s_waitcnt vmcnt(3)
	v_pk_mul_f32 v[150:151], v[150:151], s[14:15] op_sel_hi:[1,0]
	v_pk_mul_f32 v[148:149], v[148:149], s[14:15] op_sel_hi:[1,0]
	s_waitcnt vmcnt(2)
	v_pk_mul_f32 v[154:155], v[154:155], s[14:15] op_sel_hi:[1,0]
	v_pk_mul_f32 v[152:153], v[152:153], s[14:15] op_sel_hi:[1,0]
	s_waitcnt vmcnt(1)
	v_pk_mul_f32 v[158:159], v[158:159], s[14:15] op_sel_hi:[1,0]
	v_pk_mul_f32 v[156:157], v[156:157], s[14:15] op_sel_hi:[1,0]
	s_waitcnt vmcnt(0)
	v_pk_mul_f32 v[166:167], v[166:167], s[14:15] op_sel_hi:[1,0]
	v_pk_mul_f32 v[164:165], v[164:165], s[14:15] op_sel_hi:[1,0]
	v_ashrrev_i32_e32 v143, 31, v142
	v_pk_fma_f32 v[138:139], v[126:127], s[6:7], v[130:131] op_sel_hi:[1,0,1]
	v_pk_fma_f32 v[136:137], v[124:125], s[6:7], v[128:129] op_sel_hi:[1,0,1]
	v_pk_fma_f32 v[134:135], v[122:123], s[6:7], v[134:135] op_sel_hi:[1,0,1]
	v_pk_fma_f32 v[130:131], v[110:111], s[6:7], v[174:175] op_sel_hi:[1,0,1]
	v_pk_fma_f32 v[128:129], v[108:109], s[6:7], v[176:177] op_sel_hi:[1,0,1]
	v_pk_fma_f32 v[122:123], v[106:107], s[6:7], v[144:145] op_sel_hi:[1,0,1]
	v_pk_fma_f32 v[118:119], v[118:119], s[6:7], v[150:151] op_sel_hi:[1,0,1]
	v_pk_fma_f32 v[116:117], v[116:117], s[6:7], v[148:149] op_sel_hi:[1,0,1]
	v_pk_fma_f32 v[106:107], v[114:115], s[6:7], v[154:155] op_sel_hi:[1,0,1]
	v_pk_fma_f32 v[104:105], v[112:113], s[6:7], v[152:153] op_sel_hi:[1,0,1]
	v_pk_fma_f32 v[102:103], v[102:103], s[6:7], v[158:159] op_sel_hi:[1,0,1]
	v_pk_fma_f32 v[100:101], v[100:101], s[6:7], v[156:157] op_sel_hi:[1,0,1]
	v_pk_fma_f32 v[98:99], v[98:99], s[6:7], v[166:167] op_sel_hi:[1,0,1]
	v_pk_fma_f32 v[96:97], v[96:97], s[6:7], v[164:165] op_sel_hi:[1,0,1]
	v_lshlrev_b64 v[148:149], 13, v[142:143]
	v_lshl_add_u64 v[164:165], v[170:171], 0, v[148:149]
	global_load_dwordx4 v[108:111], v[172:173], off
	global_load_dwordx4 v[112:115], v[172:173], off offset:64
	global_load_dwordx4 v[124:127], v[172:173], off offset:512
	global_load_dwordx4 v[142:145], v[172:173], off offset:576
	global_load_dwordx4 v[148:151], v[164:165], off
	global_load_dwordx4 v[152:155], v[164:165], off offset:64
	global_load_dwordx4 v[156:159], v[164:165], off offset:512
	s_nop 0
	global_load_dwordx4 v[164:167], v[164:165], off offset:576
	v_add_co_u32_e32 v170, vcc, s5, v140
	s_mov_b32 s7, 0x120000
	s_nop 0
	v_addc_co_u32_e32 v171, vcc, 0, v141, vcc
	v_lshl_add_u64 v[168:169], v[140:141], 0, s[10:11]
	s_mov_b32 s5, 0x140000
	s_mov_b64 s[10:11], 0x140000
	v_mul_f32_e32 v177, v138, v138
	v_mul_f32_e32 v179, v139, v139
	v_mov_b32_e32 v176, v134
	v_mov_b32_e32 v178, v135
	v_mul_f32_e32 v181, v128, v128
	v_mul_f32_e32 v183, v129, v129
	v_mul_f32_e32 v185, v130, v130
	v_mul_f32_e32 v187, v131, v131
	v_mov_b32_e32 v180, v128
	v_mov_b32_e32 v182, v129
	v_mov_b32_e32 v184, v130
	v_mov_b32_e32 v186, v131
	v_mul_f32_e32 v189, v120, v120
	v_mul_f32_e32 v191, v121, v121
	v_mul_f32_e32 v193, v122, v122
	v_mul_f32_e32 v195, v123, v123
	v_mov_b32_e32 v188, v120
	v_mov_b32_e32 v190, v121
	v_mov_b32_e32 v192, v122
	v_mov_b32_e32 v194, v123
	s_waitcnt vmcnt(7)
	v_pk_mul_f32 v[110:111], v[110:111], s[14:15] op_sel_hi:[1,0]
	v_pk_mul_f32 v[108:109], v[108:109], s[14:15] op_sel_hi:[1,0]
	s_waitcnt vmcnt(6)
	v_pk_mul_f32 v[114:115], v[114:115], s[14:15] op_sel_hi:[1,0]
	v_pk_mul_f32 v[112:113], v[112:113], s[14:15] op_sel_hi:[1,0]
	s_waitcnt vmcnt(5)
	v_pk_mul_f32 v[172:173], v[126:127], s[14:15] op_sel_hi:[1,0]
	v_pk_mul_f32 v[174:175], v[124:125], s[14:15] op_sel_hi:[1,0]
	s_waitcnt vmcnt(4)
	v_pk_mul_f32 v[144:145], v[144:145], s[14:15] op_sel_hi:[1,0]
	v_pk_mul_f32 v[142:143], v[142:143], s[14:15] op_sel_hi:[1,0]
	s_waitcnt vmcnt(3)
	v_pk_mul_f32 v[150:151], v[150:151], s[14:15] op_sel_hi:[1,0]
	v_pk_mul_f32 v[148:149], v[148:149], s[14:15] op_sel_hi:[1,0]
	s_waitcnt vmcnt(2)
	v_pk_mul_f32 v[154:155], v[154:155], s[14:15] op_sel_hi:[1,0]
	v_pk_mul_f32 v[152:153], v[152:153], s[14:15] op_sel_hi:[1,0]
	s_waitcnt vmcnt(1)
	v_pk_mul_f32 v[158:159], v[158:159], s[14:15] op_sel_hi:[1,0]
	v_pk_mul_f32 v[156:157], v[156:157], s[14:15] op_sel_hi:[1,0]
	s_waitcnt vmcnt(0)
	v_pk_mul_f32 v[166:167], v[166:167], s[14:15] op_sel_hi:[1,0]
	v_pk_mul_f32 v[164:165], v[164:165], s[14:15] op_sel_hi:[1,0]
	v_pk_fma_f32 v[126:127], v[94:95], s[6:7], v[110:111] op_sel_hi:[1,0,1]
	v_pk_fma_f32 v[124:125], v[92:93], s[6:7], v[108:109] op_sel_hi:[1,0,1]
	v_pk_fma_f32 v[114:115], v[90:91], s[6:7], v[114:115] op_sel_hi:[1,0,1]
	v_pk_fma_f32 v[112:113], v[88:89], s[6:7], v[112:113] op_sel_hi:[1,0,1]
	v_pk_fma_f32 v[110:111], v[78:79], s[6:7], v[172:173] op_sel_hi:[1,0,1]
	v_pk_fma_f32 v[108:109], v[76:77], s[6:7], v[174:175] op_sel_hi:[1,0,1]
	v_pk_fma_f32 v[90:91], v[74:75], s[6:7], v[144:145] op_sel_hi:[1,0,1]
	v_pk_fma_f32 v[88:89], v[72:73], s[6:7], v[142:143] op_sel_hi:[1,0,1]
	v_pk_fma_f32 v[86:87], v[86:87], s[6:7], v[150:151] op_sel_hi:[1,0,1]
	v_pk_fma_f32 v[84:85], v[84:85], s[6:7], v[148:149] op_sel_hi:[1,0,1]
	v_pk_fma_f32 v[74:75], v[82:83], s[6:7], v[154:155] op_sel_hi:[1,0,1]
	v_pk_fma_f32 v[72:73], v[80:81], s[6:7], v[152:153] op_sel_hi:[1,0,1]
	v_pk_fma_f32 v[70:71], v[70:71], s[6:7], v[158:159] op_sel_hi:[1,0,1]
	v_pk_fma_f32 v[68:69], v[68:69], s[6:7], v[156:157] op_sel_hi:[1,0,1]
	v_pk_fma_f32 v[66:67], v[66:67], s[6:7], v[166:167] op_sel_hi:[1,0,1]
	v_pk_fma_f32 v[64:65], v[64:65], s[6:7], v[164:165] op_sel_hi:[1,0,1]
	v_add_co_u32_e32 v148, vcc, s7, v140
	v_lshl_add_u64 v[164:165], v[140:141], 0, s[16:17]
	s_nop 0
	v_addc_co_u32_e32 v149, vcc, 0, v141, vcc
	global_load_dwordx4 v[76:79], v[170:171], off
	global_load_dwordx4 v[80:83], v[168:169], off offset:64
	global_load_dwordx4 v[92:95], v[168:169], off offset:512
	global_load_dwordx4 v[142:145], v[168:169], off offset:576
	v_add_co_u32_e32 v170, vcc, s5, v140
	global_load_dwordx4 v[148:151], v[148:149], off
	s_nop 0
	global_load_dwordx4 v[152:155], v[164:165], off offset:64
	global_load_dwordx4 v[156:159], v[164:165], off offset:512
	s_nop 0
	global_load_dwordx4 v[164:167], v[164:165], off offset:576
	s_mov_b32 s7, 0x160000
	v_addc_co_u32_e32 v171, vcc, 0, v141, vcc
	s_mov_b64 s[16:17], 0x160000
	v_lshl_add_u64 v[168:169], v[140:141], 0, s[10:11]
	s_waitcnt vmcnt(7)
	v_pk_mul_f32 v[78:79], v[78:79], s[14:15] op_sel_hi:[1,0]
	v_pk_mul_f32 v[76:77], v[76:77], s[14:15] op_sel_hi:[1,0]
	s_waitcnt vmcnt(6)
	v_pk_mul_f32 v[82:83], v[82:83], s[14:15] op_sel_hi:[1,0]
	v_pk_mul_f32 v[80:81], v[80:81], s[14:15] op_sel_hi:[1,0]
	s_waitcnt vmcnt(5)
	v_pk_mul_f32 v[172:173], v[94:95], s[14:15] op_sel_hi:[1,0]
	v_pk_mul_f32 v[174:175], v[92:93], s[14:15] op_sel_hi:[1,0]
	s_waitcnt vmcnt(4)
	v_pk_mul_f32 v[144:145], v[144:145], s[14:15] op_sel_hi:[1,0]
	v_pk_mul_f32 v[142:143], v[142:143], s[14:15] op_sel_hi:[1,0]
	s_waitcnt vmcnt(3)
	v_pk_mul_f32 v[150:151], v[150:151], s[14:15] op_sel_hi:[1,0]
	v_pk_mul_f32 v[148:149], v[148:149], s[14:15] op_sel_hi:[1,0]
	s_waitcnt vmcnt(2)
	v_pk_mul_f32 v[154:155], v[154:155], s[14:15] op_sel_hi:[1,0]
	v_pk_mul_f32 v[152:153], v[152:153], s[14:15] op_sel_hi:[1,0]
	s_waitcnt vmcnt(1)
	v_pk_mul_f32 v[158:159], v[158:159], s[14:15] op_sel_hi:[1,0]
	v_pk_mul_f32 v[156:157], v[156:157], s[14:15] op_sel_hi:[1,0]
	s_waitcnt vmcnt(0)
	v_pk_mul_f32 v[166:167], v[166:167], s[14:15] op_sel_hi:[1,0]
	v_pk_mul_f32 v[164:165], v[164:165], s[14:15] op_sel_hi:[1,0]
	v_pk_fma_f32 v[94:95], v[62:63], s[6:7], v[78:79] op_sel_hi:[1,0,1]
	v_pk_fma_f32 v[92:93], v[60:61], s[6:7], v[76:77] op_sel_hi:[1,0,1]
	v_pk_fma_f32 v[78:79], v[58:59], s[6:7], v[82:83] op_sel_hi:[1,0,1]
	v_pk_fma_f32 v[76:77], v[56:57], s[6:7], v[80:81] op_sel_hi:[1,0,1]
	v_pk_fma_f32 v[62:63], v[46:47], s[6:7], v[172:173] op_sel_hi:[1,0,1]
	v_pk_fma_f32 v[60:61], v[44:45], s[6:7], v[174:175] op_sel_hi:[1,0,1]
	v_pk_fma_f32 v[58:59], v[42:43], s[6:7], v[144:145] op_sel_hi:[1,0,1]
	v_pk_fma_f32 v[56:57], v[40:41], s[6:7], v[142:143] op_sel_hi:[1,0,1]
	v_pk_fma_f32 v[46:47], v[54:55], s[6:7], v[150:151] op_sel_hi:[1,0,1]
	v_pk_fma_f32 v[44:45], v[52:53], s[6:7], v[148:149] op_sel_hi:[1,0,1]
	v_pk_fma_f32 v[42:43], v[50:51], s[6:7], v[154:155] op_sel_hi:[1,0,1]
	v_pk_fma_f32 v[40:41], v[48:49], s[6:7], v[152:153] op_sel_hi:[1,0,1]
	v_pk_fma_f32 v[38:39], v[38:39], s[6:7], v[158:159] op_sel_hi:[1,0,1]
	v_pk_fma_f32 v[36:37], v[36:37], s[6:7], v[156:157] op_sel_hi:[1,0,1]
	v_pk_fma_f32 v[22:23], v[22:23], s[6:7], v[166:167] op_sel_hi:[1,0,1]
	v_pk_fma_f32 v[20:21], v[20:21], s[6:7], v[164:165] op_sel_hi:[1,0,1]
	v_add_co_u32_e32 v142, vcc, s7, v140
	global_load_dwordx4 v[48:51], v[170:171], off
	global_load_dwordx4 v[52:55], v[168:169], off offset:64
	global_load_dwordx4 v[80:83], v[168:169], off offset:512
	global_load_dwordx4 v[150:153], v[168:169], off offset:576
	v_addc_co_u32_e32 v143, vcc, 0, v141, vcc
	v_lshl_add_u64 v[140:141], v[140:141], 0, s[16:17]
	global_load_dwordx4 v[154:157], v[142:143], off
	global_load_dwordx4 v[164:167], v[140:141], off offset:64
	global_load_dwordx4 v[168:171], v[140:141], off offset:512
	global_load_dwordx4 v[172:175], v[140:141], off offset:576
	v_mbcnt_lo_u32_b32 v140, -1, 0
	v_mbcnt_hi_u32_b32 v163, -1, v140
	v_and_b32_e32 v141, 64, v163
	v_xor_b32_e32 v140, 16, v163
	v_add_u32_e32 v196, 64, v141
	v_cmp_lt_i32_e32 vcc, v140, v196
	v_add_f32_e32 v142, v136, v137
	v_add_f32_e32 v144, v138, v139
	v_cndmask_b32_e32 v140, v163, v140, vcc
	v_lshlrev_b32_e32 v147, 2, v140
	v_mul_f32_e32 v140, v134, v134
	v_mul_f32_e32 v149, v136, v136
	v_mul_f32_e32 v159, v137, v137
	v_mul_f32_e32 v143, v132, v132
	v_mul_f32_e32 v145, v133, v133
	v_mov_b32_e32 v148, v132
	v_mov_b32_e32 v158, v133
	v_pk_fma_f32 v[140:141], v[134:135], v[134:135], v[140:141] op_sel_hi:[1,1,0]
	v_pk_add_f32 v[148:149], v[148:149], v[158:159]
	v_pk_add_f32 v[158:159], v[176:177], v[178:179]
	v_pk_add_f32 v[142:143], v[142:143], v[144:145]
	v_mov_b32_e32 v140, 0
	v_pk_add_f32 v[144:145], v[180:181], v[182:183]
	v_pk_add_f32 v[176:177], v[184:185], v[186:187]
	v_pk_add_f32 v[148:149], v[148:149], v[158:159]
	v_pk_add_f32 v[142:143], v[142:143], v[140:141]
	v_pk_add_f32 v[178:179], v[188:189], v[190:191]
	v_pk_add_f32 v[180:181], v[192:193], v[194:195]
	v_pk_add_f32 v[144:145], v[144:145], v[176:177]
	v_pk_add_f32 v[142:143], v[148:149], v[142:143]
	v_pk_add_f32 v[158:159], v[178:179], v[180:181]
	v_pk_add_f32 v[142:143], v[144:145], v[142:143]
	v_xor_b32_e32 v141, 32, v163
	v_pk_add_f32 v[142:143], v[158:159], v[142:143]
	v_mov_b32_e32 v144, v142
	v_mov_b32_e32 v145, v143
	s_nop 1
	v_permlane16_swap_b32_e32 v142, v144
	v_permlane16_swap_b32_e32 v143, v145
	v_cmp_lt_i32_e32 vcc, v141, v196
	s_waitcnt lgkmcnt(0)
	v_pk_add_f32 v[142:143], v[142:143], v[144:145]
	v_cndmask_b32_e32 v141, v163, v141, vcc
	v_lshlrev_b32_e32 v148, 2, v141
	v_mov_b32_e32 v144, v142
	v_mov_b32_e32 v145, v143
	s_nop 1
	v_permlane32_swap_b32_e32 v142, v144
	v_permlane32_swap_b32_e32 v143, v145
	v_cmp_gt_u32_e32 vcc, 16, v146
	s_waitcnt vmcnt(7)
	v_pk_mul_f32 v[50:51], v[50:51], s[14:15] op_sel_hi:[1,0]
	v_pk_mul_f32 v[48:49], v[48:49], s[14:15] op_sel_hi:[1,0]
	s_waitcnt vmcnt(6)
	v_pk_mul_f32 v[54:55], v[54:55], s[14:15] op_sel_hi:[1,0]
	v_pk_mul_f32 v[52:53], v[52:53], s[14:15] op_sel_hi:[1,0]
	s_waitcnt vmcnt(5)
	v_pk_mul_f32 v[158:159], v[82:83], s[14:15] op_sel_hi:[1,0]
	v_pk_mul_f32 v[176:177], v[80:81], s[14:15] op_sel_hi:[1,0]
	s_waitcnt vmcnt(4)
	v_pk_mul_f32 v[152:153], v[152:153], s[14:15] op_sel_hi:[1,0]
	v_pk_mul_f32 v[150:151], v[150:151], s[14:15] op_sel_hi:[1,0]
	s_waitcnt vmcnt(3)
	v_pk_mul_f32 v[156:157], v[156:157], s[14:15] op_sel_hi:[1,0]
	v_pk_mul_f32 v[154:155], v[154:155], s[14:15] op_sel_hi:[1,0]
	s_waitcnt vmcnt(2)
	v_pk_mul_f32 v[166:167], v[166:167], s[14:15] op_sel_hi:[1,0]
	v_pk_mul_f32 v[164:165], v[164:165], s[14:15] op_sel_hi:[1,0]
	s_waitcnt vmcnt(1)
	v_pk_mul_f32 v[170:171], v[170:171], s[14:15] op_sel_hi:[1,0]
	v_pk_mul_f32 v[168:169], v[168:169], s[14:15] op_sel_hi:[1,0]
	s_waitcnt vmcnt(0)
	v_pk_mul_f32 v[174:175], v[174:175], s[14:15] op_sel_hi:[1,0]
	v_pk_mul_f32 v[172:173], v[172:173], s[14:15] op_sel_hi:[1,0]
	v_pk_fma_f32 v[82:83], v[14:15], s[6:7], v[50:51] op_sel_hi:[1,0,1]
	v_pk_fma_f32 v[80:81], v[12:13], s[6:7], v[48:49] op_sel_hi:[1,0,1]
	v_pk_fma_f32 v[54:55], v[10:11], s[6:7], v[54:55] op_sel_hi:[1,0,1]
	v_pk_fma_f32 v[52:53], v[8:9], s[6:7], v[52:53] op_sel_hi:[1,0,1]
	v_pk_fma_f32 v[50:51], v[18:19], s[6:7], v[158:159] op_sel_hi:[1,0,1]
	v_pk_fma_f32 v[48:49], v[16:17], s[6:7], v[176:177] op_sel_hi:[1,0,1]
	v_pk_fma_f32 v[18:19], v[26:27], s[6:7], v[152:153] op_sel_hi:[1,0,1]
	v_pk_fma_f32 v[16:17], v[24:25], s[6:7], v[150:151] op_sel_hi:[1,0,1]
	v_pk_fma_f32 v[14:15], v[6:7], s[6:7], v[156:157] op_sel_hi:[1,0,1]
	v_pk_fma_f32 v[12:13], v[4:5], s[6:7], v[154:155] op_sel_hi:[1,0,1]
	v_pk_fma_f32 v[10:11], v[2:3], s[6:7], v[166:167] op_sel_hi:[1,0,1]
	v_pk_fma_f32 v[8:9], v[0:1], s[6:7], v[164:165] op_sel_hi:[1,0,1]
	v_pk_fma_f32 v[6:7], v[30:31], s[6:7], v[170:171] op_sel_hi:[1,0,1]
	v_pk_fma_f32 v[4:5], v[28:29], s[6:7], v[168:169] op_sel_hi:[1,0,1]
	v_pk_fma_f32 v[2:3], v[34:35], s[6:7], v[174:175] op_sel_hi:[1,0,1]
	v_pk_fma_f32 v[0:1], v[32:33], s[6:7], v[172:173] op_sel_hi:[1,0,1]
	s_nop 0
	s_and_saveexec_b64 s[6:7], vcc
	s_cbranch_execz .LBB0_703
	s_lshl_b32 s5, s1, 11
	s_add_i32 s5, s2, s5
	v_lshl_add_u32 v26, v146, 5, s5
	s_waitcnt lgkmcnt(0)
	v_pk_add_f32 v[24:25], v[142:143], v[144:145]
	ds_write_b64 v26, v[24:25]
.LBB0_703:
	s_or_b64 exec, exec, s[6:7]
	v_mul_f32_e32 v29, v116, v116
	v_mul_f32_e32 v28, v106, v106
	v_add_f32_e32 v24, v116, v117
	v_add_f32_e32 v26, v118, v119
	v_mul_f32_e32 v31, v117, v117
	v_mul_f32_e32 v33, v118, v118
	v_mul_f32_e32 v35, v119, v119
	v_mul_f32_e32 v25, v104, v104
	v_mul_f32_e32 v27, v105, v105
	v_pk_fma_f32 v[142:143], v[106:107], v[106:107], v[28:29] op_sel_hi:[1,1,0]
	v_mov_b32_e32 v28, v104
	v_mov_b32_e32 v30, v105
	v_mov_b32_e32 v32, v106
	v_mov_b32_e32 v34, v107
	v_pk_add_f32 v[28:29], v[28:29], v[30:31]
	v_pk_add_f32 v[30:31], v[32:33], v[34:35]
	v_pk_add_f32 v[24:25], v[24:25], v[26:27]
	v_mov_b32_e32 v141, v143
	s_waitcnt lgkmcnt(0)
	v_mul_f32_e32 v145, v100, v100
	v_mul_f32_e32 v151, v101, v101
	v_mul_f32_e32 v153, v102, v102
	v_mul_f32_e32 v155, v103, v103
	v_pk_add_f32 v[28:29], v[28:29], v[30:31]
	v_pk_add_f32 v[24:25], v[24:25], v[140:141]
	v_mov_b32_e32 v144, v100
	v_mov_b32_e32 v150, v101
	v_mov_b32_e32 v152, v102
	v_mov_b32_e32 v154, v103
	v_pk_add_f32 v[24:25], v[28:29], v[24:25]
	v_pk_add_f32 v[26:27], v[144:145], v[150:151]
	v_pk_add_f32 v[28:29], v[152:153], v[154:155]
	v_mul_f32_e32 v157, v96, v96
	v_mul_f32_e32 v159, v97, v97
	v_mul_f32_e32 v165, v98, v98
	v_mul_f32_e32 v167, v99, v99
	v_pk_add_f32 v[26:27], v[26:27], v[28:29]
	v_mov_b32_e32 v156, v96
	v_mov_b32_e32 v158, v97
	v_mov_b32_e32 v164, v98
	v_mov_b32_e32 v166, v99
	v_pk_add_f32 v[24:25], v[26:27], v[24:25]
	v_pk_add_f32 v[26:27], v[156:157], v[158:159]
	v_pk_add_f32 v[28:29], v[164:165], v[166:167]
	s_nop 0
	v_pk_add_f32 v[26:27], v[26:27], v[28:29]
	s_nop 0
	v_pk_add_f32 v[24:25], v[26:27], v[24:25]
	v_mov_b32_e32 v26, v24
	v_mov_b32_e32 v27, v25
	s_nop 1
	v_permlane16_swap_b32_e32 v24, v26
	v_permlane16_swap_b32_e32 v25, v27
	s_waitcnt lgkmcnt(0)
	v_pk_add_f32 v[24:25], v[24:25], v[26:27]
	v_mov_b32_e32 v26, v24
	v_mov_b32_e32 v27, v25
	s_nop 1
	v_permlane32_swap_b32_e32 v24, v26
	v_permlane32_swap_b32_e32 v25, v27
	s_and_saveexec_b64 s[6:7], vcc
	v_readlane_b32 s86, v255, 26
	v_readlane_b32 s36, v255, 30
	v_readlane_b32 s87, v255, 27
	v_readlane_b32 s37, v255, 31
	s_cbranch_execz .LBB0_705
	s_lshl_b32 s5, s1, 11
	s_add_i32 s5, s2, s5
	v_lshl_add_u32 v28, v146, 5, s5
	s_waitcnt lgkmcnt(0)
	v_pk_add_f32 v[24:25], v[24:25], v[26:27]
	ds_write_b64 v28, v[24:25] offset:512
.LBB0_705:
	s_or_b64 exec, exec, s[6:7]
	v_mul_f32_e32 v24, v114, v114
	s_waitcnt lgkmcnt(1)
	v_add_f32_e32 v26, v124, v125
	v_add_f32_e32 v28, v126, v127
	v_mul_f32_e32 v31, v124, v124
	v_mul_f32_e32 v33, v125, v125
	v_mul_f32_e32 v35, v126, v126
	v_mul_f32_e32 v141, v127, v127
	s_waitcnt lgkmcnt(0)
	v_mul_f32_e32 v27, v112, v112
	v_mul_f32_e32 v29, v113, v113
	v_pk_fma_f32 v[24:25], v[114:115], v[114:115], v[24:25] op_sel_hi:[1,1,0]
	v_mov_b32_e32 v30, v112
	v_mov_b32_e32 v32, v113
	v_mov_b32_e32 v34, v114
	v_mov_b32_e32 v140, v115
	v_pk_add_f32 v[30:31], v[30:31], v[32:33]
	v_pk_add_f32 v[32:33], v[34:35], v[140:141]
	v_pk_add_f32 v[26:27], v[26:27], v[28:29]
	v_mov_b32_e32 v24, 0
	v_mul_f32_e32 v143, v108, v108
	v_mul_f32_e32 v145, v109, v109
	v_mul_f32_e32 v151, v110, v110
	v_mul_f32_e32 v153, v111, v111
	v_pk_add_f32 v[30:31], v[30:31], v[32:33]
	v_pk_add_f32 v[26:27], v[26:27], v[24:25]
	v_mov_b32_e32 v142, v108
	v_mov_b32_e32 v144, v109
	v_mov_b32_e32 v150, v110
	v_mov_b32_e32 v152, v111
	v_pk_add_f32 v[26:27], v[30:31], v[26:27]
	v_pk_add_f32 v[28:29], v[142:143], v[144:145]
	v_pk_add_f32 v[30:31], v[150:151], v[152:153]
	v_mul_f32_e32 v155, v88, v88
	v_mul_f32_e32 v157, v89, v89
	v_mul_f32_e32 v159, v90, v90
	v_mul_f32_e32 v165, v91, v91
	v_pk_add_f32 v[28:29], v[28:29], v[30:31]
	v_mov_b32_e32 v154, v88
	v_mov_b32_e32 v156, v89
	v_mov_b32_e32 v158, v90
	v_mov_b32_e32 v164, v91
	v_pk_add_f32 v[26:27], v[28:29], v[26:27]
	v_pk_add_f32 v[28:29], v[154:155], v[156:157]
	v_pk_add_f32 v[30:31], v[158:159], v[164:165]
	s_nop 0
	v_pk_add_f32 v[28:29], v[28:29], v[30:31]
	s_nop 0
	v_pk_add_f32 v[26:27], v[28:29], v[26:27]
	v_mov_b32_e32 v28, v26
	v_mov_b32_e32 v29, v27
	s_nop 1
	v_permlane16_swap_b32_e32 v26, v28
	v_permlane16_swap_b32_e32 v27, v29
	s_waitcnt lgkmcnt(0)
	v_pk_add_f32 v[26:27], v[26:27], v[28:29]
	v_mov_b32_e32 v28, v26
	v_mov_b32_e32 v29, v27
	s_nop 1
	v_permlane32_swap_b32_e32 v26, v28
	v_permlane32_swap_b32_e32 v27, v29
	s_and_saveexec_b64 s[6:7], vcc
	s_cbranch_execz .LBB0_707
	s_lshl_b32 s5, s1, 11
	s_add_i32 s5, s2, s5
	v_lshl_add_u32 v25, v146, 5, s5
	s_waitcnt lgkmcnt(0)
	v_pk_add_f32 v[26:27], v[26:27], v[28:29]
	ds_write_b64 v25, v[26:27] offset:1024
.LBB0_707:
	s_or_b64 exec, exec, s[6:7]
	v_mul_f32_e32 v31, v84, v84
	v_mul_f32_e32 v30, v74, v74
	v_add_f32_e32 v26, v84, v85
	s_waitcnt lgkmcnt(1)
	v_add_f32_e32 v28, v86, v87
	v_mul_f32_e32 v33, v85, v85
	v_mul_f32_e32 v35, v86, v86
	v_mul_f32_e32 v141, v87, v87
	v_mul_f32_e32 v27, v72, v72
	s_waitcnt lgkmcnt(0)
	v_mul_f32_e32 v29, v73, v73
	v_pk_fma_f32 v[142:143], v[74:75], v[74:75], v[30:31] op_sel_hi:[1,1,0]
	v_mov_b32_e32 v30, v72
	v_mov_b32_e32 v32, v73
	v_mov_b32_e32 v34, v74
	v_mov_b32_e32 v140, v75
	v_mul_f32_e32 v145, v68, v68
	v_mul_f32_e32 v151, v69, v69
	v_mul_f32_e32 v153, v70, v70
	v_mul_f32_e32 v155, v71, v71
	v_pk_add_f32 v[30:31], v[30:31], v[32:33]
	v_pk_add_f32 v[32:33], v[34:35], v[140:141]
	v_pk_add_f32 v[26:27], v[26:27], v[28:29]
	v_mov_b32_e32 v25, v143
	v_mov_b32_e32 v144, v68
	v_mov_b32_e32 v150, v69
	v_mov_b32_e32 v152, v70
	v_mov_b32_e32 v154, v71
	v_pk_add_f32 v[30:31], v[30:31], v[32:33]
	v_pk_add_f32 v[24:25], v[26:27], v[24:25]
	v_pk_add_f32 v[26:27], v[144:145], v[150:151]
	v_pk_add_f32 v[28:29], v[152:153], v[154:155]
	v_mul_f32_e32 v157, v64, v64
	v_mul_f32_e32 v159, v65, v65
	v_mul_f32_e32 v165, v66, v66
	v_mul_f32_e32 v167, v67, v67
	v_pk_add_f32 v[24:25], v[30:31], v[24:25]
	v_pk_add_f32 v[26:27], v[26:27], v[28:29]
	v_mov_b32_e32 v156, v64
	v_mov_b32_e32 v158, v65
	v_mov_b32_e32 v164, v66
	v_mov_b32_e32 v166, v67
	v_pk_add_f32 v[24:25], v[26:27], v[24:25]
	v_pk_add_f32 v[26:27], v[156:157], v[158:159]
	v_pk_add_f32 v[28:29], v[164:165], v[166:167]
	s_nop 0
	v_pk_add_f32 v[26:27], v[26:27], v[28:29]
	s_nop 0
	v_pk_add_f32 v[24:25], v[26:27], v[24:25]
	v_mov_b32_e32 v26, v24
	v_mov_b32_e32 v27, v25
	s_nop 1
	v_permlane16_swap_b32_e32 v24, v26
	v_permlane16_swap_b32_e32 v25, v27
	s_waitcnt lgkmcnt(0)
	v_pk_add_f32 v[24:25], v[24:25], v[26:27]
	v_mov_b32_e32 v26, v24
	v_mov_b32_e32 v27, v25
	s_nop 1
	v_permlane32_swap_b32_e32 v24, v26
	v_permlane32_swap_b32_e32 v25, v27
	s_and_saveexec_b64 s[6:7], vcc
	s_cbranch_execz .LBB0_709
	s_lshl_b32 s5, s1, 11
	s_add_i32 s5, s2, s5
	v_lshl_add_u32 v28, v146, 5, s5
	s_waitcnt lgkmcnt(0)
	v_pk_add_f32 v[24:25], v[24:25], v[26:27]
	ds_write_b64 v28, v[24:25] offset:1536
.LBB0_709:
	s_or_b64 exec, exec, s[6:7]
	v_mul_f32_e32 v24, v78, v78
	s_waitcnt lgkmcnt(1)
	v_add_f32_e32 v26, v92, v93
	v_add_f32_e32 v28, v94, v95
	v_mul_f32_e32 v31, v92, v92
	v_mul_f32_e32 v33, v93, v93
	v_mul_f32_e32 v35, v94, v94
	v_mul_f32_e32 v141, v95, v95
	s_waitcnt lgkmcnt(0)
	v_mul_f32_e32 v27, v76, v76
	v_mul_f32_e32 v29, v77, v77
	v_pk_fma_f32 v[24:25], v[78:79], v[78:79], v[24:25] op_sel_hi:[1,1,0]
	v_mov_b32_e32 v30, v76
	v_mov_b32_e32 v32, v77
	v_mov_b32_e32 v34, v78
	v_mov_b32_e32 v140, v79
	v_pk_add_f32 v[30:31], v[30:31], v[32:33]
	v_pk_add_f32 v[32:33], v[34:35], v[140:141]
	v_pk_add_f32 v[26:27], v[26:27], v[28:29]
	v_mov_b32_e32 v24, 0
	v_mul_f32_e32 v143, v60, v60
	v_mul_f32_e32 v145, v61, v61
	v_mul_f32_e32 v151, v62, v62
	v_mul_f32_e32 v153, v63, v63
	v_pk_add_f32 v[30:31], v[30:31], v[32:33]
	v_pk_add_f32 v[26:27], v[26:27], v[24:25]
	v_mov_b32_e32 v142, v60
	v_mov_b32_e32 v144, v61
	v_mov_b32_e32 v150, v62
	v_mov_b32_e32 v152, v63
	v_pk_add_f32 v[26:27], v[30:31], v[26:27]
	v_pk_add_f32 v[28:29], v[142:143], v[144:145]
	v_pk_add_f32 v[30:31], v[150:151], v[152:153]
	v_mul_f32_e32 v155, v56, v56
	v_mul_f32_e32 v157, v57, v57
	v_mul_f32_e32 v159, v58, v58
	v_mul_f32_e32 v165, v59, v59
	v_pk_add_f32 v[28:29], v[28:29], v[30:31]
	v_mov_b32_e32 v154, v56
	v_mov_b32_e32 v156, v57
	v_mov_b32_e32 v158, v58
	v_mov_b32_e32 v164, v59
	v_pk_add_f32 v[26:27], v[28:29], v[26:27]
	v_pk_add_f32 v[28:29], v[154:155], v[156:157]
	v_pk_add_f32 v[30:31], v[158:159], v[164:165]
	s_nop 0
	v_pk_add_f32 v[28:29], v[28:29], v[30:31]
	s_nop 0
	v_pk_add_f32 v[26:27], v[28:29], v[26:27]
	v_mov_b32_e32 v28, v26
	v_mov_b32_e32 v29, v27
	s_nop 1
	v_permlane16_swap_b32_e32 v26, v28
	v_permlane16_swap_b32_e32 v27, v29
	s_waitcnt lgkmcnt(0)
	v_pk_add_f32 v[26:27], v[26:27], v[28:29]
	v_mov_b32_e32 v28, v26
	v_mov_b32_e32 v29, v27
	s_nop 1
	v_permlane32_swap_b32_e32 v26, v28
	v_permlane32_swap_b32_e32 v27, v29
	s_and_saveexec_b64 s[6:7], vcc
	s_cbranch_execz .LBB0_711
	s_lshl_b32 s5, s1, 11
	s_add_i32 s5, s2, s5
	v_lshl_add_u32 v25, v146, 5, s5
	s_waitcnt lgkmcnt(0)
	v_pk_add_f32 v[26:27], v[26:27], v[28:29]
	ds_write_b64 v25, v[26:27] offset:4096
.LBB0_711:
	s_or_b64 exec, exec, s[6:7]
	v_mul_f32_e32 v31, v44, v44
	v_mul_f32_e32 v30, v42, v42
	v_add_f32_e32 v26, v44, v45
	s_waitcnt lgkmcnt(1)
	v_add_f32_e32 v28, v46, v47
	v_mul_f32_e32 v33, v45, v45
	v_mul_f32_e32 v35, v46, v46
	v_mul_f32_e32 v141, v47, v47
	v_mul_f32_e32 v27, v40, v40
	s_waitcnt lgkmcnt(0)
	v_mul_f32_e32 v29, v41, v41
	v_pk_fma_f32 v[142:143], v[42:43], v[42:43], v[30:31] op_sel_hi:[1,1,0]
	v_mov_b32_e32 v30, v40
	v_mov_b32_e32 v32, v41
	v_mov_b32_e32 v34, v42
	v_mov_b32_e32 v140, v43
	v_mul_f32_e32 v145, v36, v36
	v_mul_f32_e32 v151, v37, v37
	v_mul_f32_e32 v153, v38, v38
	v_mul_f32_e32 v155, v39, v39
	v_pk_add_f32 v[30:31], v[30:31], v[32:33]
	v_pk_add_f32 v[32:33], v[34:35], v[140:141]
	v_pk_add_f32 v[26:27], v[26:27], v[28:29]
	v_mov_b32_e32 v25, v143
	v_mov_b32_e32 v144, v36
	v_mov_b32_e32 v150, v37
	v_mov_b32_e32 v152, v38
	v_mov_b32_e32 v154, v39
	v_pk_add_f32 v[30:31], v[30:31], v[32:33]
	v_pk_add_f32 v[24:25], v[26:27], v[24:25]
	v_pk_add_f32 v[26:27], v[144:145], v[150:151]
	v_pk_add_f32 v[28:29], v[152:153], v[154:155]
	v_mul_f32_e32 v157, v20, v20
	v_mul_f32_e32 v159, v21, v21
	v_mul_f32_e32 v165, v22, v22
	v_mul_f32_e32 v167, v23, v23
	v_pk_add_f32 v[24:25], v[30:31], v[24:25]
	v_pk_add_f32 v[26:27], v[26:27], v[28:29]
	v_mov_b32_e32 v156, v20
	v_mov_b32_e32 v158, v21
	v_mov_b32_e32 v164, v22
	v_mov_b32_e32 v166, v23
	v_pk_add_f32 v[24:25], v[26:27], v[24:25]
	v_pk_add_f32 v[26:27], v[156:157], v[158:159]
	v_pk_add_f32 v[28:29], v[164:165], v[166:167]
	s_nop 0
	v_pk_add_f32 v[26:27], v[26:27], v[28:29]
	s_nop 0
	v_pk_add_f32 v[24:25], v[26:27], v[24:25]
	v_mov_b32_e32 v26, v24
	v_mov_b32_e32 v27, v25
	s_nop 1
	v_permlane16_swap_b32_e32 v24, v26
	v_permlane16_swap_b32_e32 v25, v27
	s_waitcnt lgkmcnt(0)
	v_pk_add_f32 v[24:25], v[24:25], v[26:27]
	v_mov_b32_e32 v26, v24
	v_mov_b32_e32 v27, v25
	s_nop 1
	v_permlane32_swap_b32_e32 v24, v26
	v_permlane32_swap_b32_e32 v25, v27
	s_and_saveexec_b64 s[6:7], vcc
	s_cbranch_execz .LBB0_713
	s_lshl_b32 s5, s1, 11
	s_add_i32 s5, s2, s5
	v_lshl_add_u32 v28, v146, 5, s5
	s_waitcnt lgkmcnt(0)
	v_pk_add_f32 v[24:25], v[24:25], v[26:27]
	ds_write_b64 v28, v[24:25] offset:4608
.LBB0_713:
	s_or_b64 exec, exec, s[6:7]
	v_mul_f32_e32 v24, v54, v54
	s_waitcnt lgkmcnt(1)
	v_add_f32_e32 v26, v80, v81
	v_add_f32_e32 v28, v82, v83
	v_mul_f32_e32 v31, v80, v80
	v_mul_f32_e32 v33, v81, v81
	v_mul_f32_e32 v35, v82, v82
	v_mul_f32_e32 v141, v83, v83
	s_waitcnt lgkmcnt(0)
	v_mul_f32_e32 v27, v52, v52
	v_mul_f32_e32 v29, v53, v53
	v_pk_fma_f32 v[24:25], v[54:55], v[54:55], v[24:25] op_sel_hi:[1,1,0]
	v_mov_b32_e32 v30, v52
	v_mov_b32_e32 v32, v53
	v_mov_b32_e32 v34, v54
	v_mov_b32_e32 v140, v55
	v_pk_add_f32 v[30:31], v[30:31], v[32:33]
	v_pk_add_f32 v[32:33], v[34:35], v[140:141]
	v_pk_add_f32 v[26:27], v[26:27], v[28:29]
	v_mov_b32_e32 v24, 0
	v_mul_f32_e32 v143, v48, v48
	v_mul_f32_e32 v145, v49, v49
	v_mul_f32_e32 v151, v50, v50
	v_mul_f32_e32 v153, v51, v51
	v_pk_add_f32 v[30:31], v[30:31], v[32:33]
	v_pk_add_f32 v[26:27], v[26:27], v[24:25]
	v_mov_b32_e32 v142, v48
	v_mov_b32_e32 v144, v49
	v_mov_b32_e32 v150, v50
	v_mov_b32_e32 v152, v51
	v_pk_add_f32 v[26:27], v[30:31], v[26:27]
	v_pk_add_f32 v[28:29], v[142:143], v[144:145]
	v_pk_add_f32 v[30:31], v[150:151], v[152:153]
	v_mul_f32_e32 v155, v16, v16
	v_mul_f32_e32 v157, v17, v17
	v_mul_f32_e32 v159, v18, v18
	v_mul_f32_e32 v165, v19, v19
	v_pk_add_f32 v[28:29], v[28:29], v[30:31]
	v_mov_b32_e32 v154, v16
	v_mov_b32_e32 v156, v17
	v_mov_b32_e32 v158, v18
	v_mov_b32_e32 v164, v19
	v_pk_add_f32 v[26:27], v[28:29], v[26:27]
	v_pk_add_f32 v[28:29], v[154:155], v[156:157]
	v_pk_add_f32 v[30:31], v[158:159], v[164:165]
	s_nop 0
	v_pk_add_f32 v[28:29], v[28:29], v[30:31]
	s_nop 0
	v_pk_add_f32 v[26:27], v[28:29], v[26:27]
	v_mov_b32_e32 v28, v26
	v_mov_b32_e32 v29, v27
	s_nop 1
	v_permlane16_swap_b32_e32 v26, v28
	v_permlane16_swap_b32_e32 v27, v29
	s_waitcnt lgkmcnt(0)
	v_pk_add_f32 v[26:27], v[26:27], v[28:29]
	v_mov_b32_e32 v28, v26
	v_mov_b32_e32 v29, v27
	s_nop 1
	v_permlane32_swap_b32_e32 v26, v28
	v_permlane32_swap_b32_e32 v27, v29
	s_and_saveexec_b64 s[6:7], vcc
	s_cbranch_execz .LBB0_715
	s_lshl_b32 s5, s1, 11
	s_add_i32 s5, s2, s5
	v_lshl_add_u32 v25, v146, 5, s5
	s_waitcnt lgkmcnt(0)
	v_pk_add_f32 v[26:27], v[26:27], v[28:29]
	ds_write_b64 v25, v[26:27] offset:5120
.LBB0_715:
	s_or_b64 exec, exec, s[6:7]
	v_mul_f32_e32 v31, v12, v12
	v_mul_f32_e32 v30, v10, v10
	v_add_f32_e32 v26, v12, v13
	s_waitcnt lgkmcnt(1)
	v_add_f32_e32 v28, v14, v15
	v_mul_f32_e32 v33, v13, v13
	v_mul_f32_e32 v35, v14, v14
	v_mul_f32_e32 v141, v15, v15
	v_mul_f32_e32 v27, v8, v8
	s_waitcnt lgkmcnt(0)
	v_mul_f32_e32 v29, v9, v9
	v_pk_fma_f32 v[142:143], v[10:11], v[10:11], v[30:31] op_sel_hi:[1,1,0]
	v_mov_b32_e32 v30, v8
	v_mov_b32_e32 v32, v9
	v_mov_b32_e32 v34, v10
	v_mov_b32_e32 v140, v11
	v_mul_f32_e32 v145, v4, v4
	v_mul_f32_e32 v151, v5, v5
	v_mul_f32_e32 v153, v6, v6
	v_mul_f32_e32 v155, v7, v7
	v_pk_add_f32 v[30:31], v[30:31], v[32:33]
	v_pk_add_f32 v[32:33], v[34:35], v[140:141]
	v_pk_add_f32 v[26:27], v[26:27], v[28:29]
	v_mov_b32_e32 v25, v143
	v_mov_b32_e32 v144, v4
	v_mov_b32_e32 v150, v5
	v_mov_b32_e32 v152, v6
	v_mov_b32_e32 v154, v7
	v_pk_add_f32 v[30:31], v[30:31], v[32:33]
	v_pk_add_f32 v[24:25], v[26:27], v[24:25]
	v_pk_add_f32 v[26:27], v[144:145], v[150:151]
	v_pk_add_f32 v[28:29], v[152:153], v[154:155]
	v_mul_f32_e32 v157, v0, v0
	v_mul_f32_e32 v159, v1, v1
	v_mul_f32_e32 v165, v2, v2
	v_mul_f32_e32 v167, v3, v3
	v_pk_add_f32 v[24:25], v[30:31], v[24:25]
	v_pk_add_f32 v[26:27], v[26:27], v[28:29]
	v_mov_b32_e32 v156, v0
	v_mov_b32_e32 v158, v1
	v_mov_b32_e32 v164, v2
	v_mov_b32_e32 v166, v3
	v_pk_add_f32 v[24:25], v[26:27], v[24:25]
	v_pk_add_f32 v[26:27], v[156:157], v[158:159]
	v_pk_add_f32 v[28:29], v[164:165], v[166:167]
	s_nop 0
	v_pk_add_f32 v[26:27], v[26:27], v[28:29]
	s_nop 0
	v_pk_add_f32 v[24:25], v[26:27], v[24:25]
	v_mov_b32_e32 v26, v24
	v_mov_b32_e32 v27, v25
	s_nop 1
	v_permlane16_swap_b32_e32 v24, v26
	v_permlane16_swap_b32_e32 v25, v27
	s_waitcnt lgkmcnt(0)
	v_pk_add_f32 v[24:25], v[24:25], v[26:27]
	v_mov_b32_e32 v26, v24
	v_mov_b32_e32 v27, v25
	s_nop 1
	v_permlane32_swap_b32_e32 v24, v26
	v_permlane32_swap_b32_e32 v25, v27
	s_and_saveexec_b64 s[6:7], vcc
	s_cbranch_execz .LBB0_717
	s_lshl_b32 s1, s1, 11
	s_add_i32 s2, s2, s1
	v_lshl_add_u32 v28, v146, 5, s2
	s_waitcnt lgkmcnt(0)
	v_pk_add_f32 v[24:25], v[24:25], v[26:27]
	ds_write_b64 v28, v[24:25] offset:5632

.LBB0_1263:
	v_lshl_add_u64 v[98:99], s[90:91], 0, v[94:95]
	s_waitcnt vmcnt(28)
	v_add_co_u32_e32 v64, vcc, s7, v98
	s_ashr_i32 s11, s10, 31
	s_nop 0
	v_addc_co_u32_e32 v65, vcc, 0, v99, vcc
	s_add_i32 s20, s19, s6
	v_lshl_add_u64 v[66:67], s[90:91], 0, v[96:97]
	s_lshl_b64 s[22:23], s[10:11], 2
	global_load_dwordx4 v[74:77], v[64:65], off
	global_load_dwordx4 v[102:105], v[64:65], off offset:1024
	global_load_dwordx4 v[106:109], v[64:65], off offset:2048
	global_load_dwordx4 v[68:71], v[64:65], off offset:3072
	v_add_co_u32_e32 v64, vcc, s27, v66
	s_add_u32 s22, s2, s22
	s_nop 0
	v_addc_co_u32_e32 v65, vcc, 0, v67, vcc
	s_addc_u32 s23, s3, s23
	global_load_dwordx2 v[72:73], v[64:65], off offset:1536
	global_load_dwordx2 v[142:143], v[64:65], off offset:3584
	global_load_dwordx4 v[110:113], v138, s[22:23]
	v_add_co_u32_e32 v66, vcc, s9, v66
	s_cmpk_lt_i32 s20, 0x2000
	s_nop 0
	v_addc_co_u32_e32 v67, vcc, 0, v67, vcc
	global_load_dwordx2 v[80:81], v[66:67], off offset:3584
	global_load_dwordx2 v[100:101], v[66:67], off offset:1536
	global_load_dwordx2 v[124:125], v[66:67], off offset:2560
	global_load_dwordx2 v[132:133], v[66:67], off offset:3072
	global_load_dwordx2 v[126:127], v[66:67], off offset:512
	global_load_dwordx2 v[134:135], v[66:67], off offset:1024
	global_load_dwordx2 v[114:115], v[66:67], off offset:2048
	global_load_dwordx2 v[120:121], v[64:65], off offset:-4096
	global_load_dwordx2 v[116:117], v[64:65], off
	global_load_dwordx2 v[128:129], v[64:65], off offset:512
	global_load_dwordx2 v[136:137], v[64:65], off offset:1024
	global_load_dwordx2 v[122:123], v[64:65], off offset:2048
	global_load_dwordx2 v[130:131], v[64:65], off offset:2560
	global_load_dwordx2 v[156:157], v[64:65], off offset:3072
	s_cselect_b32 s24, s20, s6
	s_lshl_b32 s34, s24, 2
	s_ashr_i32 s25, s24, 31
	s_ashr_i32 s35, s34, 31
	s_lshl_b64 s[22:23], s[24:25], 12
	s_lshl_b64 s[34:35], s[34:35], 2
	s_add_u32 s34, s2, s34
	s_addc_u32 s35, s3, s35
	s_lshl_b64 s[24:25], s[24:25], 13
	s_add_u32 s24, s0, s24
	s_addc_u32 s25, s1, s25
	global_load_dwordx4 v[64:67], v138, s[34:35]
	s_cmpk_gt_i32 s20, 0x1fff
	s_waitcnt vmcnt(21)
	v_lshlrev_b32_e32 v162, 16, v76
	v_and_b32_e32 v163, 0xffff0000, v76
	s_waitcnt vmcnt(19)
	v_lshlrev_b32_e32 v150, 16, v109
	v_and_b32_e32 v148, 0xffff0000, v109
	v_lshlrev_b32_e32 v166, 16, v104
	s_waitcnt vmcnt(13)
	v_cvt_f32_fp8_sdwa v109, v100 src0_sel:BYTE_2
	v_and_b32_e32 v160, 0xffff0000, v104
	v_lshlrev_b32_e32 v104, 16, v69
	v_mul_f32_e32 v145, 0x3f9837f0, v104
	v_lshlrev_b32_e32 v83, 16, v74
	v_and_b32_e32 v141, 0xffff0000, v74
	v_mul_f32_e32 v82, 0x3d800000, v110
	v_cvt_f32_fp8_sdwa v110, v80 src0_sel:BYTE_2
	v_mul_f32_e32 v76, 0x3d800000, v111
	v_cvt_f32_fp8_sdwa v111, v72 src0_sel:BYTE_2
	v_fmac_f32_e32 v145, v82, v109
	v_mul_f32_e32 v74, 0x3d800000, v112
	v_fmac_f32_e32 v145, v76, v110
	v_fmac_f32_e32 v145, v74, v111
	v_cvt_f32_fp8_sdwa v111, v100 src0_sel:BYTE_1
	v_cvt_f32_fp8_sdwa v112, v80 src0_sel:BYTE_1
	v_lshlrev_b32_e32 v161, 16, v105
	v_and_b32_e32 v167, 0xffff0000, v105
	v_and_b32_e32 v105, 0xffff0000, v68
	v_mul_f32_e32 v146, 0x3f9837f0, v105
	v_fmac_f32_e32 v146, v82, v111
	v_lshlrev_b32_e32 v154, 16, v108
	v_and_b32_e32 v152, 0xffff0000, v108
	v_cvt_f32_fp8_sdwa v168, v142 src0_sel:BYTE_3
	v_cvt_f32_fp8_sdwa v108, v142 src0_sel:BYTE_2
	v_cvt_f32_fp8_sdwa v109, v142 src0_sel:BYTE_1
	v_fmac_f32_e32 v146, v76, v112
	v_cvt_f32_fp8_e32 v112, v142
	v_cvt_f32_fp8_e32 v142, v100
	v_cvt_f32_fp8_sdwa v78, v143 src0_sel:BYTE_3
	v_cvt_f32_fp8_sdwa v79, v143 src0_sel:BYTE_2
	v_cvt_f32_fp8_sdwa v104, v143 src0_sel:BYTE_1
	v_cvt_f32_fp8_e32 v105, v143
	v_cvt_f32_fp8_e32 v143, v80
	v_lshlrev_b32_e32 v147, 16, v68
	v_cvt_f32_fp8_e32 v153, v72
	v_mul_f32_e32 v147, 0x3f9837f0, v147
	v_fmac_f32_e32 v147, v82, v142
	s_waitcnt vmcnt(9)
	v_cvt_f32_fp8_sdwa v142, v135 src0_sel:BYTE_3
	v_fmac_f32_e32 v147, v76, v143
	v_cvt_f32_fp8_sdwa v143, v133 src0_sel:BYTE_3
	v_mul_f32_e32 v68, 0x3d800000, v113
	v_fmac_f32_e32 v147, v74, v153
	s_waitcnt vmcnt(4)
	v_cvt_f32_fp8_sdwa v153, v137 src0_sel:BYTE_3
	v_fmac_f32_e32 v147, v68, v112
	s_waitcnt vmcnt(1)
	v_cvt_f32_fp8_sdwa v112, v157 src0_sel:BYTE_3
	v_mul_f32_e32 v148, 0x3f9837f0, v148
	v_fmac_f32_e32 v148, v82, v142
	v_cvt_f32_fp8_sdwa v142, v134 src0_sel:BYTE_3
	v_fmac_f32_e32 v148, v76, v143
	v_cvt_f32_fp8_sdwa v143, v132 src0_sel:BYTE_3
	v_and_b32_e32 v149, 0xffff0000, v107
	v_fmac_f32_e32 v148, v74, v153
	v_cvt_f32_fp8_sdwa v153, v136 src0_sel:BYTE_3
	v_fmac_f32_e32 v148, v68, v112
	v_cvt_f32_fp8_sdwa v112, v156 src0_sel:BYTE_3
	v_mul_f32_e32 v149, 0x3f9837f0, v149
	v_fmac_f32_e32 v149, v82, v142
	v_cvt_f32_fp8_sdwa v142, v135 src0_sel:BYTE_2
	v_fmac_f32_e32 v149, v76, v143
	v_cvt_f32_fp8_sdwa v143, v133 src0_sel:BYTE_2
	v_fmac_f32_e32 v149, v74, v153
	v_cvt_f32_fp8_sdwa v153, v137 src0_sel:BYTE_2
	v_fmac_f32_e32 v149, v68, v112
	v_cvt_f32_fp8_sdwa v112, v157 src0_sel:BYTE_2
	v_mul_f32_e32 v150, 0x3f9837f0, v150
	v_fmac_f32_e32 v150, v82, v142
	v_cvt_f32_fp8_sdwa v142, v134 src0_sel:BYTE_2
	v_fmac_f32_e32 v150, v76, v143
	v_cvt_f32_fp8_sdwa v143, v132 src0_sel:BYTE_2
	v_lshlrev_b32_e32 v151, 16, v107
	v_fmac_f32_e32 v150, v74, v153
	v_cvt_f32_fp8_sdwa v153, v136 src0_sel:BYTE_2
	v_fmac_f32_e32 v150, v68, v112
	v_cvt_f32_fp8_sdwa v112, v156 src0_sel:BYTE_2
	v_mul_f32_e32 v151, 0x3f9837f0, v151
	v_fmac_f32_e32 v151, v82, v142
	v_cvt_f32_fp8_sdwa v142, v135 src0_sel:BYTE_1
	v_fmac_f32_e32 v151, v76, v143
	v_cvt_f32_fp8_sdwa v143, v133 src0_sel:BYTE_1
	v_fmac_f32_e32 v151, v74, v153
	v_cvt_f32_fp8_sdwa v153, v137 src0_sel:BYTE_1
	v_fmac_f32_e32 v151, v68, v112
	v_cvt_f32_fp8_sdwa v112, v157 src0_sel:BYTE_1
	v_mul_f32_e32 v152, 0x3f9837f0, v152
	v_fmac_f32_e32 v152, v82, v142
	v_cvt_f32_fp8_sdwa v142, v134 src0_sel:BYTE_1
	v_fmac_f32_e32 v152, v76, v143
	v_cvt_f32_fp8_sdwa v143, v132 src0_sel:BYTE_1
	v_lshlrev_b32_e32 v155, 16, v106
	v_and_b32_e32 v106, 0xffff0000, v106
	v_fmac_f32_e32 v152, v74, v153
	v_cvt_f32_fp8_sdwa v169, v136 src0_sel:BYTE_1
	v_fmac_f32_e32 v152, v68, v112
	v_cvt_f32_fp8_sdwa v112, v156 src0_sel:BYTE_1
	v_mul_f32_e32 v153, 0x3f9837f0, v106
	v_fmac_f32_e32 v153, v82, v142
	v_fmac_f32_e32 v153, v76, v143
	v_fmac_f32_e32 v153, v74, v169
	v_fmac_f32_e32 v153, v68, v112
	v_cvt_f32_fp8_e32 v112, v135
	v_cvt_f32_fp8_e32 v133, v133
	v_cvt_f32_fp8_e32 v135, v137
	v_cvt_f32_fp8_e32 v106, v157
	v_mul_f32_e32 v154, 0x3f9837f0, v154
	v_fmac_f32_e32 v154, v82, v112
	v_cvt_f32_fp8_e32 v112, v134
	v_fmac_f32_e32 v154, v76, v133
	v_cvt_f32_fp8_e32 v132, v132
	v_fmac_f32_e32 v154, v74, v135
	v_cvt_f32_fp8_e32 v133, v136
	v_fmac_f32_e32 v154, v68, v106
	v_cvt_f32_fp8_e32 v106, v156
	v_mul_f32_e32 v155, 0x3f9837f0, v155
	v_fmac_f32_e32 v155, v82, v112
	v_cvt_f32_fp8_sdwa v112, v127 src0_sel:BYTE_3
	v_fmac_f32_e32 v155, v76, v132
	v_cvt_f32_fp8_sdwa v132, v125 src0_sel:BYTE_3
	v_fmac_f32_e32 v155, v74, v133
	v_cvt_f32_fp8_sdwa v133, v129 src0_sel:BYTE_3
	v_fmac_f32_e32 v155, v68, v106
	v_cvt_f32_fp8_sdwa v106, v131 src0_sel:BYTE_3
	v_mul_f32_e32 v156, 0x3f9837f0, v167
	v_fmac_f32_e32 v156, v82, v112
	v_cvt_f32_fp8_sdwa v112, v126 src0_sel:BYTE_3
	v_fmac_f32_e32 v156, v76, v132
	v_cvt_f32_fp8_sdwa v132, v124 src0_sel:BYTE_3
	v_and_b32_e32 v158, 0xffff0000, v103
	v_fmac_f32_e32 v156, v74, v133
	v_cvt_f32_fp8_sdwa v133, v128 src0_sel:BYTE_3
	v_fmac_f32_e32 v156, v68, v106
	v_cvt_f32_fp8_sdwa v106, v130 src0_sel:BYTE_3
	v_mul_f32_e32 v157, 0x3f9837f0, v158
	v_fmac_f32_e32 v157, v82, v112
	v_cvt_f32_fp8_sdwa v112, v127 src0_sel:BYTE_2
	v_fmac_f32_e32 v157, v76, v132
	v_cvt_f32_fp8_sdwa v132, v125 src0_sel:BYTE_2
	v_fmac_f32_e32 v157, v74, v133
	v_cvt_f32_fp8_sdwa v133, v129 src0_sel:BYTE_2
	v_fmac_f32_e32 v157, v68, v106
	v_cvt_f32_fp8_sdwa v106, v131 src0_sel:BYTE_2
	v_mul_f32_e32 v158, 0x3f9837f0, v161
	v_fmac_f32_e32 v158, v82, v112
	v_cvt_f32_fp8_sdwa v112, v126 src0_sel:BYTE_2
	v_fmac_f32_e32 v158, v76, v132
	v_cvt_f32_fp8_sdwa v132, v124 src0_sel:BYTE_2
	v_lshlrev_b32_e32 v159, 16, v103
	v_fmac_f32_e32 v158, v74, v133
	v_cvt_f32_fp8_sdwa v133, v128 src0_sel:BYTE_2
	v_fmac_f32_e32 v158, v68, v106
	v_cvt_f32_fp8_sdwa v106, v130 src0_sel:BYTE_2
	v_mul_f32_e32 v159, 0x3f9837f0, v159
	v_fmac_f32_e32 v159, v82, v112
	v_cvt_f32_fp8_sdwa v112, v127 src0_sel:BYTE_1
	v_fmac_f32_e32 v159, v76, v132
	v_cvt_f32_fp8_sdwa v132, v125 src0_sel:BYTE_1
	v_fmac_f32_e32 v159, v74, v133
	v_cvt_f32_fp8_sdwa v133, v129 src0_sel:BYTE_1
	v_fmac_f32_e32 v159, v68, v106
	v_cvt_f32_fp8_sdwa v106, v131 src0_sel:BYTE_1
	v_mul_f32_e32 v160, 0x3f9837f0, v160
	v_fmac_f32_e32 v160, v82, v112
	v_cvt_f32_fp8_sdwa v112, v126 src0_sel:BYTE_1
	v_fmac_f32_e32 v160, v76, v132
	v_cvt_f32_fp8_sdwa v132, v124 src0_sel:BYTE_1
	v_lshlrev_b32_e32 v165, 16, v102
	v_and_b32_e32 v102, 0xffff0000, v102
	v_fmac_f32_e32 v160, v74, v133
	v_cvt_f32_fp8_sdwa v133, v128 src0_sel:BYTE_1
	v_fmac_f32_e32 v160, v68, v106
	v_cvt_f32_fp8_sdwa v106, v130 src0_sel:BYTE_1
	v_mul_f32_e32 v161, 0x3f9837f0, v102
	v_fmac_f32_e32 v161, v82, v112
	v_fmac_f32_e32 v161, v76, v132
	v_fmac_f32_e32 v161, v74, v133
	v_fmac_f32_e32 v161, v68, v106
	v_cvt_f32_fp8_e32 v106, v127
	v_cvt_f32_fp8_e32 v112, v125
	v_cvt_f32_fp8_e32 v127, v129
	v_cvt_f32_fp8_e32 v102, v131
	v_mul_f32_e32 v125, 0x3f9837f0, v166
	v_fmac_f32_e32 v125, v82, v106
	v_cvt_f32_fp8_e32 v106, v126
	v_fmac_f32_e32 v125, v76, v112
	v_cvt_f32_fp8_e32 v112, v124
	v_fmac_f32_e32 v125, v74, v127
	v_cvt_f32_fp8_e32 v124, v128
	v_fmac_f32_e32 v125, v68, v102
	v_cvt_f32_fp8_e32 v102, v130
	v_mul_f32_e32 v170, 0x3f9837f0, v165
	v_fmac_f32_e32 v170, v82, v106
	v_cvt_f32_fp8_sdwa v106, v121 src0_sel:BYTE_3
	v_fmac_f32_e32 v170, v76, v112
	v_cvt_f32_fp8_sdwa v112, v115 src0_sel:BYTE_3
	v_lshlrev_b32_e32 v164, 16, v77
	v_and_b32_e32 v77, 0xffff0000, v77
	v_fmac_f32_e32 v170, v74, v124
	v_cvt_f32_fp8_sdwa v124, v117 src0_sel:BYTE_3
	v_fmac_f32_e32 v170, v68, v102
	v_cvt_f32_fp8_sdwa v102, v123 src0_sel:BYTE_3
	v_mul_f32_e32 v165, 0x3f9837f0, v77
	v_fmac_f32_e32 v165, v82, v106
	v_fmac_f32_e32 v165, v76, v112
	v_fmac_f32_e32 v165, v74, v124
	v_fmac_f32_e32 v165, v68, v102
	v_cvt_f32_fp8_sdwa v102, v120 src0_sel:BYTE_3
	v_cvt_f32_fp8_sdwa v106, v114 src0_sel:BYTE_3
	v_lshlrev_b32_e32 v144, 16, v75
	v_and_b32_e32 v75, 0xffff0000, v75
	v_cvt_f32_fp8_sdwa v112, v116 src0_sel:BYTE_3
	v_cvt_f32_fp8_sdwa v77, v122 src0_sel:BYTE_3
	v_mul_f32_e32 v124, 0x3f9837f0, v75
	v_fmac_f32_e32 v124, v82, v102
	v_fmac_f32_e32 v124, v76, v106
	v_fmac_f32_e32 v124, v74, v112
	v_fmac_f32_e32 v124, v68, v77
	v_cvt_f32_fp8_sdwa v77, v121 src0_sel:BYTE_2
	v_cvt_f32_fp8_sdwa v102, v115 src0_sel:BYTE_2
	v_cvt_f32_fp8_sdwa v106, v117 src0_sel:BYTE_2
	v_cvt_f32_fp8_sdwa v75, v123 src0_sel:BYTE_2
	v_mul_f32_e32 v164, 0x3f9837f0, v164
	v_fmac_f32_e32 v164, v82, v77
	v_cvt_f32_fp8_sdwa v77, v120 src0_sel:BYTE_2
	v_fmac_f32_e32 v164, v76, v102
	v_cvt_f32_fp8_sdwa v102, v114 src0_sel:BYTE_2
	v_fmac_f32_e32 v164, v74, v106
	v_cvt_f32_fp8_sdwa v106, v116 src0_sel:BYTE_2
	v_fmac_f32_e32 v164, v68, v75
	v_cvt_f32_fp8_sdwa v75, v122 src0_sel:BYTE_2
	v_mul_f32_e32 v171, 0x3f9837f0, v144
	v_fmac_f32_e32 v171, v82, v77
	v_cvt_f32_fp8_sdwa v77, v121 src0_sel:BYTE_1
	v_fmac_f32_e32 v171, v76, v102
	v_cvt_f32_fp8_sdwa v102, v115 src0_sel:BYTE_1
	v_fmac_f32_e32 v171, v74, v106
	v_cvt_f32_fp8_sdwa v106, v117 src0_sel:BYTE_1
	v_fmac_f32_e32 v171, v68, v75
	v_cvt_f32_fp8_sdwa v75, v123 src0_sel:BYTE_1
	v_mul_f32_e32 v163, 0x3f9837f0, v163
	v_fmac_f32_e32 v163, v82, v77
	v_cvt_f32_fp8_sdwa v77, v120 src0_sel:BYTE_1
	v_fmac_f32_e32 v163, v76, v102
	v_cvt_f32_fp8_sdwa v102, v114 src0_sel:BYTE_1
	v_fmac_f32_e32 v163, v74, v106
	v_cvt_f32_fp8_sdwa v106, v116 src0_sel:BYTE_1
	v_fmac_f32_e32 v163, v68, v75
	v_cvt_f32_fp8_sdwa v75, v122 src0_sel:BYTE_1
	v_mul_f32_e32 v172, 0x3f9837f0, v141
	v_fmac_f32_e32 v172, v82, v77
	v_cvt_f32_fp8_e32 v77, v121
	v_fmac_f32_e32 v172, v76, v102
	v_cvt_f32_fp8_e32 v102, v115
	v_fmac_f32_e32 v172, v74, v106
	v_cvt_f32_fp8_e32 v106, v117
	v_fmac_f32_e32 v172, v68, v75
	v_cvt_f32_fp8_e32 v75, v123
	v_mul_f32_e32 v162, 0x3f9837f0, v162
	v_fmac_f32_e32 v162, v82, v77
	v_cvt_f32_fp8_e32 v77, v120
	v_fmac_f32_e32 v162, v76, v102
	v_cvt_f32_fp8_e32 v102, v114
	v_fmac_f32_e32 v162, v74, v106
	v_cvt_f32_fp8_e32 v106, v116
	v_fmac_f32_e32 v162, v68, v75
	v_cvt_f32_fp8_e32 v75, v122
	v_mul_f32_e32 v173, 0x3f9837f0, v83
	v_fmac_f32_e32 v173, v82, v77
	v_fmac_f32_e32 v173, v76, v102
	v_fmac_f32_e32 v173, v74, v106
	v_and_b32_e32 v69, 0xffff0000, v69
	v_fmac_f32_e32 v173, v68, v75
	v_mul_f32_e32 v174, 0x3f9837f0, v69
	v_add_f32_e32 v69, 0, v173
	v_add_f32_e32 v69, v172, v69
	v_add_f32_e32 v69, v171, v69
	v_add_f32_e32 v69, v124, v69
	v_add_f32_e32 v69, v162, v69
	v_add_f32_e32 v69, v163, v69
	v_add_f32_e32 v69, v164, v69
	v_add_f32_e32 v69, v165, v69
	v_add_f32_e32 v69, v170, v69
	v_add_f32_e32 v69, v161, v69
	v_add_f32_e32 v69, v159, v69
	v_add_f32_e32 v69, v157, v69
	v_add_f32_e32 v69, v125, v69
	v_add_f32_e32 v69, v160, v69
	v_cvt_f32_fp8_sdwa v119, v72 src0_sel:BYTE_1
	v_add_f32_e32 v69, v158, v69
	v_add_f32_e32 v69, v156, v69
	v_add_f32_e32 v69, v155, v69
	v_add_f32_e32 v69, v153, v69
	v_fmac_f32_e32 v146, v74, v119
	v_add_f32_e32 v69, v151, v69
	v_cvt_f32_fp8_sdwa v103, v73 src0_sel:BYTE_2
	v_fmac_f32_e32 v145, v68, v108
	v_cvt_f32_fp8_sdwa v108, v73 src0_sel:BYTE_1
	v_fmac_f32_e32 v146, v68, v109
	v_cvt_f32_fp8_e32 v109, v73
	v_cvt_f32_fp8_sdwa v102, v73 src0_sel:BYTE_3
	v_cvt_f32_fp8_sdwa v73, v100 src0_sel:BYTE_3
	v_add_f32_e32 v69, v149, v69
	v_cvt_f32_fp8_sdwa v75, v80 src0_sel:BYTE_3
	v_add_f32_e32 v69, v154, v69
	v_cvt_f32_fp8_sdwa v72, v72 src0_sel:BYTE_3
	v_add_f32_e32 v69, v152, v69
	v_add_f32_e32 v69, v150, v69
	v_fmac_f32_e32 v174, v82, v73
	v_add_f32_e32 v69, v148, v69
	v_cvt_f32_fp8_sdwa v113, v101 src0_sel:BYTE_2
	v_cvt_f32_fp8_sdwa v112, v101 src0_sel:BYTE_3
	v_fmac_f32_e32 v174, v76, v75
	v_add_f32_e32 v69, v147, v69
	v_cvt_f32_fp8_sdwa v107, v81 src0_sel:BYTE_2
	v_cvt_f32_fp8_sdwa v106, v81 src0_sel:BYTE_3
	v_fmac_f32_e32 v174, v74, v72
	v_add_f32_e32 v69, v146, v69
	v_fmac_f32_e32 v174, v68, v168
	v_add_f32_e32 v69, v145, v69
	v_and_b32_e32 v72, 0xffff0000, v71
	v_lshlrev_b32_e32 v73, 16, v71
	v_add_f32_e32 v75, v174, v69
	v_and_b32_e32 v69, 64, v140
	v_pk_mul_f32 v[72:73], v[72:73], s[18:19] op_sel_hi:[1,0]
	v_add_u32_e32 v77, 64, v69
	v_xor_b32_e32 v69, 1, v140
	v_pk_fma_f32 v[72:73], v[82:83], v[112:113], v[72:73] op_sel_hi:[0,1,1]
	v_cvt_f32_fp8_sdwa v118, v101 src0_sel:BYTE_1
	v_cvt_f32_fp8_e32 v119, v101
	v_cmp_lt_i32_e32 vcc, v69, v77
	v_pk_fma_f32 v[72:73], v[76:77], v[106:107], v[72:73] op_sel_hi:[0,1,1]
	v_cvt_f32_fp8_sdwa v110, v81 src0_sel:BYTE_1
	v_cvt_f32_fp8_e32 v111, v81
	v_cndmask_b32_e32 v69, v140, v69, vcc
	v_pk_fma_f32 v[72:73], v[74:75], v[102:103], v[72:73] op_sel_hi:[0,1,1]
	v_pk_fma_f32 v[72:73], v[68:69], v[78:79], v[72:73] op_sel_hi:[0,1,1]
	v_and_b32_e32 v78, 0xffff0000, v70
	v_lshlrev_b32_e32 v79, 16, v70
	v_pk_mul_f32 v[70:71], v[78:79], s[18:19] op_sel_hi:[1,0]
	v_lshlrev_b32_e32 v136, 2, v69
	v_pk_fma_f32 v[70:71], v[82:83], v[118:119], v[70:71] op_sel_hi:[0,1,1]
	v_pk_fma_f32 v[70:71], v[76:77], v[110:111], v[70:71] op_sel_hi:[0,1,1]
	v_pk_fma_f32 v[70:71], v[74:75], v[108:109], v[70:71] op_sel_hi:[0,1,1]
	v_pk_fma_f32 v[68:69], v[68:69], v[104:105], v[70:71] op_sel_hi:[0,1,1]
	v_add_f32_e32 v70, v69, v75
	v_add_f32_e32 v70, v68, v70
	v_add_f32_e32 v70, v73, v70
	v_add_f32_e32 v70, v72, v70
	v_xor_b32_e32 v74, 2, v140
	v_cmp_lt_i32_e32 vcc, v74, v77
	v_lshl_add_u64 v[106:107], s[24:25], 0, v[84:85]
	s_waitcnt lgkmcnt(0)
	s_nop 1
	v_add_f32_dpp v70, v70, v70 quad_perm:[1,0,3,2] row_mask:0xf bank_mask:0xf
	v_cndmask_b32_e32 v74, v140, v74, vcc
	v_lshlrev_b32_e32 v137, 2, v74
	v_xor_b32_e32 v74, 4, v140
	v_cmp_lt_i32_e32 vcc, v74, v77
	s_waitcnt lgkmcnt(0)
	s_nop 1
	v_add_f32_dpp v70, v70, v70 quad_perm:[2,3,0,1] row_mask:0xf bank_mask:0xf
	v_cndmask_b32_e32 v74, v140, v74, vcc
	v_lshlrev_b32_e32 v141, 2, v74
	v_xor_b32_e32 v74, 8, v140
	v_cmp_lt_i32_e32 vcc, v74, v77
	s_waitcnt lgkmcnt(0)
	s_nop 1
	v_add_f32_dpp v70, v70, v70 row_half_mirror row_mask:0xf bank_mask:0xf
	v_cndmask_b32_e32 v74, v140, v74, vcc
	v_lshlrev_b32_e32 v142, 2, v74
	v_xor_b32_e32 v74, 16, v140
	v_cmp_lt_i32_e32 vcc, v74, v77
	s_waitcnt lgkmcnt(0)
	s_nop 1
	v_add_f32_dpp v70, v70, v70 row_mirror row_mask:0xf bank_mask:0xf
	v_cndmask_b32_e32 v74, v140, v74, vcc
	v_lshlrev_b32_e32 v143, 2, v74
	v_xor_b32_e32 v74, 32, v140
	v_cmp_lt_i32_e32 vcc, v74, v77
	s_waitcnt lgkmcnt(0)
	v_mov_b32_e32 v71, v70
	s_nop 1
	v_permlane16_swap_b32_e32 v70, v71
	v_add_f32_e32 v70, v70, v71
	v_cndmask_b32_e32 v74, v140, v74, vcc
	v_lshlrev_b32_e32 v144, 2, v74
	v_add_co_u32_e32 v122, vcc, s28, v106
	s_waitcnt lgkmcnt(0)
	v_mov_b32_e32 v71, v70
	s_nop 1
	v_permlane32_swap_b32_e32 v70, v71
	v_add_f32_e32 v71, v70, v71
	v_fmac_f32_e32 v172, 0xba000000, v71
	v_fmac_f32_e32 v173, 0xba000000, v71
	v_mul_f32_e32 v74, v172, v172
	v_fmac_f32_e32 v74, v173, v173
	v_fmac_f32_e32 v171, 0xba000000, v71
	v_fmac_f32_e32 v74, v171, v171
	v_fmac_f32_e32 v124, 0xba000000, v71
	v_fmac_f32_e32 v74, v124, v124
	v_fmac_f32_e32 v162, 0xba000000, v71
	v_fmac_f32_e32 v74, v162, v162
	v_fmac_f32_e32 v163, 0xba000000, v71
	v_fmac_f32_e32 v74, v163, v163
	v_fmac_f32_e32 v164, 0xba000000, v71
	v_fmac_f32_e32 v74, v164, v164
	v_fmac_f32_e32 v165, 0xba000000, v71
	v_fmac_f32_e32 v74, v165, v165
	v_fmac_f32_e32 v170, 0xba000000, v71
	v_fmac_f32_e32 v74, v170, v170
	v_fmac_f32_e32 v161, 0xba000000, v71
	v_fmac_f32_e32 v74, v161, v161
	v_fmac_f32_e32 v159, 0xba000000, v71
	v_fmac_f32_e32 v74, v159, v159
	v_fmac_f32_e32 v157, 0xba000000, v71
	v_fmac_f32_e32 v74, v157, v157
	v_fmac_f32_e32 v125, 0xba000000, v71
	v_fmac_f32_e32 v74, v125, v125
	v_fmac_f32_e32 v160, 0xba000000, v71
	v_fmac_f32_e32 v74, v160, v160
	v_fmac_f32_e32 v158, 0xba000000, v71
	v_fmac_f32_e32 v74, v158, v158
	v_fmac_f32_e32 v156, 0xba000000, v71
	v_fmac_f32_e32 v74, v156, v156
	v_fmac_f32_e32 v155, 0xba000000, v71
	v_fmac_f32_e32 v74, v155, v155
	v_fmac_f32_e32 v153, 0xba000000, v71
	v_fmac_f32_e32 v74, v153, v153
	v_fmac_f32_e32 v151, 0xba000000, v71
	v_fmac_f32_e32 v74, v151, v151
	v_fmac_f32_e32 v149, 0xba000000, v71
	v_fmac_f32_e32 v74, v149, v149
	v_fmac_f32_e32 v154, 0xba000000, v71
	v_fmac_f32_e32 v74, v154, v154
	v_fmac_f32_e32 v152, 0xba000000, v71
	v_fmac_f32_e32 v74, v152, v152
	v_fmac_f32_e32 v150, 0xba000000, v71
	v_fmac_f32_e32 v74, v150, v150
	v_fmac_f32_e32 v148, 0xba000000, v71
	v_fmac_f32_e32 v74, v148, v148
	v_fmac_f32_e32 v147, 0xba000000, v71
	v_fmac_f32_e32 v74, v147, v147
	v_fmac_f32_e32 v146, 0xba000000, v71
	v_mul_f32_e32 v70, 0x3a000000, v71
	v_fmac_f32_e32 v74, v146, v146
	v_fmac_f32_e32 v145, 0xba000000, v71
	v_fmac_f32_e32 v74, v145, v145
	v_fmac_f32_e32 v174, 0xba000000, v71
	v_pk_add_f32 v[166:167], v[68:69], v[70:71] op_sel_hi:[1,0] neg_lo:[0,1] neg_hi:[0,1]
	v_fmac_f32_e32 v74, v174, v174
	v_pk_mul_f32 v[68:69], v[166:167], v[166:167]
	v_addc_co_u32_e32 v123, vcc, 0, v107, vcc
	v_add_f32_e32 v69, v69, v74
	v_add_f32_e32 v71, v68, v69
	v_pk_add_f32 v[168:169], v[72:73], v[70:71] op_sel_hi:[1,0] neg_lo:[0,1] neg_hi:[0,1]
	s_nop 0
	v_pk_mul_f32 v[68:69], v[168:169], v[168:169]
	s_nop 0
	v_add_f32_e32 v69, v69, v71
	v_add_f32_e32 v70, v68, v69
	v_lshl_add_u64 v[68:69], v[86:87], 0, s[22:23]
	s_waitcnt lgkmcnt(0)
	s_nop 1
	v_add_f32_dpp v100, v70, v70 quad_perm:[1,0,3,2] row_mask:0xf bank_mask:0xf
	global_load_dwordx4 v[72:75], v[68:69], off
	global_load_dwordx4 v[76:79], v[68:69], off offset:1024
	global_load_dwordx4 v[80:83], v[68:69], off offset:2048
	s_nop 0
	global_load_dwordx4 v[68:71], v[68:69], off offset:3072
	s_waitcnt lgkmcnt(0)
	s_nop 1
	v_add_f32_dpp v102, v100, v100 quad_perm:[2,3,0,1] row_mask:0xf bank_mask:0xf
	global_load_dwordx2 v[104:105], v[106:107], off
	global_load_dwordx2 v[114:115], v[106:107], off offset:512
	global_load_dwordx2 v[126:127], v[106:107], off offset:1024
	global_load_dwordx2 v[100:101], v[106:107], off offset:1536
	s_waitcnt lgkmcnt(0)
	s_nop 1
	v_add_f32_dpp v110, v102, v102 row_half_mirror row_mask:0xf bank_mask:0xf
	global_load_dwordx2 v[108:109], v[106:107], off offset:2048
	global_load_dwordx2 v[116:117], v[106:107], off offset:2560
	global_load_dwordx2 v[128:129], v[106:107], off offset:3072
	global_load_dwordx2 v[102:103], v[106:107], off offset:3584
	s_waitcnt lgkmcnt(0)
	s_nop 1
	v_add_f32_dpp v110, v110, v110 row_mirror row_mask:0xf bank_mask:0xf
	s_waitcnt lgkmcnt(0)
	v_mov_b32_e32 v111, v110
	s_nop 1
	v_permlane16_swap_b32_e32 v110, v111
	v_add_f32_e32 v112, v110, v111
	global_load_dwordx2 v[110:111], v[122:123], off
	global_load_dwordx2 v[118:119], v[122:123], off offset:512
	global_load_dwordx2 v[130:131], v[122:123], off offset:1024
	global_load_dwordx2 v[106:107], v[122:123], off offset:1536
	s_waitcnt lgkmcnt(0)
	v_mov_b32_e32 v113, v112
	s_nop 1
	v_permlane32_swap_b32_e32 v112, v113
	v_add_f32_e32 v112, v112, v113
	v_fmamk_f32 v112, v112, 0x3a000000, v139
	v_mul_f32_e32 v113, 0x4b800000, v112
	v_cmp_gt_f32_e32 vcc, s29, v112
	s_nop 1
	v_cndmask_b32_e32 v112, v112, v113, vcc
	v_rsq_f32_e32 v175, v112
	global_load_dwordx2 v[112:113], v[122:123], off offset:2048
	global_load_dwordx2 v[120:121], v[122:123], off offset:2560
	global_load_dwordx2 v[132:133], v[122:123], off offset:3072
	global_load_dwordx2 v[134:135], v[122:123], off offset:3584
	v_mul_f32_e32 v122, 0x45800000, v175
	v_cndmask_b32_e32 v175, v175, v122, vcc
	v_mul_f32_e32 v122, v173, v175
	v_fma_f32 v123, v56, v122, v48
	v_mul_f32_e32 v122, v162, v175
	v_fma_f32 v173, v60, v122, v52
	v_mul_f32_e32 v122, v172, v175
	v_fma_f32 v172, v57, v122, v49
	v_mul_f32_e32 v122, v163, v175
	v_fma_f32 v176, v61, v122, v53
	v_mul_f32_e32 v122, v171, v175
	v_fma_f32 v171, v58, v122, v50
	v_mul_f32_e32 v122, v164, v175
	v_fma_f32 v177, v62, v122, v54
	v_mul_f32_e32 v122, v124, v175
	v_fma_f32 v124, v59, v122, v51
	v_mul_f32_e32 v122, v165, v175
	v_fma_f32 v178, v63, v122, v55
	v_mov_b32_e32 v122, 0
	v_cvt_pk_bf16_f32 v162, v123, v172
	v_cvt_pk_fp8_f32 v122, v123, v172
	v_mov_b32_e32 v123, 0
	v_cvt_pk_fp8_f32 v123, v173, v176
	v_add_co_u32_e32 v98, vcc, s30, v98
	v_cvt_pk_bf16_f32 v163, v171, v124
	v_cvt_pk_fp8_f32 v122, v171, v124 op_sel:[0,0,1]
	s_nop 0
	v_addc_co_u32_e32 v99, vcc, 0, v99, vcc
	v_cvt_pk_fp8_f32 v123, v177, v178 op_sel:[0,0,1]
	v_cvt_pk_bf16_f32 v164, v173, v176
	v_cvt_pk_bf16_f32 v165, v177, v178
	global_store_dwordx4 v[98:99], v[162:165], off
	v_mul_f32_e32 v157, v157, v175
	v_mul_f32_e32 v156, v156, v175
	v_lshl_add_u64 v[162:163], s[90:91], 0, v[92:93]
	v_add_co_u32_e32 v162, vcc, s31, v162
	v_mul_f32_e32 v159, v159, v175
	s_nop 0
	v_addc_co_u32_e32 v163, vcc, 0, v163, vcc
	global_store_dwordx2 v[162:163], v[122:123], off
	v_mul_f32_e32 v123, v125, v175
	v_mul_f32_e32 v122, v170, v175
	v_fma_f32 v124, v44, v123, v36
	v_mul_f32_e32 v123, v161, v175
	v_mul_f32_e32 v125, v160, v175
	v_fma_f32 v122, v40, v122, v32
	v_fma_f32 v123, v41, v123, v33
	v_fma_f32 v125, v45, v125, v37
	v_fma_f32 v160, v43, v157, v35
	v_fma_f32 v161, v47, v156, v39
	v_mov_b32_e32 v156, 0
	v_mov_b32_e32 v157, 0
	v_cvt_pk_fp8_f32 v156, v122, v123
	v_cvt_pk_fp8_f32 v157, v124, v125
	v_mul_f32_e32 v158, v158, v175
	v_fma_f32 v159, v42, v159, v34
	v_fma_f32 v158, v46, v158, v38
	v_cvt_pk_fp8_f32 v156, v159, v160 op_sel:[0,0,1]
	v_cvt_pk_fp8_f32 v157, v158, v161 op_sel:[0,0,1]
	v_cvt_pk_bf16_f32 v122, v122, v123
	v_cvt_pk_bf16_f32 v123, v159, v160
	v_cvt_pk_bf16_f32 v124, v124, v125
	v_cvt_pk_bf16_f32 v125, v158, v161
	global_store_dwordx4 v[98:99], v[122:125], off offset:1024
	global_store_dwordx2 v[162:163], v[156:157], off offset:512
	v_mul_f32_e32 v149, v149, v175
	v_mul_f32_e32 v123, v154, v175
	v_mul_f32_e32 v122, v155, v175
	v_fma_f32 v124, v28, v123, v20
	v_mul_f32_e32 v123, v153, v175
	v_mul_f32_e32 v125, v152, v175
	v_mul_f32_e32 v148, v148, v175
	v_fma_f32 v122, v24, v122, v16
	v_fma_f32 v123, v25, v123, v17
	v_fma_f32 v125, v29, v125, v21
	v_fma_f32 v152, v27, v149, v19
	v_fma_f32 v153, v31, v148, v23
	v_mov_b32_e32 v148, 0
	v_mov_b32_e32 v149, 0
	v_cvt_pk_fp8_f32 v148, v122, v123
	v_cvt_pk_fp8_f32 v149, v124, v125
	v_mul_f32_e32 v151, v151, v175
	v_mul_f32_e32 v150, v150, v175
	v_fma_f32 v151, v26, v151, v18
	v_fma_f32 v150, v30, v150, v22
	v_cvt_pk_fp8_f32 v148, v151, v152 op_sel:[0,0,1]
	v_cvt_pk_fp8_f32 v149, v150, v153 op_sel:[0,0,1]
	v_cvt_pk_bf16_f32 v122, v122, v123
	v_cvt_pk_bf16_f32 v123, v151, v152
	v_cvt_pk_bf16_f32 v124, v124, v125
	v_cvt_pk_bf16_f32 v125, v150, v153
	global_store_dwordx4 v[98:99], v[122:125], off offset:2048
	global_store_dwordx2 v[162:163], v[148:149], off offset:1024
	v_mul_f32_e32 v145, v145, v175
	v_mul_f32_e32 v123, v167, v175
	v_fma_f32 v124, v12, v123, v4
	v_mul_f32_e32 v123, v146, v175
	v_mul_f32_e32 v146, v169, v175
	v_fma_f32 v148, v14, v146, v6
	v_mul_f32_e32 v146, v174, v175
	v_mul_f32_e32 v122, v147, v175
	v_mul_f32_e32 v125, v166, v175
	v_fma_f32 v149, v11, v146, v3
	v_mul_f32_e32 v146, v168, v175
	v_fma_f32 v122, v8, v122, v0
	v_fma_f32 v123, v9, v123, v1
	v_fma_f32 v125, v13, v125, v5
	v_fma_f32 v150, v15, v146, v7
	v_mov_b32_e32 v146, 0
	v_mov_b32_e32 v147, 0
	v_cvt_pk_fp8_f32 v146, v122, v123
	v_cvt_pk_fp8_f32 v147, v124, v125
	v_fma_f32 v145, v10, v145, v2
	v_cvt_pk_bf16_f32 v122, v122, v123
	v_cvt_pk_fp8_f32 v146, v145, v149 op_sel:[0,0,1]
	v_cvt_pk_fp8_f32 v147, v148, v150 op_sel:[0,0,1]
	v_cvt_pk_bf16_f32 v123, v145, v149
	v_cvt_pk_bf16_f32 v124, v124, v125
	v_cvt_pk_bf16_f32 v125, v148, v150
	global_store_dwordx4 v[98:99], v[122:125], off offset:3072
	global_store_dwordx2 v[162:163], v[146:147], off offset:1536
	s_cbranch_scc1 .LBB0_1262
	s_waitcnt vmcnt(24)
	v_lshlrev_b32_e32 v98, 16, v69
	v_and_b32_e32 v148, 0xffff0000, v69
	s_waitcnt vmcnt(20)
	v_cvt_f32_fp8_sdwa v69, v100 src0_sel:BYTE_2
	v_lshlrev_b32_e32 v166, 16, v73
	v_and_b32_e32 v167, 0xffff0000, v73
	s_waitcnt vmcnt(16)
	v_cvt_f32_fp8_sdwa v73, v102 src0_sel:BYTE_2
	v_lshlrev_b32_e32 v153, 16, v78
	v_and_b32_e32 v154, 0xffff0000, v78
	v_lshlrev_b32_e32 v164, 16, v72
	v_and_b32_e32 v165, 0xffff0000, v72
	v_mul_f32_e32 v72, 0x3d800000, v65
	v_mul_f32_e32 v64, 0x3d800000, v64
	s_waitcnt vmcnt(12)
	v_cvt_f32_fp8_sdwa v78, v106 src0_sel:BYTE_2
	v_mul_f32_e32 v65, 0x3f9837f0, v98
	v_lshlrev_b32_e32 v122, 16, v68
	v_and_b32_e32 v99, 0xffff0000, v68
	v_mul_f32_e32 v68, 0x3d800000, v67
	s_waitcnt vmcnt(8)
	v_cvt_f32_fp8_sdwa v67, v134 src0_sel:BYTE_2
	v_fmac_f32_e32 v65, v64, v69
	v_fmac_f32_e32 v65, v72, v73
	v_cvt_f32_fp8_sdwa v73, v100 src0_sel:BYTE_1
	v_lshlrev_b32_e32 v155, 16, v79
	v_and_b32_e32 v156, 0xffff0000, v79
	v_mul_f32_e32 v66, 0x3d800000, v66
	v_cvt_f32_fp8_sdwa v79, v102 src0_sel:BYTE_1
	v_lshlrev_b32_e32 v145, 16, v83
	v_and_b32_e32 v147, 0xffff0000, v83
	v_fmac_f32_e32 v65, v66, v78
	v_cvt_f32_fp8_sdwa v83, v106 src0_sel:BYTE_1
	v_fmac_f32_e32 v65, v68, v67
	v_cvt_f32_fp8_sdwa v69, v134 src0_sel:BYTE_1
	v_mul_f32_e32 v67, 0x3f9837f0, v99
	v_cvt_f32_fp8_sdwa v168, v134 src0_sel:BYTE_3
	v_fmac_f32_e32 v67, v64, v73
	v_cvt_f32_fp8_e32 v73, v134
	v_cvt_f32_fp8_e32 v134, v100
	v_lshlrev_b32_e32 v160, 16, v74
	v_and_b32_e32 v161, 0xffff0000, v74
	v_lshlrev_b32_e32 v162, 16, v75
	v_and_b32_e32 v163, 0xffff0000, v75
	v_cvt_f32_fp8_sdwa v74, v135 src0_sel:BYTE_3
	v_cvt_f32_fp8_sdwa v75, v135 src0_sel:BYTE_2
	v_cvt_f32_fp8_sdwa v78, v135 src0_sel:BYTE_1
	v_fmac_f32_e32 v67, v72, v79
	v_cvt_f32_fp8_e32 v79, v135
	v_cvt_f32_fp8_e32 v135, v102
	v_fmac_f32_e32 v67, v66, v83
	v_cvt_f32_fp8_e32 v169, v106
	v_fmac_f32_e32 v67, v68, v69
	v_mul_f32_e32 v69, 0x3f9837f0, v122
	v_fmac_f32_e32 v69, v64, v134
	v_cvt_f32_fp8_sdwa v134, v127 src0_sel:BYTE_3
	v_fmac_f32_e32 v69, v72, v135
	v_cvt_f32_fp8_sdwa v135, v129 src0_sel:BYTE_3
	v_fmac_f32_e32 v69, v66, v169
	v_fmac_f32_e32 v69, v68, v73
	v_mul_f32_e32 v73, 0x3f9837f0, v147
	v_fmac_f32_e32 v73, v64, v134
	v_cvt_f32_fp8_sdwa v169, v131 src0_sel:BYTE_3
	v_fmac_f32_e32 v73, v72, v135
	v_cvt_f32_fp8_sdwa v135, v126 src0_sel:BYTE_3
	v_cvt_f32_fp8_sdwa v122, v133 src0_sel:BYTE_3
	v_cvt_f32_fp8_sdwa v147, v128 src0_sel:BYTE_3
	v_and_b32_e32 v152, 0xffff0000, v81
	v_mul_f32_e32 v134, 0x3f9837f0, v152
	v_fmac_f32_e32 v73, v66, v169
	v_cvt_f32_fp8_sdwa v169, v130 src0_sel:BYTE_3
	v_fmac_f32_e32 v134, v64, v135
	v_fmac_f32_e32 v73, v68, v122
	v_cvt_f32_fp8_sdwa v122, v132 src0_sel:BYTE_3
	v_fmac_f32_e32 v134, v72, v147
	v_cvt_f32_fp8_sdwa v147, v127 src0_sel:BYTE_2
	v_cvt_f32_fp8_sdwa v152, v129 src0_sel:BYTE_2
	v_fmac_f32_e32 v134, v66, v169
	v_cvt_f32_fp8_sdwa v169, v131 src0_sel:BYTE_2
	v_mul_f32_e32 v135, 0x3f9837f0, v145
	v_fmac_f32_e32 v134, v68, v122
	v_cvt_f32_fp8_sdwa v122, v133 src0_sel:BYTE_2
	v_fmac_f32_e32 v135, v64, v147
	v_cvt_f32_fp8_sdwa v147, v126 src0_sel:BYTE_2
	v_lshlrev_b32_e32 v151, 16, v81
	v_fmac_f32_e32 v135, v72, v152
	v_cvt_f32_fp8_sdwa v152, v128 src0_sel:BYTE_2
	v_fmac_f32_e32 v135, v66, v169
	v_cvt_f32_fp8_sdwa v169, v130 src0_sel:BYTE_2
	v_mul_f32_e32 v145, 0x3f9837f0, v151
	v_fmac_f32_e32 v135, v68, v122
	v_cvt_f32_fp8_sdwa v122, v132 src0_sel:BYTE_2
	v_fmac_f32_e32 v145, v64, v147
	v_cvt_f32_fp8_sdwa v147, v127 src0_sel:BYTE_1
	v_cvt_f32_fp8_sdwa v151, v129 src0_sel:BYTE_1
	v_and_b32_e32 v146, 0xffff0000, v82
	v_fmac_f32_e32 v145, v72, v152
	v_cvt_f32_fp8_sdwa v152, v131 src0_sel:BYTE_1
	v_fmac_f32_e32 v145, v66, v169
	v_mul_f32_e32 v146, 0x3f9837f0, v146
	v_fmac_f32_e32 v145, v68, v122
	v_cvt_f32_fp8_sdwa v122, v133 src0_sel:BYTE_1
	v_fmac_f32_e32 v146, v64, v147
	v_fmac_f32_e32 v146, v72, v151
	v_cvt_f32_fp8_sdwa v151, v126 src0_sel:BYTE_1
	v_fmac_f32_e32 v146, v66, v152
	v_cvt_f32_fp8_sdwa v152, v128 src0_sel:BYTE_1
	v_lshlrev_b32_e32 v150, 16, v80
	v_and_b32_e32 v80, 0xffff0000, v80
	v_cvt_f32_fp8_sdwa v169, v130 src0_sel:BYTE_1
	v_fmac_f32_e32 v146, v68, v122
	v_cvt_f32_fp8_sdwa v122, v132 src0_sel:BYTE_1
	v_mul_f32_e32 v147, 0x3f9837f0, v80
	v_fmac_f32_e32 v147, v64, v151
	v_fmac_f32_e32 v147, v72, v152
	v_fmac_f32_e32 v147, v66, v169
	v_fmac_f32_e32 v147, v68, v122
	v_cvt_f32_fp8_e32 v122, v127
	v_lshlrev_b32_e32 v149, 16, v82
	v_cvt_f32_fp8_e32 v129, v129
	v_mul_f32_e32 v127, 0x3f9837f0, v149
	v_fmac_f32_e32 v127, v64, v122
	v_cvt_f32_fp8_e32 v122, v126
	v_cvt_f32_fp8_e32 v131, v131
	v_cvt_f32_fp8_e32 v128, v128
	v_cvt_f32_fp8_e32 v80, v133
	v_fmac_f32_e32 v127, v72, v129
	v_cvt_f32_fp8_e32 v129, v130
	v_mul_f32_e32 v126, 0x3f9837f0, v150
	v_fmac_f32_e32 v126, v64, v122
	v_fmac_f32_e32 v127, v66, v131
	v_fmac_f32_e32 v126, v72, v128
	v_cvt_f32_fp8_sdwa v122, v115 src0_sel:BYTE_3
	v_fmac_f32_e32 v127, v68, v80
	v_cvt_f32_fp8_e32 v80, v132
	v_fmac_f32_e32 v126, v66, v129
	v_cvt_f32_fp8_sdwa v129, v117 src0_sel:BYTE_3
	v_cvt_f32_fp8_sdwa v130, v119 src0_sel:BYTE_3
	v_mul_f32_e32 v128, 0x3f9837f0, v156
	v_fmac_f32_e32 v128, v64, v122
	v_fmac_f32_e32 v126, v68, v80
	v_cvt_f32_fp8_sdwa v80, v121 src0_sel:BYTE_3
	v_fmac_f32_e32 v128, v72, v129
	v_cvt_f32_fp8_sdwa v122, v114 src0_sel:BYTE_3
	v_fmac_f32_e32 v128, v66, v130
	v_cvt_f32_fp8_sdwa v130, v116 src0_sel:BYTE_3
	v_and_b32_e32 v159, 0xffff0000, v77
	v_cvt_f32_fp8_sdwa v131, v118 src0_sel:BYTE_3
	v_mul_f32_e32 v129, 0x3f9837f0, v159
	v_fmac_f32_e32 v128, v68, v80
	v_cvt_f32_fp8_sdwa v80, v120 src0_sel:BYTE_3
	v_fmac_f32_e32 v129, v64, v122
	v_fmac_f32_e32 v129, v72, v130
	v_cvt_f32_fp8_sdwa v122, v115 src0_sel:BYTE_2
	v_fmac_f32_e32 v129, v66, v131
	v_cvt_f32_fp8_sdwa v131, v117 src0_sel:BYTE_2
	v_cvt_f32_fp8_sdwa v132, v119 src0_sel:BYTE_2
	v_fmac_f32_e32 v129, v68, v80
	v_cvt_f32_fp8_sdwa v80, v121 src0_sel:BYTE_2
	v_mul_f32_e32 v130, 0x3f9837f0, v155
	v_fmac_f32_e32 v130, v64, v122
	v_cvt_f32_fp8_sdwa v122, v114 src0_sel:BYTE_2
	v_fmac_f32_e32 v130, v72, v131
	v_cvt_f32_fp8_sdwa v131, v116 src0_sel:BYTE_2
	v_lshlrev_b32_e32 v158, 16, v77
	v_fmac_f32_e32 v130, v66, v132
	v_cvt_f32_fp8_sdwa v132, v118 src0_sel:BYTE_2
	v_fmac_f32_e32 v130, v68, v80
	v_cvt_f32_fp8_sdwa v80, v120 src0_sel:BYTE_2
	v_mul_f32_e32 v133, 0x3f9837f0, v158
	v_fmac_f32_e32 v133, v64, v122
	v_cvt_f32_fp8_sdwa v122, v115 src0_sel:BYTE_1
	v_fmac_f32_e32 v133, v72, v131
	v_cvt_f32_fp8_sdwa v131, v117 src0_sel:BYTE_1
	v_fmac_f32_e32 v133, v66, v132
	v_cvt_f32_fp8_sdwa v132, v119 src0_sel:BYTE_1
	v_fmac_f32_e32 v133, v68, v80
	v_cvt_f32_fp8_sdwa v80, v121 src0_sel:BYTE_1
	v_mul_f32_e32 v149, 0x3f9837f0, v154
	v_fmac_f32_e32 v149, v64, v122
	v_cvt_f32_fp8_sdwa v122, v114 src0_sel:BYTE_1
	v_fmac_f32_e32 v149, v72, v131
	v_cvt_f32_fp8_sdwa v131, v116 src0_sel:BYTE_1
	v_lshlrev_b32_e32 v157, 16, v76
	v_and_b32_e32 v76, 0xffff0000, v76
	v_fmac_f32_e32 v149, v66, v132
	v_cvt_f32_fp8_sdwa v132, v118 src0_sel:BYTE_1
	v_fmac_f32_e32 v149, v68, v80
	v_cvt_f32_fp8_sdwa v80, v120 src0_sel:BYTE_1
	v_mul_f32_e32 v150, 0x3f9837f0, v76
	v_fmac_f32_e32 v150, v64, v122
	v_fmac_f32_e32 v150, v72, v131
	v_fmac_f32_e32 v150, v66, v132
	v_fmac_f32_e32 v150, v68, v80
	v_cvt_f32_fp8_e32 v80, v115
	v_cvt_f32_fp8_e32 v115, v117
	v_cvt_f32_fp8_e32 v117, v119
	v_cvt_f32_fp8_e32 v76, v121
	v_mul_f32_e32 v119, 0x3f9837f0, v153
	v_fmac_f32_e32 v119, v64, v80
	v_cvt_f32_fp8_e32 v80, v114
	v_fmac_f32_e32 v119, v72, v115
	v_cvt_f32_fp8_e32 v114, v116
	v_fmac_f32_e32 v119, v66, v117
	v_cvt_f32_fp8_e32 v115, v118
	v_fmac_f32_e32 v119, v68, v76
	v_cvt_f32_fp8_e32 v76, v120
	v_mul_f32_e32 v116, 0x3f9837f0, v157
	v_fmac_f32_e32 v116, v64, v80
	v_cvt_f32_fp8_sdwa v80, v105 src0_sel:BYTE_3
	v_fmac_f32_e32 v116, v72, v114
	v_cvt_f32_fp8_sdwa v114, v109 src0_sel:BYTE_3
	v_fmac_f32_e32 v116, v66, v115
	v_cvt_f32_fp8_sdwa v115, v111 src0_sel:BYTE_3
	v_fmac_f32_e32 v116, v68, v76
	v_cvt_f32_fp8_sdwa v76, v113 src0_sel:BYTE_3
	v_mul_f32_e32 v117, 0x3f9837f0, v163
	v_fmac_f32_e32 v117, v64, v80
	v_cvt_f32_fp8_sdwa v80, v104 src0_sel:BYTE_3
	v_fmac_f32_e32 v117, v72, v114
	v_cvt_f32_fp8_sdwa v114, v108 src0_sel:BYTE_3
	v_fmac_f32_e32 v117, v66, v115
	v_cvt_f32_fp8_sdwa v115, v110 src0_sel:BYTE_3
	v_fmac_f32_e32 v117, v68, v76
	v_cvt_f32_fp8_sdwa v76, v112 src0_sel:BYTE_3
	v_mul_f32_e32 v118, 0x3f9837f0, v167
	v_fmac_f32_e32 v118, v64, v80
	v_cvt_f32_fp8_sdwa v80, v105 src0_sel:BYTE_2
	v_fmac_f32_e32 v118, v72, v114
	v_cvt_f32_fp8_sdwa v114, v109 src0_sel:BYTE_2
	v_fmac_f32_e32 v118, v66, v115
	v_cvt_f32_fp8_sdwa v115, v111 src0_sel:BYTE_2
	v_fmac_f32_e32 v118, v68, v76
	v_cvt_f32_fp8_sdwa v76, v113 src0_sel:BYTE_2
	v_mul_f32_e32 v120, 0x3f9837f0, v162
	v_fmac_f32_e32 v120, v64, v80
	v_cvt_f32_fp8_sdwa v80, v104 src0_sel:BYTE_2
	v_fmac_f32_e32 v120, v72, v114
	v_cvt_f32_fp8_sdwa v114, v108 src0_sel:BYTE_2
	v_fmac_f32_e32 v120, v66, v115
	v_cvt_f32_fp8_sdwa v115, v110 src0_sel:BYTE_2
	v_fmac_f32_e32 v120, v68, v76
	v_cvt_f32_fp8_sdwa v76, v112 src0_sel:BYTE_2
	v_mul_f32_e32 v121, 0x3f9837f0, v166
	v_fmac_f32_e32 v121, v64, v80
	v_cvt_f32_fp8_sdwa v80, v105 src0_sel:BYTE_1
	v_fmac_f32_e32 v121, v72, v114
	v_cvt_f32_fp8_sdwa v114, v109 src0_sel:BYTE_1
	v_fmac_f32_e32 v121, v66, v115
	v_cvt_f32_fp8_sdwa v115, v111 src0_sel:BYTE_1
	v_fmac_f32_e32 v121, v68, v76
	v_cvt_f32_fp8_sdwa v76, v113 src0_sel:BYTE_1
	v_mul_f32_e32 v131, 0x3f9837f0, v161
	v_fmac_f32_e32 v131, v64, v80
	v_cvt_f32_fp8_sdwa v80, v104 src0_sel:BYTE_1
	v_fmac_f32_e32 v131, v72, v114
	v_cvt_f32_fp8_sdwa v114, v108 src0_sel:BYTE_1
	v_fmac_f32_e32 v131, v66, v115
	v_cvt_f32_fp8_sdwa v115, v110 src0_sel:BYTE_1
	v_fmac_f32_e32 v131, v68, v76
	v_cvt_f32_fp8_sdwa v76, v112 src0_sel:BYTE_1
	v_mul_f32_e32 v132, 0x3f9837f0, v165
	v_fmac_f32_e32 v132, v64, v80
	v_cvt_f32_fp8_e32 v80, v105
	v_fmac_f32_e32 v132, v72, v114
	v_cvt_f32_fp8_e32 v105, v109
	v_fmac_f32_e32 v132, v66, v115
	v_cvt_f32_fp8_e32 v109, v111
	v_fmac_f32_e32 v132, v68, v76
	v_cvt_f32_fp8_e32 v76, v113
	v_mul_f32_e32 v111, 0x3f9837f0, v160
	v_fmac_f32_e32 v111, v64, v80
	v_cvt_f32_fp8_e32 v80, v104
	v_fmac_f32_e32 v111, v72, v105
	v_cvt_f32_fp8_e32 v104, v108
	v_fmac_f32_e32 v111, v66, v109
	v_cvt_f32_fp8_e32 v105, v110
	v_fmac_f32_e32 v111, v68, v76
	v_cvt_f32_fp8_e32 v76, v112
	v_mul_f32_e32 v108, 0x3f9837f0, v164
	v_fmac_f32_e32 v108, v64, v80
	v_cvt_f32_fp8_sdwa v100, v100 src0_sel:BYTE_3
	v_fmac_f32_e32 v108, v72, v104
	v_fmac_f32_e32 v108, v66, v105
	v_cvt_f32_fp8_sdwa v81, v103 src0_sel:BYTE_2
	v_cvt_f32_fp8_sdwa v98, v103 src0_sel:BYTE_1
	v_cvt_f32_fp8_e32 v99, v103
	v_fmac_f32_e32 v108, v68, v76
	v_cvt_f32_fp8_sdwa v80, v103 src0_sel:BYTE_3
	v_mul_f32_e32 v103, 0x3f9837f0, v148
	v_fmac_f32_e32 v103, v64, v100
	v_add_f32_e32 v100, 0, v108
	v_add_f32_e32 v100, v132, v100
	v_add_f32_e32 v100, v121, v100
	v_add_f32_e32 v100, v118, v100
	v_add_f32_e32 v100, v111, v100
	v_add_f32_e32 v100, v131, v100
	v_add_f32_e32 v100, v120, v100
	v_add_f32_e32 v100, v117, v100
	v_add_f32_e32 v100, v116, v100
	v_add_f32_e32 v100, v150, v100
	v_add_f32_e32 v100, v133, v100
	v_add_f32_e32 v100, v129, v100
	v_add_f32_e32 v100, v119, v100
	v_add_f32_e32 v100, v149, v100
	v_add_f32_e32 v100, v130, v100
	v_add_f32_e32 v100, v128, v100
	v_add_f32_e32 v100, v126, v100
	v_add_f32_e32 v100, v147, v100
	v_add_f32_e32 v100, v145, v100
	v_add_f32_e32 v100, v134, v100
	v_cvt_f32_fp8_sdwa v123, v101 src0_sel:BYTE_2
	v_cvt_f32_fp8_sdwa v124, v101 src0_sel:BYTE_1
	v_cvt_f32_fp8_e32 v125, v101
	v_cvt_f32_fp8_sdwa v122, v101 src0_sel:BYTE_3
	v_cvt_f32_fp8_sdwa v101, v102 src0_sel:BYTE_3
	v_add_f32_e32 v100, v127, v100
	v_cvt_f32_fp8_sdwa v102, v106 src0_sel:BYTE_3
	v_add_f32_e32 v100, v146, v100
	v_add_f32_e32 v100, v135, v100
	v_add_f32_e32 v100, v73, v100
	v_fmac_f32_e32 v103, v72, v101
	v_add_f32_e32 v100, v69, v100
	v_fmac_f32_e32 v103, v66, v102
	v_add_f32_e32 v100, v67, v100
	v_fmac_f32_e32 v103, v68, v168
	v_add_f32_e32 v100, v65, v100
	v_cvt_f32_fp8_sdwa v77, v107 src0_sel:BYTE_2
	v_cvt_f32_fp8_sdwa v76, v107 src0_sel:BYTE_3
	v_add_f32_e32 v102, v103, v100
	v_and_b32_e32 v100, 0xffff0000, v71
	v_lshlrev_b32_e32 v101, 16, v71
	v_pk_mul_f32 v[100:101], v[100:101], s[18:19] op_sel_hi:[1,0]
	v_cvt_f32_fp8_sdwa v82, v107 src0_sel:BYTE_1
	v_pk_fma_f32 v[100:101], v[64:65], v[122:123], v[100:101] op_sel_hi:[0,1,1]
	v_pk_fma_f32 v[80:81], v[72:73], v[80:81], v[100:101] op_sel_hi:[0,1,1]
	v_pk_fma_f32 v[76:77], v[66:67], v[76:77], v[80:81] op_sel_hi:[0,1,1]
	v_cvt_f32_fp8_e32 v83, v107
	v_pk_fma_f32 v[74:75], v[68:69], v[74:75], v[76:77] op_sel_hi:[0,1,1]
	v_and_b32_e32 v76, 0xffff0000, v70
	v_lshlrev_b32_e32 v77, 16, v70
	v_pk_mul_f32 v[70:71], v[76:77], s[18:19] op_sel_hi:[1,0]
	s_ashr_i32 s21, s20, 31
	v_pk_fma_f32 v[70:71], v[64:65], v[124:125], v[70:71] op_sel_hi:[0,1,1]
	v_pk_fma_f32 v[70:71], v[72:73], v[98:99], v[70:71] op_sel_hi:[0,1,1]
	v_pk_fma_f32 v[70:71], v[66:67], v[82:83], v[70:71] op_sel_hi:[0,1,1]
	v_pk_fma_f32 v[70:71], v[68:69], v[78:79], v[70:71] op_sel_hi:[0,1,1]
	v_add_f32_e32 v64, v71, v102
	v_add_f32_e32 v64, v70, v64
	v_add_f32_e32 v64, v75, v64
	v_add_f32_e32 v64, v74, v64
	s_lshl_b64 s[22:23], s[20:21], 11
	s_lshl_b64 s[20:21], s[20:21], 12
	s_waitcnt lgkmcnt(0)
	s_nop 1
	v_add_f32_dpp v64, v64, v64 quad_perm:[1,0,3,2] row_mask:0xf bank_mask:0xf
	s_waitcnt lgkmcnt(0)
	s_nop 1
	v_add_f32_dpp v64, v64, v64 quad_perm:[2,3,0,1] row_mask:0xf bank_mask:0xf
	s_waitcnt lgkmcnt(0)
	s_nop 1
	v_add_f32_dpp v64, v64, v64 row_half_mirror row_mask:0xf bank_mask:0xf
	s_waitcnt lgkmcnt(0)
	s_nop 1
	v_add_f32_dpp v64, v64, v64 row_mirror row_mask:0xf bank_mask:0xf
	s_waitcnt lgkmcnt(0)
	v_mov_b32_e32 v66, v64
	s_nop 1
	v_permlane16_swap_b32_e32 v64, v66
	v_add_f32_e32 v64, v64, v66
	s_waitcnt lgkmcnt(0)
	v_mov_b32_e32 v66, v64
	s_nop 1
	v_permlane32_swap_b32_e32 v64, v66
	v_add_f32_e32 v66, v64, v66
	v_fmac_f32_e32 v132, 0xba000000, v66
	v_fmac_f32_e32 v108, 0xba000000, v66
	v_mul_f32_e32 v68, v132, v132
	v_fmac_f32_e32 v68, v108, v108
	v_fmac_f32_e32 v121, 0xba000000, v66
	v_fmac_f32_e32 v68, v121, v121
	v_fmac_f32_e32 v118, 0xba000000, v66
	v_fmac_f32_e32 v68, v118, v118
	v_fmac_f32_e32 v111, 0xba000000, v66
	v_fmac_f32_e32 v68, v111, v111
	v_fmac_f32_e32 v131, 0xba000000, v66
	v_fmac_f32_e32 v68, v131, v131
	v_fmac_f32_e32 v120, 0xba000000, v66
	v_fmac_f32_e32 v68, v120, v120
	v_fmac_f32_e32 v117, 0xba000000, v66
	v_fmac_f32_e32 v68, v117, v117
	v_fmac_f32_e32 v116, 0xba000000, v66
	v_fmac_f32_e32 v68, v116, v116
	v_fmac_f32_e32 v150, 0xba000000, v66
	v_fmac_f32_e32 v68, v150, v150
	v_fmac_f32_e32 v133, 0xba000000, v66
	v_fmac_f32_e32 v68, v133, v133
	v_fmac_f32_e32 v129, 0xba000000, v66
	v_fmac_f32_e32 v68, v129, v129
	v_fmac_f32_e32 v119, 0xba000000, v66
	v_fmac_f32_e32 v68, v119, v119
	v_fmac_f32_e32 v149, 0xba000000, v66
	v_fmac_f32_e32 v68, v149, v149
	v_fmac_f32_e32 v130, 0xba000000, v66
	v_fmac_f32_e32 v68, v130, v130
	v_fmac_f32_e32 v128, 0xba000000, v66
	v_fmac_f32_e32 v68, v128, v128
	v_fmac_f32_e32 v126, 0xba000000, v66
	v_fmac_f32_e32 v68, v126, v126
	v_fmac_f32_e32 v147, 0xba000000, v66
	v_fmac_f32_e32 v68, v147, v147
	v_fmac_f32_e32 v145, 0xba000000, v66
	v_fmac_f32_e32 v68, v145, v145
	v_fmac_f32_e32 v134, 0xba000000, v66
	v_fmac_f32_e32 v68, v134, v134
	v_fmac_f32_e32 v127, 0xba000000, v66
	v_fmac_f32_e32 v68, v127, v127
	v_fmac_f32_e32 v146, 0xba000000, v66
	v_fmac_f32_e32 v68, v146, v146
	v_fmac_f32_e32 v135, 0xba000000, v66
	v_fmac_f32_e32 v68, v135, v135
	v_fmac_f32_e32 v73, 0xba000000, v66
	v_fmac_f32_e32 v68, v73, v73
	v_fmac_f32_e32 v69, 0xba000000, v66
	v_fmac_f32_e32 v68, v69, v69
	v_fmac_f32_e32 v67, 0xba000000, v66
	v_mul_f32_e32 v64, 0x3a000000, v66
	v_fmac_f32_e32 v68, v67, v67
	v_fmac_f32_e32 v65, 0xba000000, v66
	v_fmac_f32_e32 v68, v65, v65
	v_fmac_f32_e32 v103, 0xba000000, v66
	v_pk_add_f32 v[78:79], v[70:71], v[64:65] op_sel_hi:[1,0] neg_lo:[0,1] neg_hi:[0,1]
	v_fmac_f32_e32 v68, v103, v103
	v_pk_mul_f32 v[70:71], v[78:79], v[78:79]
	v_pk_add_f32 v[80:81], v[74:75], v[64:65] op_sel_hi:[1,0] neg_lo:[0,1] neg_hi:[0,1]
	v_add_f32_e32 v66, v71, v68
	v_add_f32_e32 v66, v70, v66
	v_pk_mul_f32 v[70:71], v[80:81], v[80:81]
	s_nop 0
	v_add_f32_e32 v64, v71, v66
	v_add_f32_e32 v64, v70, v64
	s_waitcnt lgkmcnt(0)
	s_nop 1
	v_add_f32_dpp v64, v64, v64 quad_perm:[1,0,3,2] row_mask:0xf bank_mask:0xf
	s_waitcnt lgkmcnt(0)
	s_nop 1
	v_add_f32_dpp v64, v64, v64 quad_perm:[2,3,0,1] row_mask:0xf bank_mask:0xf
	s_waitcnt lgkmcnt(0)
	s_nop 1
	v_add_f32_dpp v64, v64, v64 row_half_mirror row_mask:0xf bank_mask:0xf
	s_waitcnt lgkmcnt(0)
	s_nop 1
	v_add_f32_dpp v64, v64, v64 row_mirror row_mask:0xf bank_mask:0xf
	s_waitcnt lgkmcnt(0)
	v_mov_b32_e32 v66, v64
	s_nop 1
	v_permlane16_swap_b32_e32 v64, v66
	v_add_f32_e32 v64, v64, v66
	s_waitcnt lgkmcnt(0)
	v_mov_b32_e32 v66, v64
	s_nop 1
	v_permlane32_swap_b32_e32 v64, v66
	v_add_f32_e32 v64, v64, v66
	v_fmamk_f32 v64, v64, 0x3a000000, v139
	v_mul_f32_e32 v66, 0x4b800000, v64
	v_cmp_gt_f32_e32 vcc, s29, v64
	s_nop 1
	v_cndmask_b32_e32 v64, v64, v66, vcc
	v_rsq_f32_e32 v64, v64
	s_nop 0
	v_mul_f32_e32 v66, 0x45800000, v64
	v_cndmask_b32_e32 v64, v64, v66, vcc
	v_mul_f32_e32 v70, v132, v64
	v_fma_f32 v71, v57, v70, v49
	v_mul_f32_e32 v70, v131, v64
	v_fma_f32 v72, v61, v70, v53
	v_mul_f32_e32 v70, v121, v64
	v_fma_f32 v82, v58, v70, v50
	v_mul_f32_e32 v70, v120, v64
	v_fma_f32 v83, v62, v70, v54
	v_mul_f32_e32 v70, v118, v64
	v_mul_f32_e32 v66, v108, v64
	v_fma_f32 v98, v59, v70, v51
	v_mul_f32_e32 v70, v117, v64
	v_fma_f32 v66, v56, v66, v48
	v_mul_f32_e32 v68, v111, v64
	v_fma_f32 v99, v63, v70, v55
	v_mov_b32_e32 v70, 0
	v_fma_f32 v68, v60, v68, v52
	v_cvt_pk_bf16_f32 v74, v66, v71
	v_cvt_pk_fp8_f32 v70, v66, v71
	v_mov_b32_e32 v71, 0
	v_cvt_pk_fp8_f32 v71, v68, v72
	v_cvt_pk_bf16_f32 v75, v82, v98
	v_cvt_pk_fp8_f32 v70, v82, v98 op_sel:[0,0,1]
	v_cvt_pk_bf16_f32 v76, v68, v72
	v_cvt_pk_fp8_f32 v71, v83, v99 op_sel:[0,0,1]
	v_cvt_pk_bf16_f32 v77, v83, v99
	v_lshl_add_u64 v[82:83], v[88:89], 0, s[20:21]
	v_lshl_add_u64 v[98:99], v[90:91], 0, s[22:23]
	global_store_dwordx4 v[82:83], v[74:77], off
	global_store_dwordx2 v[98:99], v[70:71], off
	v_mul_f32_e32 v70, v150, v64
	v_fma_f32 v72, v41, v70, v33
	v_mul_f32_e32 v70, v149, v64
	v_fma_f32 v76, v45, v70, v37
	v_mul_f32_e32 v70, v133, v64
	v_fma_f32 v77, v42, v70, v34
	v_mul_f32_e32 v70, v130, v64
	v_fma_f32 v100, v46, v70, v38
	v_mul_f32_e32 v70, v129, v64
	v_mul_f32_e32 v66, v116, v64
	v_mul_f32_e32 v68, v119, v64
	v_fma_f32 v101, v43, v70, v35
	v_mul_f32_e32 v70, v128, v64
	v_fma_f32 v66, v40, v66, v32
	v_fma_f32 v68, v44, v68, v36
	v_fma_f32 v102, v47, v70, v39
	v_mov_b32_e32 v70, 0
	v_mov_b32_e32 v71, 0
	v_cvt_pk_fp8_f32 v70, v66, v72
	v_cvt_pk_fp8_f32 v71, v68, v76
	v_cvt_pk_bf16_f32 v74, v66, v72
	v_cvt_pk_bf16_f32 v75, v77, v101
	v_cvt_pk_fp8_f32 v70, v77, v101 op_sel:[0,0,1]
	v_cvt_pk_fp8_f32 v71, v100, v102 op_sel:[0,0,1]
	v_cvt_pk_bf16_f32 v76, v68, v76
	v_cvt_pk_bf16_f32 v77, v100, v102
	global_store_dwordx4 v[82:83], v[74:77], off offset:1024
	global_store_dwordx2 v[98:99], v[70:71], off offset:512
	v_mul_f32_e32 v66, v126, v64
	v_mul_f32_e32 v68, v127, v64
	v_mul_f32_e32 v70, v147, v64
	v_mul_f32_e32 v71, v146, v64
	v_fma_f32 v66, v24, v66, v16
	v_fma_f32 v68, v28, v68, v20
	v_fma_f32 v70, v25, v70, v17
	v_fma_f32 v72, v29, v71, v21
	v_mul_f32_e32 v71, v145, v64
	v_mov_b32_e32 v74, 0
	v_mov_b32_e32 v75, 0
	v_fma_f32 v76, v26, v71, v18
	v_mul_f32_e32 v71, v135, v64
	v_cvt_pk_fp8_f32 v74, v66, v70
	v_cvt_pk_fp8_f32 v75, v68, v72
	v_fma_f32 v77, v30, v71, v22
	v_mul_f32_e32 v71, v134, v64
	v_fma_f32 v100, v27, v71, v19
	v_mul_f32_e32 v71, v73, v64
	v_fma_f32 v73, v31, v71, v23
	v_cvt_pk_fp8_f32 v74, v76, v100 op_sel:[0,0,1]
	v_cvt_pk_fp8_f32 v75, v77, v73 op_sel:[0,0,1]
	v_cvt_pk_bf16_f32 v70, v66, v70
	v_cvt_pk_bf16_f32 v71, v76, v100
	v_cvt_pk_bf16_f32 v72, v68, v72
	v_cvt_pk_bf16_f32 v73, v77, v73
	v_mul_f32_e32 v68, v79, v64
	global_store_dwordx4 v[82:83], v[70:73], off offset:2048
	global_store_dwordx2 v[98:99], v[74:75], off offset:1024
	v_mul_f32_e32 v66, v69, v64
	v_fma_f32 v70, v12, v68, v4
	v_mul_f32_e32 v67, v67, v64
	v_mul_f32_e32 v68, v78, v64
	v_fma_f32 v66, v8, v66, v0
	v_fma_f32 v67, v9, v67, v1
	v_fma_f32 v71, v13, v68, v5
	v_mov_b32_e32 v68, 0
	v_mov_b32_e32 v69, 0
	v_mul_f32_e32 v65, v65, v64
	v_cvt_pk_fp8_f32 v68, v66, v67
	v_cvt_pk_fp8_f32 v69, v70, v71
	v_fma_f32 v72, v10, v65, v2
	v_mul_f32_e32 v65, v81, v64
	v_fma_f32 v73, v14, v65, v6
	v_mul_f32_e32 v65, v103, v64
	v_mul_f32_e32 v64, v80, v64
	v_fma_f32 v74, v11, v65, v3
	v_fma_f32 v75, v15, v64, v7
	v_cvt_pk_fp8_f32 v68, v72, v74 op_sel:[0,0,1]
	v_cvt_pk_fp8_f32 v69, v73, v75 op_sel:[0,0,1]
	v_cvt_pk_bf16_f32 v64, v66, v67
	v_cvt_pk_bf16_f32 v65, v72, v74
	v_cvt_pk_bf16_f32 v66, v70, v71
	v_cvt_pk_bf16_f32 v67, v73, v75
	global_store_dwordx4 v[82:83], v[64:67], off offset:3072
	global_store_dwordx2 v[98:99], v[68:69], off offset:1536
	s_branch .LBB0_1262

.LBB0_1347:
	s_add_u32 s8, s90, 0x1d100000
	s_addc_u32 s9, s91, 0
	s_add_u32 s10, s90, 0x6100000
	s_addc_u32 s11, s91, 0
	s_lshl_b32 s0, s5, 5
	s_waitcnt vmcnt(0)
	s_barrier
	v_mbcnt_lo_u32_b32 v197, -1, 0
	v_mbcnt_hi_u32_b32 v197, -1, v197
	s_lshl_b32 s14, s4, 8
	s_lshl_b32 s2, s6, 8
	v_ashrrev_i32_e32 v128, 2, v197
	v_and_b32_e32 v196, 15, v197
	s_add_i32 s1, s14, s38
	s_or_b32 s0, s2, s0
	v_and_b32_e32 v128, -4, v128
	v_add_u32_e32 v144, s0, v128
	v_or_b32_e32 v128, s1, v196
	v_ashrrev_i32_e32 v129, 31, v128
	v_readlane_b32 s16, v255, 5
	v_ashrrev_i32_e32 v145, 31, v144
	v_lshlrev_b64 v[130:131], 11, v[128:129]
	v_readlane_b32 s24, v255, 13
	v_readlane_b32 s25, v255, 14
	v_lshl_add_u64 v[130:131], v[130:131], 0, v[144:145]
	s_mov_b64 s[12:13], s[24:25]
	v_lshlrev_b64 v[146:147], 1, v[130:131]
	v_mov_b32_e32 v130, s12
	v_mov_b32_e32 v131, s13
	v_lshl_add_u64 v[130:131], v[144:145], 2, v[130:131]
	global_load_dwordx4 v[140:143], v[130:131], off
	v_lshl_add_u64 v[148:149], s[8:9], 0, v[146:147]
	v_lshl_add_u64 v[150:151], s[10:11], 0, v[146:147]
	global_load_dwordx2 v[198:199], v[148:149], off
	global_load_dwordx2 v[200:201], v[150:151], off
	v_or_b32_e32 v152, 16, v128
	v_or_b32_e32 v154, 32, v128
	v_or_b32_e32 v156, 48, v128
	global_load_dwordx4 v[136:139], v[130:131], off offset:64
	global_load_dwordx2 v[202:203], v[148:149], off offset:32
	global_load_dwordx4 v[132:135], v[130:131], off offset:512
	s_nop 0
	global_load_dwordx4 v[128:131], v[130:131], off offset:576
	v_ashrrev_i32_e32 v153, 31, v152
	global_load_dwordx2 v[204:205], v[150:151], off offset:32
	global_load_dwordx2 v[206:207], v[148:149], off offset:256
	global_load_dwordx2 v[208:209], v[148:149], off offset:288
	global_load_dwordx2 v[210:211], v[150:151], off offset:256
	global_load_dwordx2 v[212:213], v[150:151], off offset:288
	v_ashrrev_i32_e32 v155, 31, v154
	v_ashrrev_i32_e32 v157, 31, v156
	v_lshlrev_b64 v[152:153], 11, v[152:153]
	v_lshlrev_b64 v[154:155], 11, v[154:155]
	v_lshlrev_b64 v[156:157], 11, v[156:157]
	v_lshl_add_u64 v[152:153], v[152:153], 0, v[144:145]
	v_lshl_add_u64 v[154:155], v[154:155], 0, v[144:145]
	v_lshl_add_u64 v[156:157], v[156:157], 0, v[144:145]
	v_lshlrev_b64 v[152:153], 1, v[152:153]
	v_lshlrev_b64 v[154:155], 1, v[154:155]
	v_lshlrev_b64 v[156:157], 1, v[156:157]
	v_lshl_add_u64 v[148:149], s[8:9], 0, v[152:153]
	v_lshl_add_u64 v[150:151], s[10:11], 0, v[152:153]
	v_lshl_add_u64 v[152:153], s[8:9], 0, v[154:155]
	v_lshl_add_u64 v[154:155], s[10:11], 0, v[154:155]
	v_lshl_add_u64 v[160:161], s[8:9], 0, v[156:157]
	v_lshl_add_u64 v[214:215], s[10:11], 0, v[156:157]
	global_load_dwordx2 v[194:195], v[148:149], off
	global_load_dwordx2 v[190:191], v[148:149], off offset:32
	global_load_dwordx2 v[186:187], v[148:149], off offset:256
	global_load_dwordx2 v[182:183], v[148:149], off offset:288
	global_load_dwordx2 v[192:193], v[150:151], off
	global_load_dwordx2 v[188:189], v[150:151], off offset:32
	global_load_dwordx2 v[184:185], v[150:151], off offset:256
	global_load_dwordx2 v[180:181], v[150:151], off offset:288
	global_load_dwordx2 v[178:179], v[152:153], off
	global_load_dwordx2 v[174:175], v[152:153], off offset:32
	global_load_dwordx2 v[170:171], v[152:153], off offset:256
	global_load_dwordx2 v[166:167], v[152:153], off offset:288
	global_load_dwordx2 v[176:177], v[154:155], off
	global_load_dwordx2 v[172:173], v[154:155], off offset:32
	global_load_dwordx2 v[168:169], v[154:155], off offset:256
	global_load_dwordx2 v[164:165], v[154:155], off offset:288
	global_load_dwordx2 v[162:163], v[160:161], off
	global_load_dwordx2 v[158:159], v[160:161], off offset:32
	s_nop 0
	global_load_dwordx2 v[154:155], v[160:161], off offset:256
	global_load_dwordx2 v[150:151], v[160:161], off offset:288
	s_nop 0
	global_load_dwordx2 v[160:161], v[214:215], off
	global_load_dwordx2 v[156:157], v[214:215], off offset:32
	global_load_dwordx2 v[152:153], v[214:215], off offset:256
	global_load_dwordx2 v[148:149], v[214:215], off offset:288
	s_mov_b32 s0, 0x3b000000
	s_mov_b32 s2, 0x3f9837f0
	s_mov_b64 s[12:13], 0x80000
	v_readlane_b32 s17, v255, 6
	v_readlane_b32 s18, v255, 7
	v_readlane_b32 s19, v255, 8
	v_readlane_b32 s20, v255, 9
	v_readlane_b32 s21, v255, 10
	v_readlane_b32 s22, v255, 11
	v_readlane_b32 s23, v255, 12
	v_readlane_b32 s26, v255, 15
	v_readlane_b32 s27, v255, 16
	v_readlane_b32 s28, v255, 17
	v_readlane_b32 s29, v255, 18
	v_readlane_b32 s30, v255, 19
	v_readlane_b32 s31, v255, 20
	s_waitcnt vmcnt(35)
	v_pk_fma_f32 v[66:67], v[66:67], s[0:1], v[142:143] op_sel_hi:[1,0,1]
	s_nop 0
	v_mul_f32_e32 v66, 0xbfb8aa3b, v66
	v_mul_f32_e32 v67, 0xbfb8aa3b, v67
	v_exp_f32_e32 v66, v66
	v_exp_f32_e32 v67, v67
	s_waitcnt vmcnt(32)
	v_pk_fma_f32 v[74:75], v[74:75], s[0:1], v[138:139] op_sel_hi:[1,0,1]
	v_pk_fma_f32 v[72:73], v[72:73], s[0:1], v[136:137] op_sel_hi:[1,0,1]
	v_mul_f32_e32 v74, 0xbfb8aa3b, v74
	v_mul_f32_e32 v75, 0xbfb8aa3b, v75
	s_waitcnt vmcnt(30)
	v_pk_fma_f32 v[82:83], v[82:83], s[0:1], v[134:135] op_sel_hi:[1,0,1]
	v_mul_f32_e32 v72, 0xbfb8aa3b, v72
	v_mul_f32_e32 v73, 0xbfb8aa3b, v73
	v_exp_f32_e32 v74, v74
	v_exp_f32_e32 v75, v75
	v_pk_fma_f32 v[80:81], v[80:81], s[0:1], v[132:133] op_sel_hi:[1,0,1]
	v_mul_f32_e32 v82, 0xbfb8aa3b, v82
	v_mul_f32_e32 v83, 0xbfb8aa3b, v83
	s_waitcnt vmcnt(29)
	v_pk_fma_f32 v[86:87], v[86:87], s[0:1], v[130:131] op_sel_hi:[1,0,1]
	v_exp_f32_e32 v72, v72
	v_exp_f32_e32 v73, v73
	v_mul_f32_e32 v80, 0xbfb8aa3b, v80
	v_mul_f32_e32 v81, 0xbfb8aa3b, v81
	v_exp_f32_e32 v82, v82
	v_exp_f32_e32 v83, v83
	v_pk_fma_f32 v[84:85], v[84:85], s[0:1], v[128:129] op_sel_hi:[1,0,1]
	v_mul_f32_e32 v86, 0xbfb8aa3b, v86
	v_mul_f32_e32 v87, 0xbfb8aa3b, v87
	v_add_f32_e32 v66, 1.0, v66
	v_add_f32_e32 v67, 1.0, v67
	v_exp_f32_e32 v80, v80
	v_exp_f32_e32 v81, v81
	v_mul_f32_e32 v84, 0xbfb8aa3b, v84
	v_mul_f32_e32 v85, 0xbfb8aa3b, v85
	v_exp_f32_e32 v86, v86
	v_exp_f32_e32 v87, v87
	v_pk_fma_f32 v[90:91], v[90:91], s[0:1], v[142:143] op_sel_hi:[1,0,1]
	v_rcp_f32_e32 v66, v66
	v_rcp_f32_e32 v67, v67
	v_exp_f32_e32 v84, v84
	v_exp_f32_e32 v85, v85
	v_mul_f32_e32 v90, 0xbfb8aa3b, v90
	v_mul_f32_e32 v91, 0xbfb8aa3b, v91
	v_add_f32_e32 v74, 1.0, v74
	v_add_f32_e32 v75, 1.0, v75
	v_exp_f32_e32 v90, v90
	v_exp_f32_e32 v91, v91
	v_pk_fma_f32 v[98:99], v[98:99], s[0:1], v[138:139] op_sel_hi:[1,0,1]
	v_add_f32_e32 v72, 1.0, v72
	v_add_f32_e32 v73, 1.0, v73
	v_rcp_f32_e32 v74, v74
	v_rcp_f32_e32 v75, v75
	v_add_f32_e32 v82, 1.0, v82
	v_add_f32_e32 v83, 1.0, v83
	v_mul_f32_e32 v98, 0xbfb8aa3b, v98
	v_mul_f32_e32 v99, 0xbfb8aa3b, v99
	v_lshlrev_b32_e32 v216, 16, v200
	v_and_b32_e32 v217, 0xffff0000, v200
	v_lshlrev_b32_e32 v200, 16, v201
	v_and_b32_e32 v201, 0xffff0000, v201
	v_rcp_f32_e32 v72, v72
	v_rcp_f32_e32 v73, v73
	v_add_f32_e32 v80, 1.0, v80
	v_add_f32_e32 v81, 1.0, v81
	v_rcp_f32_e32 v82, v82
	v_rcp_f32_e32 v83, v83
	v_add_f32_e32 v86, 1.0, v86
	v_add_f32_e32 v87, 1.0, v87
	v_exp_f32_e32 v98, v98
	v_exp_f32_e32 v99, v99
	v_pk_fma_f32 v[110:111], v[110:111], s[0:1], v[134:135] op_sel_hi:[1,0,1]
	v_lshlrev_b32_e32 v214, 16, v198
	v_and_b32_e32 v215, 0xffff0000, v198
	v_lshlrev_b32_e32 v198, 16, v199
	v_and_b32_e32 v199, 0xffff0000, v199
	v_pk_mul_f32 v[66:67], v[66:67], v[200:201]
	v_rcp_f32_e32 v80, v80
	v_rcp_f32_e32 v81, v81
	v_add_f32_e32 v84, 1.0, v84
	v_add_f32_e32 v85, 1.0, v85
	v_rcp_f32_e32 v86, v86
	v_rcp_f32_e32 v87, v87
	v_mul_f32_e32 v110, 0xbfb8aa3b, v110
	v_mul_f32_e32 v111, 0xbfb8aa3b, v111
	v_pk_fma_f32 v[66:67], v[198:199], s[2:3], v[66:67] op_sel_hi:[1,0,1]
	v_lshlrev_b32_e32 v198, 16, v202
	v_and_b32_e32 v199, 0xffff0000, v202
	v_lshlrev_b32_e32 v200, 16, v203
	v_and_b32_e32 v201, 0xffff0000, v203
	s_waitcnt vmcnt(28)
	v_lshlrev_b32_e32 v202, 16, v204
	v_and_b32_e32 v203, 0xffff0000, v204
	v_lshlrev_b32_e32 v204, 16, v205
	v_and_b32_e32 v205, 0xffff0000, v205
	v_rcp_f32_e32 v84, v84
	v_rcp_f32_e32 v85, v85
	v_add_f32_e32 v90, 1.0, v90
	v_add_f32_e32 v91, 1.0, v91
	v_exp_f32_e32 v110, v110
	v_exp_f32_e32 v111, v111
	v_pk_fma_f32 v[114:115], v[114:115], s[0:1], v[130:131] op_sel_hi:[1,0,1]
	v_pk_mul_f32 v[74:75], v[74:75], v[204:205]
	s_waitcnt vmcnt(25)
	v_lshlrev_b32_e32 v204, 16, v211
	v_and_b32_e32 v205, 0xffff0000, v211
	v_rcp_f32_e32 v90, v90
	v_rcp_f32_e32 v91, v91
	v_mul_f32_e32 v114, 0xbfb8aa3b, v114
	v_mul_f32_e32 v115, 0xbfb8aa3b, v115
	v_pk_mul_f32 v[72:73], v[72:73], v[202:203]
	v_pk_fma_f32 v[74:75], v[200:201], s[2:3], v[74:75] op_sel_hi:[1,0,1]
	v_lshlrev_b32_e32 v200, 16, v207
	v_and_b32_e32 v201, 0xffff0000, v207
	v_lshlrev_b32_e32 v202, 16, v210
	v_and_b32_e32 v203, 0xffff0000, v210
	v_pk_mul_f32 v[82:83], v[82:83], v[204:205]
	s_waitcnt vmcnt(24)
	v_lshlrev_b32_e32 v204, 16, v213
	v_and_b32_e32 v205, 0xffff0000, v213
	v_add_f32_e32 v98, 1.0, v98
	v_add_f32_e32 v99, 1.0, v99
	v_exp_f32_e32 v114, v114
	v_exp_f32_e32 v115, v115
	v_pk_fma_f32 v[122:123], v[122:123], s[0:1], v[142:143] op_sel_hi:[1,0,1]
	v_pk_fma_f32 v[72:73], v[198:199], s[2:3], v[72:73] op_sel_hi:[1,0,1]
	v_lshlrev_b32_e32 v198, 16, v206
	v_and_b32_e32 v199, 0xffff0000, v206
	v_pk_mul_f32 v[80:81], v[80:81], v[202:203]
	v_pk_fma_f32 v[82:83], v[200:201], s[2:3], v[82:83] op_sel_hi:[1,0,1]
	v_lshlrev_b32_e32 v200, 16, v209
	v_and_b32_e32 v201, 0xffff0000, v209
	v_lshlrev_b32_e32 v202, 16, v212
	v_and_b32_e32 v203, 0xffff0000, v212
	v_pk_mul_f32 v[86:87], v[86:87], v[204:205]
	v_rcp_f32_e32 v98, v98
	v_rcp_f32_e32 v99, v99
	v_mul_f32_e32 v122, 0xbfb8aa3b, v122
	v_mul_f32_e32 v123, 0xbfb8aa3b, v123
	v_pk_fma_f32 v[80:81], v[198:199], s[2:3], v[80:81] op_sel_hi:[1,0,1]
	v_lshlrev_b32_e32 v198, 16, v208
	v_and_b32_e32 v199, 0xffff0000, v208
	v_pk_mul_f32 v[84:85], v[84:85], v[202:203]
	v_pk_fma_f32 v[86:87], v[200:201], s[2:3], v[86:87] op_sel_hi:[1,0,1]
	s_waitcnt vmcnt(19)
	v_lshlrev_b32_e32 v200, 16, v192
	v_and_b32_e32 v201, 0xffff0000, v192
	v_lshlrev_b32_e32 v192, 16, v193
	v_and_b32_e32 v193, 0xffff0000, v193
	v_add_f32_e32 v110, 1.0, v110
	v_add_f32_e32 v111, 1.0, v111
	v_exp_f32_e32 v122, v122
	v_exp_f32_e32 v123, v123
	v_pk_fma_f32 v[126:127], v[126:127], s[0:1], v[138:139] op_sel_hi:[1,0,1]
	v_pk_fma_f32 v[84:85], v[198:199], s[2:3], v[84:85] op_sel_hi:[1,0,1]
	v_lshlrev_b32_e32 v198, 16, v194
	v_and_b32_e32 v199, 0xffff0000, v194
	v_lshlrev_b32_e32 v194, 16, v195
	v_and_b32_e32 v195, 0xffff0000, v195
	v_pk_mul_f32 v[90:91], v[90:91], v[192:193]
	v_rcp_f32_e32 v110, v110
	v_rcp_f32_e32 v111, v111
	v_mul_f32_e32 v126, 0xbfb8aa3b, v126
	v_mul_f32_e32 v127, 0xbfb8aa3b, v127
	v_pk_fma_f32 v[90:91], v[194:195], s[2:3], v[90:91] op_sel_hi:[1,0,1]
	s_waitcnt vmcnt(18)
	v_lshlrev_b32_e32 v194, 16, v188
	v_and_b32_e32 v195, 0xffff0000, v188
	v_lshlrev_b32_e32 v188, 16, v189
	v_and_b32_e32 v189, 0xffff0000, v189
	v_add_f32_e32 v114, 1.0, v114
	v_add_f32_e32 v115, 1.0, v115
	v_exp_f32_e32 v126, v126
	v_exp_f32_e32 v127, v127
	v_pk_fma_f32 v[118:119], v[118:119], s[0:1], v[134:135] op_sel_hi:[1,0,1]
	v_lshlrev_b32_e32 v192, 16, v190
	v_and_b32_e32 v193, 0xffff0000, v190
	v_lshlrev_b32_e32 v190, 16, v191
	v_and_b32_e32 v191, 0xffff0000, v191
	v_pk_mul_f32 v[98:99], v[98:99], v[188:189]
	v_rcp_f32_e32 v114, v114
	v_rcp_f32_e32 v115, v115
	v_mul_f32_e32 v118, 0xbfb8aa3b, v118
	v_mul_f32_e32 v119, 0xbfb8aa3b, v119
	v_pk_fma_f32 v[98:99], v[190:191], s[2:3], v[98:99] op_sel_hi:[1,0,1]
	s_waitcnt vmcnt(17)
	v_lshlrev_b32_e32 v190, 16, v184
	v_and_b32_e32 v191, 0xffff0000, v184
	v_lshlrev_b32_e32 v184, 16, v185
	v_and_b32_e32 v185, 0xffff0000, v185
	v_add_f32_e32 v122, 1.0, v122
	v_add_f32_e32 v123, 1.0, v123
	v_exp_f32_e32 v118, v118
	v_exp_f32_e32 v119, v119
	v_pk_fma_f32 v[106:107], v[106:107], s[0:1], v[130:131] op_sel_hi:[1,0,1]
	v_lshlrev_b32_e32 v188, 16, v186
	v_and_b32_e32 v189, 0xffff0000, v186
	v_lshlrev_b32_e32 v186, 16, v187
	v_and_b32_e32 v187, 0xffff0000, v187
	v_pk_mul_f32 v[110:111], v[110:111], v[184:185]
	v_rcp_f32_e32 v122, v122
	v_rcp_f32_e32 v123, v123
	v_mul_f32_e32 v106, 0xbfb8aa3b, v106
	v_mul_f32_e32 v107, 0xbfb8aa3b, v107
	v_pk_fma_f32 v[110:111], v[186:187], s[2:3], v[110:111] op_sel_hi:[1,0,1]
	s_waitcnt vmcnt(16)
	v_lshlrev_b32_e32 v186, 16, v180
	v_and_b32_e32 v187, 0xffff0000, v180
	v_lshlrev_b32_e32 v180, 16, v181
	v_and_b32_e32 v181, 0xffff0000, v181
	v_add_f32_e32 v126, 1.0, v126
	v_add_f32_e32 v127, 1.0, v127
	v_exp_f32_e32 v106, v106
	v_exp_f32_e32 v107, v107
	v_pk_fma_f32 v[102:103], v[102:103], s[0:1], v[142:143] op_sel_hi:[1,0,1]
	v_lshlrev_b32_e32 v184, 16, v182
	v_and_b32_e32 v185, 0xffff0000, v182
	v_lshlrev_b32_e32 v182, 16, v183
	v_and_b32_e32 v183, 0xffff0000, v183
	v_pk_mul_f32 v[114:115], v[114:115], v[180:181]
	v_rcp_f32_e32 v126, v126
	v_rcp_f32_e32 v127, v127
	v_mul_f32_e32 v102, 0xbfb8aa3b, v102
	v_mul_f32_e32 v103, 0xbfb8aa3b, v103
	v_pk_fma_f32 v[114:115], v[182:183], s[2:3], v[114:115] op_sel_hi:[1,0,1]
	s_waitcnt vmcnt(11)
	v_lshlrev_b32_e32 v182, 16, v176
	v_and_b32_e32 v183, 0xffff0000, v176
	v_lshlrev_b32_e32 v176, 16, v177
	v_and_b32_e32 v177, 0xffff0000, v177
	v_add_f32_e32 v118, 1.0, v118
	v_add_f32_e32 v119, 1.0, v119
	v_exp_f32_e32 v102, v102
	v_exp_f32_e32 v103, v103
	v_pk_fma_f32 v[94:95], v[94:95], s[0:1], v[138:139] op_sel_hi:[1,0,1]
	v_lshlrev_b32_e32 v180, 16, v178
	v_and_b32_e32 v181, 0xffff0000, v178
	v_lshlrev_b32_e32 v178, 16, v179
	v_and_b32_e32 v179, 0xffff0000, v179
	v_pk_mul_f32 v[122:123], v[122:123], v[176:177]
	v_rcp_f32_e32 v118, v118
	v_rcp_f32_e32 v119, v119
	v_mul_f32_e32 v94, 0xbfb8aa3b, v94
	v_mul_f32_e32 v95, 0xbfb8aa3b, v95
	v_pk_fma_f32 v[122:123], v[178:179], s[2:3], v[122:123] op_sel_hi:[1,0,1]
	s_waitcnt vmcnt(10)
	v_lshlrev_b32_e32 v178, 16, v172
	v_and_b32_e32 v179, 0xffff0000, v172
	v_lshlrev_b32_e32 v172, 16, v173
	v_and_b32_e32 v173, 0xffff0000, v173
	v_add_f32_e32 v106, 1.0, v106
	v_add_f32_e32 v107, 1.0, v107
	v_exp_f32_e32 v94, v94
	v_exp_f32_e32 v95, v95
	v_pk_fma_f32 v[78:79], v[78:79], s[0:1], v[134:135] op_sel_hi:[1,0,1]
	v_lshlrev_b32_e32 v176, 16, v174
	v_and_b32_e32 v177, 0xffff0000, v174
	v_lshlrev_b32_e32 v174, 16, v175
	v_and_b32_e32 v175, 0xffff0000, v175
	v_pk_mul_f32 v[126:127], v[126:127], v[172:173]
	v_rcp_f32_e32 v106, v106
	v_rcp_f32_e32 v107, v107
	v_mul_f32_e32 v78, 0xbfb8aa3b, v78
	v_mul_f32_e32 v79, 0xbfb8aa3b, v79
	v_pk_fma_f32 v[64:65], v[64:65], s[0:1], v[140:141] op_sel_hi:[1,0,1]
	v_pk_fma_f32 v[88:89], v[88:89], s[0:1], v[140:141] op_sel_hi:[1,0,1]
	v_pk_fma_f32 v[96:97], v[96:97], s[0:1], v[136:137] op_sel_hi:[1,0,1]
	v_pk_fma_f32 v[108:109], v[108:109], s[0:1], v[132:133] op_sel_hi:[1,0,1]
	v_pk_fma_f32 v[112:113], v[112:113], s[0:1], v[128:129] op_sel_hi:[1,0,1]
	v_pk_fma_f32 v[120:121], v[120:121], s[0:1], v[140:141] op_sel_hi:[1,0,1]
	v_pk_fma_f32 v[124:125], v[124:125], s[0:1], v[136:137] op_sel_hi:[1,0,1]
	v_pk_fma_f32 v[126:127], v[174:175], s[2:3], v[126:127] op_sel_hi:[1,0,1]
	v_pk_fma_f32 v[116:117], v[116:117], s[0:1], v[132:133] op_sel_hi:[1,0,1]
	s_waitcnt vmcnt(9)
	v_lshlrev_b32_e32 v174, 16, v168
	v_and_b32_e32 v175, 0xffff0000, v168
	v_lshlrev_b32_e32 v168, 16, v169
	v_and_b32_e32 v169, 0xffff0000, v169
	v_pk_fma_f32 v[104:105], v[104:105], s[0:1], v[128:129] op_sel_hi:[1,0,1]
	v_pk_fma_f32 v[100:101], v[100:101], s[0:1], v[140:141] op_sel_hi:[1,0,1]
	v_add_f32_e32 v102, 1.0, v102
	v_add_f32_e32 v103, 1.0, v103
	v_pk_fma_f32 v[92:93], v[92:93], s[0:1], v[136:137] op_sel_hi:[1,0,1]
	v_pk_fma_f32 v[76:77], v[76:77], s[0:1], v[132:133] op_sel_hi:[1,0,1]
	v_exp_f32_e32 v78, v78
	v_exp_f32_e32 v79, v79
	v_pk_fma_f32 v[68:69], v[68:69], s[0:1], v[128:129] op_sel_hi:[1,0,1]
	v_pk_fma_f32 v[70:71], v[70:71], s[0:1], v[130:131] op_sel_hi:[1,0,1]
	v_mul_f32_e32 v64, 0xbfb8aa3b, v64
	v_mul_f32_e32 v65, 0xbfb8aa3b, v65
	v_mul_f32_e32 v88, 0xbfb8aa3b, v88
	v_mul_f32_e32 v89, 0xbfb8aa3b, v89
	v_mul_f32_e32 v96, 0xbfb8aa3b, v96
	v_mul_f32_e32 v97, 0xbfb8aa3b, v97
	v_mul_f32_e32 v108, 0xbfb8aa3b, v108
	v_mul_f32_e32 v109, 0xbfb8aa3b, v109
	v_mul_f32_e32 v112, 0xbfb8aa3b, v112
	v_mul_f32_e32 v113, 0xbfb8aa3b, v113
	v_mul_f32_e32 v120, 0xbfb8aa3b, v120
	v_mul_f32_e32 v121, 0xbfb8aa3b, v121
	v_mul_f32_e32 v124, 0xbfb8aa3b, v124
	v_mul_f32_e32 v125, 0xbfb8aa3b, v125
	v_lshlrev_b32_e32 v172, 16, v170
	v_and_b32_e32 v173, 0xffff0000, v170
	v_lshlrev_b32_e32 v170, 16, v171
	v_and_b32_e32 v171, 0xffff0000, v171
	v_mul_f32_e32 v116, 0xbfb8aa3b, v116
	v_mul_f32_e32 v117, 0xbfb8aa3b, v117
	v_pk_mul_f32 v[118:119], v[118:119], v[168:169]
	v_mul_f32_e32 v104, 0xbfb8aa3b, v104
	v_mul_f32_e32 v105, 0xbfb8aa3b, v105
	v_mul_f32_e32 v100, 0xbfb8aa3b, v100
	v_mul_f32_e32 v101, 0xbfb8aa3b, v101
	v_rcp_f32_e32 v102, v102
	v_rcp_f32_e32 v103, v103
	v_mul_f32_e32 v92, 0xbfb8aa3b, v92
	v_mul_f32_e32 v93, 0xbfb8aa3b, v93
	v_mul_f32_e32 v76, 0xbfb8aa3b, v76
	v_mul_f32_e32 v77, 0xbfb8aa3b, v77
	v_mul_f32_e32 v68, 0xbfb8aa3b, v68
	v_mul_f32_e32 v69, 0xbfb8aa3b, v69
	v_mul_f32_e32 v70, 0xbfb8aa3b, v70
	v_mul_f32_e32 v71, 0xbfb8aa3b, v71
	v_exp_f32_e32 v64, v64
	v_exp_f32_e32 v65, v65
	v_exp_f32_e32 v88, v88
	v_exp_f32_e32 v89, v89
	v_exp_f32_e32 v96, v96
	v_exp_f32_e32 v97, v97
	v_exp_f32_e32 v108, v108
	v_exp_f32_e32 v109, v109
	v_exp_f32_e32 v112, v112
	v_exp_f32_e32 v113, v113
	v_exp_f32_e32 v120, v120
	v_exp_f32_e32 v121, v121
	v_exp_f32_e32 v124, v124
	v_exp_f32_e32 v125, v125
	v_exp_f32_e32 v116, v116
	v_exp_f32_e32 v117, v117
	v_pk_fma_f32 v[118:119], v[170:171], s[2:3], v[118:119] op_sel_hi:[1,0,1]
	v_exp_f32_e32 v104, v104
	s_waitcnt vmcnt(8)
	v_lshlrev_b32_e32 v170, 16, v164
	v_and_b32_e32 v171, 0xffff0000, v164
	v_exp_f32_e32 v105, v105
	v_lshlrev_b32_e32 v164, 16, v165
	v_and_b32_e32 v165, 0xffff0000, v165
	v_exp_f32_e32 v100, v100
	v_exp_f32_e32 v101, v101
	v_exp_f32_e32 v92, v92
	v_exp_f32_e32 v93, v93
	v_add_f32_e32 v94, 1.0, v94
	v_add_f32_e32 v95, 1.0, v95
	v_exp_f32_e32 v76, v76
	v_exp_f32_e32 v77, v77
	v_exp_f32_e32 v68, v68
	v_exp_f32_e32 v69, v69
	v_exp_f32_e32 v70, v70
	v_exp_f32_e32 v71, v71
	v_lshlrev_b32_e32 v168, 16, v166
	v_and_b32_e32 v169, 0xffff0000, v166
	v_lshlrev_b32_e32 v166, 16, v167
	v_and_b32_e32 v167, 0xffff0000, v167
	v_pk_mul_f32 v[106:107], v[106:107], v[164:165]
	v_rcp_f32_e32 v94, v94
	v_rcp_f32_e32 v95, v95
	v_pk_fma_f32 v[106:107], v[166:167], s[2:3], v[106:107] op_sel_hi:[1,0,1]
	s_waitcnt vmcnt(3)
	v_lshlrev_b32_e32 v166, 16, v160
	v_and_b32_e32 v167, 0xffff0000, v160
	v_lshlrev_b32_e32 v160, 16, v161
	v_and_b32_e32 v161, 0xffff0000, v161
	v_add_f32_e32 v78, 1.0, v78
	v_add_f32_e32 v79, 1.0, v79
	v_lshlrev_b32_e32 v164, 16, v162
	v_and_b32_e32 v165, 0xffff0000, v162
	v_lshlrev_b32_e32 v162, 16, v163
	v_and_b32_e32 v163, 0xffff0000, v163
	v_pk_mul_f32 v[102:103], v[102:103], v[160:161]
	v_rcp_f32_e32 v78, v78
	v_rcp_f32_e32 v79, v79
	v_add_f32_e32 v64, 1.0, v64
	v_add_f32_e32 v65, 1.0, v65
	v_add_f32_e32 v88, 1.0, v88
	v_add_f32_e32 v89, 1.0, v89
	v_add_f32_e32 v96, 1.0, v96
	v_add_f32_e32 v97, 1.0, v97
	v_add_f32_e32 v108, 1.0, v108
	v_add_f32_e32 v109, 1.0, v109
	v_add_f32_e32 v112, 1.0, v112
	v_add_f32_e32 v113, 1.0, v113
	v_add_f32_e32 v120, 1.0, v120
	v_add_f32_e32 v121, 1.0, v121
	v_add_f32_e32 v124, 1.0, v124
	v_add_f32_e32 v125, 1.0, v125
	v_add_f32_e32 v116, 1.0, v116
	v_add_f32_e32 v117, 1.0, v117
	v_add_f32_e32 v104, 1.0, v104
	v_add_f32_e32 v105, 1.0, v105
	v_add_f32_e32 v100, 1.0, v100
	v_add_f32_e32 v101, 1.0, v101
	v_pk_fma_f32 v[102:103], v[162:163], s[2:3], v[102:103] op_sel_hi:[1,0,1]
	s_waitcnt vmcnt(2)
	v_lshlrev_b32_e32 v162, 16, v156
	v_and_b32_e32 v163, 0xffff0000, v156
	v_add_f32_e32 v92, 1.0, v92
	v_add_f32_e32 v93, 1.0, v93
	v_lshlrev_b32_e32 v156, 16, v157
	v_and_b32_e32 v157, 0xffff0000, v157
	v_add_f32_e32 v76, 1.0, v76
	v_add_f32_e32 v77, 1.0, v77
	v_add_f32_e32 v68, 1.0, v68
	v_add_f32_e32 v69, 1.0, v69
	v_add_f32_e32 v70, 1.0, v70
	v_add_f32_e32 v71, 1.0, v71
	v_rcp_f32_e32 v64, v64
	v_rcp_f32_e32 v65, v65
	v_rcp_f32_e32 v88, v88
	v_rcp_f32_e32 v89, v89
	v_rcp_f32_e32 v96, v96
	v_rcp_f32_e32 v97, v97
	v_rcp_f32_e32 v108, v108
	v_rcp_f32_e32 v109, v109
	v_rcp_f32_e32 v112, v112
	v_rcp_f32_e32 v113, v113
	v_rcp_f32_e32 v120, v120
	v_rcp_f32_e32 v121, v121
	v_rcp_f32_e32 v124, v124
	v_rcp_f32_e32 v125, v125
	v_rcp_f32_e32 v116, v116
	v_rcp_f32_e32 v117, v117
	v_rcp_f32_e32 v104, v104
	v_rcp_f32_e32 v105, v105
	v_rcp_f32_e32 v100, v100
	v_rcp_f32_e32 v101, v101
	v_lshlrev_b32_e32 v160, 16, v158
	v_and_b32_e32 v161, 0xffff0000, v158
	v_lshlrev_b32_e32 v158, 16, v159
	v_and_b32_e32 v159, 0xffff0000, v159
	v_rcp_f32_e32 v92, v92
	v_rcp_f32_e32 v93, v93
	v_pk_mul_f32 v[94:95], v[94:95], v[156:157]
	v_rcp_f32_e32 v76, v76
	v_rcp_f32_e32 v77, v77
	v_rcp_f32_e32 v68, v68
	v_rcp_f32_e32 v70, v70
	v_rcp_f32_e32 v71, v71
	v_rcp_f32_e32 v69, v69
	v_pk_fma_f32 v[94:95], v[158:159], s[2:3], v[94:95] op_sel_hi:[1,0,1]
	s_waitcnt vmcnt(1)
	v_lshlrev_b32_e32 v158, 16, v152
	v_and_b32_e32 v159, 0xffff0000, v152
	v_lshlrev_b32_e32 v152, 16, v153
	v_and_b32_e32 v153, 0xffff0000, v153
	v_lshlrev_b32_e32 v156, 16, v154
	v_and_b32_e32 v157, 0xffff0000, v154
	v_lshlrev_b32_e32 v154, 16, v155
	v_and_b32_e32 v155, 0xffff0000, v155
	v_pk_mul_f32 v[78:79], v[78:79], v[152:153]
	v_pk_mul_f32 v[64:65], v[64:65], v[216:217]
	v_pk_fma_f32 v[78:79], v[154:155], s[2:3], v[78:79] op_sel_hi:[1,0,1]
	s_waitcnt vmcnt(0)
	v_lshlrev_b32_e32 v154, 16, v148
	v_and_b32_e32 v155, 0xffff0000, v148
	v_lshlrev_b32_e32 v148, 16, v149
	v_and_b32_e32 v149, 0xffff0000, v149
	v_pk_mul_f32 v[88:89], v[88:89], v[200:201]
	v_pk_mul_f32 v[96:97], v[96:97], v[194:195]
	v_pk_mul_f32 v[108:109], v[108:109], v[190:191]
	v_pk_mul_f32 v[112:113], v[112:113], v[186:187]
	v_pk_mul_f32 v[120:121], v[120:121], v[182:183]
	v_pk_mul_f32 v[124:125], v[124:125], v[178:179]
	v_pk_mul_f32 v[116:117], v[116:117], v[174:175]
	v_pk_mul_f32 v[104:105], v[104:105], v[170:171]
	v_pk_mul_f32 v[100:101], v[100:101], v[166:167]
	v_pk_mul_f32 v[92:93], v[92:93], v[162:163]
	v_pk_mul_f32 v[76:77], v[76:77], v[158:159]
	v_lshlrev_b32_e32 v152, 16, v150
	v_and_b32_e32 v153, 0xffff0000, v150
	v_lshlrev_b32_e32 v150, 16, v151
	v_and_b32_e32 v151, 0xffff0000, v151
	v_pk_mul_f32 v[70:71], v[70:71], v[148:149]
	v_pk_mul_f32 v[68:69], v[68:69], v[154:155]
	v_pk_fma_f32 v[64:65], v[214:215], s[2:3], v[64:65] op_sel_hi:[1,0,1]
	v_pk_fma_f32 v[88:89], v[198:199], s[2:3], v[88:89] op_sel_hi:[1,0,1]
	v_pk_fma_f32 v[96:97], v[192:193], s[2:3], v[96:97] op_sel_hi:[1,0,1]
	v_pk_fma_f32 v[108:109], v[188:189], s[2:3], v[108:109] op_sel_hi:[1,0,1]
	v_pk_fma_f32 v[112:113], v[184:185], s[2:3], v[112:113] op_sel_hi:[1,0,1]
	v_pk_fma_f32 v[120:121], v[180:181], s[2:3], v[120:121] op_sel_hi:[1,0,1]
	v_pk_fma_f32 v[124:125], v[176:177], s[2:3], v[124:125] op_sel_hi:[1,0,1]
	v_pk_fma_f32 v[116:117], v[172:173], s[2:3], v[116:117] op_sel_hi:[1,0,1]
	v_pk_fma_f32 v[104:105], v[168:169], s[2:3], v[104:105] op_sel_hi:[1,0,1]
	v_pk_fma_f32 v[100:101], v[164:165], s[2:3], v[100:101] op_sel_hi:[1,0,1]
	v_pk_fma_f32 v[92:93], v[160:161], s[2:3], v[92:93] op_sel_hi:[1,0,1]
	v_pk_fma_f32 v[76:77], v[156:157], s[2:3], v[76:77] op_sel_hi:[1,0,1]
	v_pk_fma_f32 v[70:71], v[150:151], s[2:3], v[70:71] op_sel_hi:[1,0,1]
	v_pk_fma_f32 v[68:69], v[152:153], s[2:3], v[68:69] op_sel_hi:[1,0,1]
	v_lshl_add_u64 v[148:149], v[146:147], 0, s[12:13]
	v_lshl_add_u64 v[150:151], s[8:9], 0, v[148:149]
	global_load_dwordx2 v[194:195], v[150:151], off
	v_lshl_add_u64 v[148:149], s[10:11], 0, v[148:149]
	global_load_dwordx2 v[198:199], v[148:149], off
	global_load_dwordx2 v[200:201], v[150:151], off offset:32
	global_load_dwordx2 v[202:203], v[150:151], off offset:256
	global_load_dwordx2 v[204:205], v[150:151], off offset:288
	global_load_dwordx2 v[206:207], v[148:149], off offset:32
	global_load_dwordx2 v[208:209], v[148:149], off offset:256
	global_load_dwordx2 v[210:211], v[148:149], off offset:288
	s_mov_b64 s[12:13], 0x90000
	v_lshl_add_u64 v[148:149], v[146:147], 0, s[12:13]
	v_lshl_add_u64 v[150:151], s[8:9], 0, v[148:149]
	v_lshl_add_u64 v[148:149], s[10:11], 0, v[148:149]
	global_load_dwordx2 v[192:193], v[150:151], off
	global_load_dwordx2 v[188:189], v[150:151], off offset:32
	global_load_dwordx2 v[184:185], v[150:151], off offset:256
	global_load_dwordx2 v[180:181], v[150:151], off offset:288
	global_load_dwordx2 v[190:191], v[148:149], off
	global_load_dwordx2 v[186:187], v[148:149], off offset:32
	global_load_dwordx2 v[182:183], v[148:149], off offset:256
	global_load_dwordx2 v[178:179], v[148:149], off offset:288
	s_mov_b64 s[12:13], 0xa0000
	v_lshl_add_u64 v[148:149], v[146:147], 0, s[12:13]
	s_mov_b64 s[12:13], 0xb0000
	v_lshl_add_u64 v[150:151], s[8:9], 0, v[148:149]
	v_lshl_add_u64 v[148:149], s[10:11], 0, v[148:149]
	v_lshl_add_u64 v[146:147], v[146:147], 0, s[12:13]
	global_load_dwordx2 v[176:177], v[150:151], off
	global_load_dwordx2 v[172:173], v[150:151], off offset:32
	global_load_dwordx2 v[168:169], v[150:151], off offset:256
	global_load_dwordx2 v[164:165], v[150:151], off offset:288
	global_load_dwordx2 v[174:175], v[148:149], off
	global_load_dwordx2 v[170:171], v[148:149], off offset:32
	global_load_dwordx2 v[166:167], v[148:149], off offset:256
	global_load_dwordx2 v[162:163], v[148:149], off offset:288
	v_lshl_add_u64 v[148:149], s[8:9], 0, v[146:147]
	v_lshl_add_u64 v[146:147], s[10:11], 0, v[146:147]
	global_load_dwordx2 v[160:161], v[148:149], off
	global_load_dwordx2 v[156:157], v[148:149], off offset:32
	global_load_dwordx2 v[152:153], v[148:149], off offset:256
	s_nop 0
	global_load_dwordx2 v[148:149], v[148:149], off offset:288
	s_nop 0
	global_load_dwordx2 v[158:159], v[146:147], off
	global_load_dwordx2 v[154:155], v[146:147], off offset:32
	global_load_dwordx2 v[150:151], v[146:147], off offset:256
	s_nop 0
	global_load_dwordx2 v[146:147], v[146:147], off offset:288
	v_pk_fma_f32 v[62:63], v[62:63], s[0:1], v[142:143] op_sel_hi:[1,0,1]
	v_pk_fma_f32 v[56:57], v[56:57], s[0:1], v[136:137] op_sel_hi:[1,0,1]
	v_mul_f32_e32 v62, 0xbfb8aa3b, v62
	v_mul_f32_e32 v63, 0xbfb8aa3b, v63
	v_exp_f32_e32 v62, v62
	v_exp_f32_e32 v63, v63
	v_pk_fma_f32 v[58:59], v[58:59], s[0:1], v[138:139] op_sel_hi:[1,0,1]
	v_mul_f32_e32 v56, 0xbfb8aa3b, v56
	v_mul_f32_e32 v57, 0xbfb8aa3b, v57
	v_mul_f32_e32 v58, 0xbfb8aa3b, v58
	v_mul_f32_e32 v59, 0xbfb8aa3b, v59
	v_exp_f32_e32 v56, v56
	v_exp_f32_e32 v57, v57
	v_exp_f32_e32 v58, v58
	v_exp_f32_e32 v59, v59
	v_pk_fma_f32 v[54:55], v[54:55], s[0:1], v[134:135] op_sel_hi:[1,0,1]
	v_pk_fma_f32 v[52:53], v[52:53], s[0:1], v[132:133] op_sel_hi:[1,0,1]
	v_mul_f32_e32 v54, 0xbfb8aa3b, v54
	v_mul_f32_e32 v55, 0xbfb8aa3b, v55
	v_pk_fma_f32 v[50:51], v[50:51], s[0:1], v[130:131] op_sel_hi:[1,0,1]
	v_add_f32_e32 v62, 1.0, v62
	v_add_f32_e32 v63, 1.0, v63
	v_mul_f32_e32 v52, 0xbfb8aa3b, v52
	v_mul_f32_e32 v53, 0xbfb8aa3b, v53
	v_exp_f32_e32 v54, v54
	v_exp_f32_e32 v55, v55
	v_pk_fma_f32 v[48:49], v[48:49], s[0:1], v[128:129] op_sel_hi:[1,0,1]
	v_mul_f32_e32 v50, 0xbfb8aa3b, v50
	v_mul_f32_e32 v51, 0xbfb8aa3b, v51
	v_rcp_f32_e32 v62, v62
	v_rcp_f32_e32 v63, v63
	v_exp_f32_e32 v52, v52
	v_exp_f32_e32 v53, v53
	v_mul_f32_e32 v48, 0xbfb8aa3b, v48
	v_mul_f32_e32 v49, 0xbfb8aa3b, v49
	v_exp_f32_e32 v50, v50
	v_exp_f32_e32 v51, v51
	v_pk_fma_f32 v[46:47], v[46:47], s[0:1], v[142:143] op_sel_hi:[1,0,1]
	v_add_f32_e32 v56, 1.0, v56
	v_add_f32_e32 v57, 1.0, v57
	v_add_f32_e32 v58, 1.0, v58
	v_add_f32_e32 v59, 1.0, v59
	v_exp_f32_e32 v48, v48
	v_exp_f32_e32 v49, v49
	v_mul_f32_e32 v46, 0xbfb8aa3b, v46
	v_mul_f32_e32 v47, 0xbfb8aa3b, v47
	v_rcp_f32_e32 v56, v56
	v_rcp_f32_e32 v58, v58
	v_rcp_f32_e32 v59, v59
	v_rcp_f32_e32 v57, v57
	v_exp_f32_e32 v46, v46
	v_exp_f32_e32 v47, v47
	v_pk_fma_f32 v[42:43], v[42:43], s[0:1], v[138:139] op_sel_hi:[1,0,1]
	v_add_f32_e32 v54, 1.0, v54
	v_add_f32_e32 v55, 1.0, v55
	v_mul_f32_e32 v42, 0xbfb8aa3b, v42
	v_mul_f32_e32 v43, 0xbfb8aa3b, v43
	v_add_f32_e32 v52, 1.0, v52
	s_waitcnt vmcnt(30)
	v_lshlrev_b32_e32 v214, 16, v198
	v_and_b32_e32 v215, 0xffff0000, v198
	v_lshlrev_b32_e32 v198, 16, v199
	v_and_b32_e32 v199, 0xffff0000, v199
	v_lshlrev_b32_e32 v212, 16, v194
	v_and_b32_e32 v213, 0xffff0000, v194
	v_lshlrev_b32_e32 v194, 16, v195
	v_and_b32_e32 v195, 0xffff0000, v195
	v_pk_mul_f32 v[62:63], v[62:63], v[198:199]
	v_add_f32_e32 v53, 1.0, v53
	v_rcp_f32_e32 v54, v54
	v_rcp_f32_e32 v55, v55
	v_add_f32_e32 v50, 1.0, v50
	v_add_f32_e32 v51, 1.0, v51
	v_exp_f32_e32 v42, v42
	v_exp_f32_e32 v43, v43
	v_pk_fma_f32 v[38:39], v[38:39], s[0:1], v[134:135] op_sel_hi:[1,0,1]
	v_pk_fma_f32 v[62:63], v[194:195], s[2:3], v[62:63] op_sel_hi:[1,0,1]
	s_waitcnt vmcnt(29)
	v_lshlrev_b32_e32 v194, 16, v200
	v_and_b32_e32 v195, 0xffff0000, v200
	v_lshlrev_b32_e32 v198, 16, v201
	v_and_b32_e32 v199, 0xffff0000, v201
	s_waitcnt vmcnt(26)
	v_lshlrev_b32_e32 v200, 16, v206
	v_and_b32_e32 v201, 0xffff0000, v206
	v_lshlrev_b32_e32 v206, 16, v207
	v_and_b32_e32 v207, 0xffff0000, v207
	v_rcp_f32_e32 v52, v52
	v_rcp_f32_e32 v53, v53
	v_add_f32_e32 v48, 1.0, v48
	v_add_f32_e32 v49, 1.0, v49
	v_rcp_f32_e32 v50, v50
	v_rcp_f32_e32 v51, v51
	v_mul_f32_e32 v38, 0xbfb8aa3b, v38
	v_mul_f32_e32 v39, 0xbfb8aa3b, v39
	v_pk_mul_f32 v[58:59], v[58:59], v[206:207]
	v_pk_mul_f32 v[56:57], v[56:57], v[200:201]
	v_rcp_f32_e32 v48, v48
	v_rcp_f32_e32 v49, v49
	v_add_f32_e32 v46, 1.0, v46
	v_add_f32_e32 v47, 1.0, v47
	v_exp_f32_e32 v38, v38
	v_exp_f32_e32 v39, v39
	v_pk_fma_f32 v[22:23], v[22:23], s[0:1], v[130:131] op_sel_hi:[1,0,1]
	v_pk_fma_f32 v[58:59], v[198:199], s[2:3], v[58:59] op_sel_hi:[1,0,1]
	v_pk_fma_f32 v[56:57], v[194:195], s[2:3], v[56:57] op_sel_hi:[1,0,1]
	v_lshlrev_b32_e32 v194, 16, v202
	v_and_b32_e32 v195, 0xffff0000, v202
	v_lshlrev_b32_e32 v198, 16, v203
	v_and_b32_e32 v199, 0xffff0000, v203
	s_waitcnt vmcnt(25)
	v_lshlrev_b32_e32 v202, 16, v209
	v_and_b32_e32 v203, 0xffff0000, v209
	v_rcp_f32_e32 v46, v46
	v_rcp_f32_e32 v47, v47
	v_mul_f32_e32 v22, 0xbfb8aa3b, v22
	v_mul_f32_e32 v23, 0xbfb8aa3b, v23
	v_lshlrev_b32_e32 v200, 16, v208
	v_and_b32_e32 v201, 0xffff0000, v208
	v_pk_mul_f32 v[54:55], v[54:55], v[202:203]
	s_waitcnt vmcnt(24)
	v_lshlrev_b32_e32 v202, 16, v211
	v_and_b32_e32 v203, 0xffff0000, v211
	v_add_f32_e32 v42, 1.0, v42
	v_add_f32_e32 v43, 1.0, v43
	v_exp_f32_e32 v22, v22
	v_exp_f32_e32 v23, v23
	v_pk_fma_f32 v[26:27], v[26:27], s[0:1], v[142:143] op_sel_hi:[1,0,1]
	v_pk_mul_f32 v[52:53], v[52:53], v[200:201]
	v_pk_fma_f32 v[54:55], v[198:199], s[2:3], v[54:55] op_sel_hi:[1,0,1]
	v_lshlrev_b32_e32 v198, 16, v205
	v_and_b32_e32 v199, 0xffff0000, v205
	v_lshlrev_b32_e32 v200, 16, v210
	v_and_b32_e32 v201, 0xffff0000, v210
	v_pk_mul_f32 v[50:51], v[50:51], v[202:203]
	v_rcp_f32_e32 v42, v42
	v_rcp_f32_e32 v43, v43
	v_mul_f32_e32 v26, 0xbfb8aa3b, v26
	v_mul_f32_e32 v27, 0xbfb8aa3b, v27
	v_pk_fma_f32 v[52:53], v[194:195], s[2:3], v[52:53] op_sel_hi:[1,0,1]
	v_lshlrev_b32_e32 v194, 16, v204
	v_and_b32_e32 v195, 0xffff0000, v204
	v_pk_mul_f32 v[48:49], v[48:49], v[200:201]
	v_pk_fma_f32 v[50:51], v[198:199], s[2:3], v[50:51] op_sel_hi:[1,0,1]
	s_waitcnt vmcnt(19)
	v_lshlrev_b32_e32 v198, 16, v190
	v_and_b32_e32 v199, 0xffff0000, v190
	v_lshlrev_b32_e32 v190, 16, v191
	v_and_b32_e32 v191, 0xffff0000, v191
	v_add_f32_e32 v38, 1.0, v38
	v_add_f32_e32 v39, 1.0, v39
	v_exp_f32_e32 v26, v26
	v_exp_f32_e32 v27, v27
	v_pk_fma_f32 v[18:19], v[18:19], s[0:1], v[138:139] op_sel_hi:[1,0,1]
	v_pk_fma_f32 v[48:49], v[194:195], s[2:3], v[48:49] op_sel_hi:[1,0,1]
	v_lshlrev_b32_e32 v194, 16, v192
	v_and_b32_e32 v195, 0xffff0000, v192
	v_lshlrev_b32_e32 v192, 16, v193
	v_and_b32_e32 v193, 0xffff0000, v193
	v_pk_mul_f32 v[46:47], v[46:47], v[190:191]
	v_rcp_f32_e32 v38, v38
	v_rcp_f32_e32 v39, v39
	v_mul_f32_e32 v18, 0xbfb8aa3b, v18
	v_mul_f32_e32 v19, 0xbfb8aa3b, v19
	v_pk_fma_f32 v[46:47], v[192:193], s[2:3], v[46:47] op_sel_hi:[1,0,1]
	s_waitcnt vmcnt(18)
	v_lshlrev_b32_e32 v192, 16, v186
	v_and_b32_e32 v193, 0xffff0000, v186
	v_lshlrev_b32_e32 v186, 16, v187
	v_and_b32_e32 v187, 0xffff0000, v187
	v_add_f32_e32 v22, 1.0, v22
	v_add_f32_e32 v23, 1.0, v23
	v_exp_f32_e32 v18, v18
	v_exp_f32_e32 v19, v19
	v_pk_fma_f32 v[34:35], v[34:35], s[0:1], v[134:135] op_sel_hi:[1,0,1]
	v_pk_fma_f32 v[14:15], v[14:15], s[0:1], v[134:135] op_sel_hi:[1,0,1]
	v_pk_fma_f32 v[8:9], v[8:9], s[0:1], v[128:129] op_sel_hi:[1,0,1]
	v_pk_fma_f32 v[10:11], v[10:11], s[0:1], v[130:131] op_sel_hi:[1,0,1]
	v_lshlrev_b32_e32 v190, 16, v188
	v_and_b32_e32 v191, 0xffff0000, v188
	v_lshlrev_b32_e32 v188, 16, v189
	v_and_b32_e32 v189, 0xffff0000, v189
	v_pk_mul_f32 v[42:43], v[42:43], v[186:187]
	v_rcp_f32_e32 v22, v22
	v_rcp_f32_e32 v23, v23
	v_mul_f32_e32 v34, 0xbfb8aa3b, v34
	v_mul_f32_e32 v35, 0xbfb8aa3b, v35
	v_mul_f32_e32 v14, 0xbfb8aa3b, v14
	v_mul_f32_e32 v15, 0xbfb8aa3b, v15
	v_mul_f32_e32 v8, 0xbfb8aa3b, v8
	v_mul_f32_e32 v9, 0xbfb8aa3b, v9
	v_mul_f32_e32 v10, 0xbfb8aa3b, v10
	v_mul_f32_e32 v11, 0xbfb8aa3b, v11
	v_pk_fma_f32 v[42:43], v[188:189], s[2:3], v[42:43] op_sel_hi:[1,0,1]
	s_waitcnt vmcnt(17)
	v_lshlrev_b32_e32 v188, 16, v182
	v_and_b32_e32 v189, 0xffff0000, v182
	v_lshlrev_b32_e32 v182, 16, v183
	v_and_b32_e32 v183, 0xffff0000, v183
	v_add_f32_e32 v26, 1.0, v26
	v_add_f32_e32 v27, 1.0, v27
	v_exp_f32_e32 v34, v34
	v_exp_f32_e32 v35, v35
	v_pk_fma_f32 v[30:31], v[30:31], s[0:1], v[130:131] op_sel_hi:[1,0,1]
	v_pk_fma_f32 v[4:5], v[4:5], s[0:1], v[140:141] op_sel_hi:[1,0,1]
	v_exp_f32_e32 v14, v14
	v_exp_f32_e32 v15, v15
	v_exp_f32_e32 v8, v8
	v_exp_f32_e32 v9, v9
	v_exp_f32_e32 v10, v10
	v_exp_f32_e32 v11, v11
	v_lshlrev_b32_e32 v186, 16, v184
	v_and_b32_e32 v187, 0xffff0000, v184
	v_lshlrev_b32_e32 v184, 16, v185
	v_and_b32_e32 v185, 0xffff0000, v185
	v_pk_mul_f32 v[38:39], v[38:39], v[182:183]
	v_rcp_f32_e32 v26, v26
	v_rcp_f32_e32 v27, v27
	v_mul_f32_e32 v30, 0xbfb8aa3b, v30
	v_mul_f32_e32 v31, 0xbfb8aa3b, v31
	v_mul_f32_e32 v4, 0xbfb8aa3b, v4
	v_mul_f32_e32 v5, 0xbfb8aa3b, v5
	v_pk_fma_f32 v[38:39], v[184:185], s[2:3], v[38:39] op_sel_hi:[1,0,1]
	s_waitcnt vmcnt(16)
	v_lshlrev_b32_e32 v184, 16, v178
	v_and_b32_e32 v185, 0xffff0000, v178
	v_lshlrev_b32_e32 v178, 16, v179
	v_and_b32_e32 v179, 0xffff0000, v179
	v_add_f32_e32 v18, 1.0, v18
	v_add_f32_e32 v19, 1.0, v19
	v_exp_f32_e32 v30, v30
	v_exp_f32_e32 v31, v31
	v_exp_f32_e32 v4, v4
	v_exp_f32_e32 v5, v5
	v_lshlrev_b32_e32 v182, 16, v180
	v_and_b32_e32 v183, 0xffff0000, v180
	v_lshlrev_b32_e32 v180, 16, v181
	v_and_b32_e32 v181, 0xffff0000, v181
	v_pk_mul_f32 v[22:23], v[22:23], v[178:179]
	v_rcp_f32_e32 v18, v18
	v_rcp_f32_e32 v19, v19
	v_pk_fma_f32 v[22:23], v[180:181], s[2:3], v[22:23] op_sel_hi:[1,0,1]
	s_waitcnt vmcnt(11)
	v_lshlrev_b32_e32 v180, 16, v174
	v_and_b32_e32 v181, 0xffff0000, v174
	v_lshlrev_b32_e32 v174, 16, v175
	v_and_b32_e32 v175, 0xffff0000, v175
	v_add_f32_e32 v34, 1.0, v34
	v_add_f32_e32 v35, 1.0, v35
	v_pk_fma_f32 v[6:7], v[6:7], s[0:1], v[142:143] op_sel_hi:[1,0,1]
	v_pk_fma_f32 v[0:1], v[0:1], s[0:1], v[136:137] op_sel_hi:[1,0,1]
	v_pk_fma_f32 v[2:3], v[2:3], s[0:1], v[138:139] op_sel_hi:[1,0,1]
	v_pk_fma_f32 v[12:13], v[12:13], s[0:1], v[132:133] op_sel_hi:[1,0,1]
	v_add_f32_e32 v14, 1.0, v14
	v_add_f32_e32 v15, 1.0, v15
	v_add_f32_e32 v8, 1.0, v8
	v_add_f32_e32 v9, 1.0, v9
	v_add_f32_e32 v10, 1.0, v10
	v_add_f32_e32 v11, 1.0, v11
	v_lshlrev_b32_e32 v178, 16, v176
	v_and_b32_e32 v179, 0xffff0000, v176
	v_lshlrev_b32_e32 v176, 16, v177
	v_and_b32_e32 v177, 0xffff0000, v177
	v_pk_mul_f32 v[26:27], v[26:27], v[174:175]
	v_rcp_f32_e32 v34, v34
	v_rcp_f32_e32 v35, v35
	v_mul_f32_e32 v6, 0xbfb8aa3b, v6
	v_mul_f32_e32 v7, 0xbfb8aa3b, v7
	v_mul_f32_e32 v0, 0xbfb8aa3b, v0
	v_mul_f32_e32 v1, 0xbfb8aa3b, v1
	v_mul_f32_e32 v2, 0xbfb8aa3b, v2
	v_mul_f32_e32 v3, 0xbfb8aa3b, v3
	v_mul_f32_e32 v12, 0xbfb8aa3b, v12
	v_mul_f32_e32 v13, 0xbfb8aa3b, v13
	v_rcp_f32_e32 v14, v14
	v_rcp_f32_e32 v15, v15
	v_rcp_f32_e32 v8, v8
	v_rcp_f32_e32 v10, v10
	v_rcp_f32_e32 v11, v11
	v_rcp_f32_e32 v9, v9
	v_pk_fma_f32 v[26:27], v[176:177], s[2:3], v[26:27] op_sel_hi:[1,0,1]
	s_waitcnt vmcnt(10)
	v_lshlrev_b32_e32 v176, 16, v170
	v_and_b32_e32 v177, 0xffff0000, v170
	v_lshlrev_b32_e32 v170, 16, v171
	v_and_b32_e32 v171, 0xffff0000, v171
	v_add_f32_e32 v30, 1.0, v30
	v_add_f32_e32 v31, 1.0, v31
	v_add_f32_e32 v4, 1.0, v4
	v_exp_f32_e32 v6, v6
	v_exp_f32_e32 v7, v7
	v_add_f32_e32 v5, 1.0, v5
	v_exp_f32_e32 v0, v0
	v_exp_f32_e32 v1, v1
	v_exp_f32_e32 v2, v2
	v_exp_f32_e32 v3, v3
	v_exp_f32_e32 v12, v12
	v_exp_f32_e32 v13, v13
	v_lshlrev_b32_e32 v174, 16, v172
	v_and_b32_e32 v175, 0xffff0000, v172
	v_lshlrev_b32_e32 v172, 16, v173
	v_and_b32_e32 v173, 0xffff0000, v173
	v_pk_mul_f32 v[18:19], v[18:19], v[170:171]
	v_rcp_f32_e32 v30, v30
	v_rcp_f32_e32 v31, v31
	v_rcp_f32_e32 v4, v4
	v_rcp_f32_e32 v5, v5
	v_pk_fma_f32 v[20:21], v[20:21], s[0:1], v[128:129] op_sel_hi:[1,0,1]
	v_pk_fma_f32 v[18:19], v[172:173], s[2:3], v[18:19] op_sel_hi:[1,0,1]
	s_waitcnt vmcnt(9)
	v_lshlrev_b32_e32 v172, 16, v166
	v_and_b32_e32 v173, 0xffff0000, v166
	v_lshlrev_b32_e32 v166, 16, v167
	v_and_b32_e32 v167, 0xffff0000, v167
	v_pk_fma_f32 v[28:29], v[28:29], s[0:1], v[128:129] op_sel_hi:[1,0,1]
	s_waitcnt vmcnt(1)
	v_lshlrev_b32_e32 v134, 16, v151
	v_and_b32_e32 v135, 0xffff0000, v151
	s_waitcnt vmcnt(0)
	v_lshlrev_b32_e32 v128, 16, v146
	v_and_b32_e32 v129, 0xffff0000, v146
	v_lshlrev_b32_e32 v130, 16, v147
	v_and_b32_e32 v131, 0xffff0000, v147
	v_lshlrev_b32_e32 v170, 16, v168
	v_and_b32_e32 v171, 0xffff0000, v168
	v_lshlrev_b32_e32 v168, 16, v169
	v_and_b32_e32 v169, 0xffff0000, v169
	v_pk_mul_f32 v[34:35], v[34:35], v[166:167]
	v_pk_mul_f32 v[14:15], v[14:15], v[134:135]
	v_lshlrev_b32_e32 v134, 16, v149
	v_and_b32_e32 v135, 0xffff0000, v149
	v_pk_mul_f32 v[10:11], v[10:11], v[130:131]
	v_pk_mul_f32 v[8:9], v[8:9], v[128:129]
	v_mbcnt_lo_u32_b32 v128, -1, 0
	v_pk_fma_f32 v[60:61], v[60:61], s[0:1], v[140:141] op_sel_hi:[1,0,1]
	v_pk_fma_f32 v[44:45], v[44:45], s[0:1], v[140:141] op_sel_hi:[1,0,1]
	v_pk_fma_f32 v[24:25], v[24:25], s[0:1], v[140:141] op_sel_hi:[1,0,1]
	v_pk_fma_f32 v[34:35], v[168:169], s[2:3], v[34:35] op_sel_hi:[1,0,1]
	v_lshlrev_b32_e32 v168, 16, v162
	v_and_b32_e32 v169, 0xffff0000, v162
	v_lshlrev_b32_e32 v162, 16, v163
	v_and_b32_e32 v163, 0xffff0000, v163
	v_lshlrev_b32_e32 v140, 16, v158
	v_and_b32_e32 v141, 0xffff0000, v158
	v_add_f32_e32 v6, 1.0, v6
	v_add_f32_e32 v7, 1.0, v7
	v_add_f32_e32 v0, 1.0, v0
	v_add_f32_e32 v1, 1.0, v1
	v_add_f32_e32 v2, 1.0, v2
	v_add_f32_e32 v3, 1.0, v3
	v_add_f32_e32 v12, 1.0, v12
	v_add_f32_e32 v13, 1.0, v13
	v_pk_fma_f32 v[10:11], v[134:135], s[2:3], v[10:11] op_sel_hi:[1,0,1]
	v_mbcnt_hi_u32_b32 v135, -1, v128
	v_pk_mul_f32 v[30:31], v[30:31], v[162:163]
	v_lshlrev_b32_e32 v162, 16, v160
	v_and_b32_e32 v163, 0xffff0000, v160
	v_rcp_f32_e32 v6, v6
	v_rcp_f32_e32 v7, v7
	v_pk_mul_f32 v[4:5], v[4:5], v[140:141]
	v_rcp_f32_e32 v0, v0
	v_rcp_f32_e32 v2, v2
	v_rcp_f32_e32 v3, v3
	v_rcp_f32_e32 v1, v1
	v_rcp_f32_e32 v12, v12
	v_rcp_f32_e32 v13, v13
	v_and_b32_e32 v129, 64, v135
	v_pk_fma_f32 v[4:5], v[162:163], s[2:3], v[4:5] op_sel_hi:[1,0,1]
	v_xor_b32_e32 v128, 16, v135
	v_add_u32_e32 v162, 64, v129
	v_cmp_lt_i32_e32 vcc, v128, v162
	v_pk_fma_f32 v[40:41], v[40:41], s[0:1], v[136:137] op_sel_hi:[1,0,1]
	v_pk_fma_f32 v[36:37], v[36:37], s[0:1], v[132:133] op_sel_hi:[1,0,1]
	v_pk_fma_f32 v[16:17], v[16:17], s[0:1], v[136:137] op_sel_hi:[1,0,1]
	v_pk_fma_f32 v[32:33], v[32:33], s[0:1], v[132:133] op_sel_hi:[1,0,1]
	v_lshlrev_b32_e32 v142, 16, v159
	v_and_b32_e32 v143, 0xffff0000, v159
	v_lshlrev_b32_e32 v136, 16, v154
	v_and_b32_e32 v137, 0xffff0000, v154
	v_lshlrev_b32_e32 v138, 16, v155
	v_and_b32_e32 v139, 0xffff0000, v155
	v_lshlrev_b32_e32 v132, 16, v150
	v_and_b32_e32 v133, 0xffff0000, v150
	v_cndmask_b32_e32 v128, v135, v128, vcc
	v_pk_mul_f32 v[6:7], v[6:7], v[142:143]
	v_lshlrev_b32_e32 v140, 16, v156
	v_and_b32_e32 v141, 0xffff0000, v156
	v_lshlrev_b32_e32 v142, 16, v157
	v_and_b32_e32 v143, 0xffff0000, v157
	v_pk_mul_f32 v[2:3], v[2:3], v[138:139]
	v_pk_mul_f32 v[0:1], v[0:1], v[136:137]
	v_lshlrev_b32_e32 v136, 16, v152
	v_and_b32_e32 v137, 0xffff0000, v152
	v_lshlrev_b32_e32 v138, 16, v153
	v_and_b32_e32 v139, 0xffff0000, v153
	v_pk_mul_f32 v[12:13], v[12:13], v[132:133]
	v_lshlrev_b32_e32 v132, 16, v148
	v_and_b32_e32 v133, 0xffff0000, v148
	v_lshlrev_b32_e32 v134, 2, v128
	v_mul_f32_e32 v128, v74, v74
	v_pk_fma_f32 v[2:3], v[142:143], s[2:3], v[2:3] op_sel_hi:[1,0,1]
	v_pk_fma_f32 v[0:1], v[140:141], s[2:3], v[0:1] op_sel_hi:[1,0,1]
	v_pk_fma_f32 v[14:15], v[138:139], s[2:3], v[14:15] op_sel_hi:[1,0,1]
	v_pk_fma_f32 v[12:13], v[136:137], s[2:3], v[12:13] op_sel_hi:[1,0,1]
	v_pk_fma_f32 v[8:9], v[132:133], s[2:3], v[8:9] op_sel_hi:[1,0,1]
	v_add_f32_e32 v130, v64, v65
	v_add_f32_e32 v132, v66, v67
	v_mul_f32_e32 v137, v64, v64
	v_mul_f32_e32 v139, v65, v65
	v_mul_f32_e32 v141, v66, v66
	v_mul_f32_e32 v143, v67, v67
	v_mul_f32_e32 v131, v72, v72
	v_mul_f32_e32 v133, v73, v73
	v_pk_fma_f32 v[128:129], v[74:75], v[74:75], v[128:129] op_sel_hi:[1,1,0]
	v_mov_b32_e32 v136, v72
	v_mov_b32_e32 v138, v73
	v_mov_b32_e32 v140, v74
	v_mov_b32_e32 v142, v75
	v_pk_add_f32 v[136:137], v[136:137], v[138:139]
	v_pk_add_f32 v[138:139], v[140:141], v[142:143]
	v_pk_add_f32 v[130:131], v[130:131], v[132:133]
	v_mov_b32_e32 v128, 0
	v_mul_f32_e32 v147, v80, v80
	v_mul_f32_e32 v149, v81, v81
	v_mul_f32_e32 v151, v82, v82
	v_mul_f32_e32 v153, v83, v83
	v_pk_add_f32 v[136:137], v[136:137], v[138:139]
	v_pk_add_f32 v[130:131], v[130:131], v[128:129]
	v_mov_b32_e32 v146, v80
	v_mov_b32_e32 v148, v81
	v_mov_b32_e32 v150, v82
	v_mov_b32_e32 v152, v83
	v_lshlrev_b32_e32 v160, 16, v161
	v_and_b32_e32 v161, 0xffff0000, v161
	v_pk_add_f32 v[130:131], v[136:137], v[130:131]
	v_pk_add_f32 v[132:133], v[146:147], v[148:149]
	v_pk_add_f32 v[136:137], v[150:151], v[152:153]
	v_mul_f32_e32 v60, 0xbfb8aa3b, v60
	v_mul_f32_e32 v61, 0xbfb8aa3b, v61
	v_mul_f32_e32 v44, 0xbfb8aa3b, v44
	v_mul_f32_e32 v45, 0xbfb8aa3b, v45
	v_mul_f32_e32 v40, 0xbfb8aa3b, v40
	v_mul_f32_e32 v41, 0xbfb8aa3b, v41
	v_mul_f32_e32 v36, 0xbfb8aa3b, v36
	v_mul_f32_e32 v37, 0xbfb8aa3b, v37
	v_mul_f32_e32 v20, 0xbfb8aa3b, v20
	v_mul_f32_e32 v21, 0xbfb8aa3b, v21
	v_mul_f32_e32 v24, 0xbfb8aa3b, v24
	v_mul_f32_e32 v25, 0xbfb8aa3b, v25
	v_mul_f32_e32 v16, 0xbfb8aa3b, v16
	v_mul_f32_e32 v17, 0xbfb8aa3b, v17
	v_mul_f32_e32 v32, 0xbfb8aa3b, v32
	v_mul_f32_e32 v33, 0xbfb8aa3b, v33
	v_mul_f32_e32 v28, 0xbfb8aa3b, v28
	v_mul_f32_e32 v29, 0xbfb8aa3b, v29
	v_pk_fma_f32 v[6:7], v[160:161], s[2:3], v[6:7] op_sel_hi:[1,0,1]
	v_mul_f32_e32 v155, v84, v84
	v_mul_f32_e32 v157, v85, v85
	v_mul_f32_e32 v159, v86, v86
	v_mul_f32_e32 v161, v87, v87
	v_pk_add_f32 v[132:133], v[132:133], v[136:137]
	v_mov_b32_e32 v154, v84
	v_mov_b32_e32 v156, v85
	v_mov_b32_e32 v158, v86
	v_mov_b32_e32 v160, v87
	v_exp_f32_e32 v60, v60
	v_exp_f32_e32 v61, v61
	v_exp_f32_e32 v44, v44
	v_exp_f32_e32 v45, v45
	v_exp_f32_e32 v40, v40
	v_exp_f32_e32 v41, v41
	v_exp_f32_e32 v36, v36
	v_exp_f32_e32 v37, v37
	v_exp_f32_e32 v20, v20
	v_exp_f32_e32 v21, v21
	v_exp_f32_e32 v24, v24
	v_exp_f32_e32 v25, v25
	v_exp_f32_e32 v16, v16
	v_exp_f32_e32 v17, v17
	v_exp_f32_e32 v32, v32
	v_exp_f32_e32 v33, v33
	v_exp_f32_e32 v28, v28
	v_exp_f32_e32 v29, v29
	v_pk_add_f32 v[130:131], v[132:133], v[130:131]
	v_pk_add_f32 v[132:133], v[154:155], v[156:157]
	v_pk_add_f32 v[136:137], v[158:159], v[160:161]
	v_add_f32_e32 v60, 1.0, v60
	v_pk_add_f32 v[132:133], v[132:133], v[136:137]
	v_add_f32_e32 v61, 1.0, v61
	v_pk_add_f32 v[130:131], v[132:133], v[130:131]
	v_mov_b32_e32 v132, v130
	v_mov_b32_e32 v133, v131
	s_nop 1
	v_permlane16_swap_b32_e32 v130, v132
	v_permlane16_swap_b32_e32 v131, v133
	v_add_f32_e32 v44, 1.0, v44
	v_add_f32_e32 v45, 1.0, v45
	v_add_f32_e32 v40, 1.0, v40
	v_add_f32_e32 v41, 1.0, v41
	v_add_f32_e32 v36, 1.0, v36
	v_add_f32_e32 v37, 1.0, v37
	v_add_f32_e32 v20, 1.0, v20
	v_add_f32_e32 v21, 1.0, v21
	v_add_f32_e32 v24, 1.0, v24
	v_add_f32_e32 v25, 1.0, v25
	v_add_f32_e32 v16, 1.0, v16
	v_add_f32_e32 v17, 1.0, v17
	v_add_f32_e32 v32, 1.0, v32
	v_add_f32_e32 v33, 1.0, v33
	v_add_f32_e32 v28, 1.0, v28
	v_add_f32_e32 v29, 1.0, v29
	v_rcp_f32_e32 v60, v60
	v_rcp_f32_e32 v61, v61
	v_rcp_f32_e32 v44, v44
	v_rcp_f32_e32 v45, v45
	v_rcp_f32_e32 v40, v40
	v_rcp_f32_e32 v41, v41
	v_rcp_f32_e32 v36, v36
	v_rcp_f32_e32 v37, v37
	v_rcp_f32_e32 v20, v20
	v_rcp_f32_e32 v21, v21
	v_rcp_f32_e32 v24, v24
	v_rcp_f32_e32 v25, v25
	v_rcp_f32_e32 v16, v16
	v_rcp_f32_e32 v17, v17
	v_rcp_f32_e32 v32, v32
	v_rcp_f32_e32 v33, v33
	v_rcp_f32_e32 v28, v28
	v_rcp_f32_e32 v29, v29
	v_xor_b32_e32 v129, 32, v135
	v_cmp_lt_i32_e32 vcc, v129, v162
	s_waitcnt lgkmcnt(0)
	v_pk_add_f32 v[130:131], v[130:131], v[132:133]
	v_pk_mul_f32 v[60:61], v[60:61], v[214:215]
	v_cndmask_b32_e32 v129, v135, v129, vcc
	v_lshlrev_b32_e32 v135, 2, v129
	v_pk_mul_f32 v[44:45], v[44:45], v[198:199]
	v_pk_mul_f32 v[40:41], v[40:41], v[192:193]
	v_pk_mul_f32 v[36:37], v[36:37], v[188:189]
	v_pk_mul_f32 v[20:21], v[20:21], v[184:185]
	v_pk_mul_f32 v[24:25], v[24:25], v[180:181]
	v_pk_mul_f32 v[16:17], v[16:17], v[176:177]
	v_pk_mul_f32 v[32:33], v[32:33], v[172:173]
	v_lshlrev_b32_e32 v166, 16, v164
	v_and_b32_e32 v167, 0xffff0000, v164
	v_lshlrev_b32_e32 v164, 16, v165
	v_and_b32_e32 v165, 0xffff0000, v165
	v_pk_mul_f32 v[28:29], v[28:29], v[168:169]
	v_mov_b32_e32 v132, v130
	v_mov_b32_e32 v133, v131
	s_nop 1
	v_permlane32_swap_b32_e32 v130, v132
	v_permlane32_swap_b32_e32 v131, v133
	v_pk_fma_f32 v[60:61], v[212:213], s[2:3], v[60:61] op_sel_hi:[1,0,1]
	v_pk_fma_f32 v[44:45], v[194:195], s[2:3], v[44:45] op_sel_hi:[1,0,1]
	v_pk_fma_f32 v[40:41], v[190:191], s[2:3], v[40:41] op_sel_hi:[1,0,1]
	v_pk_fma_f32 v[36:37], v[186:187], s[2:3], v[36:37] op_sel_hi:[1,0,1]
	v_pk_fma_f32 v[20:21], v[182:183], s[2:3], v[20:21] op_sel_hi:[1,0,1]
	v_pk_fma_f32 v[24:25], v[178:179], s[2:3], v[24:25] op_sel_hi:[1,0,1]
	v_pk_fma_f32 v[16:17], v[174:175], s[2:3], v[16:17] op_sel_hi:[1,0,1]
	v_pk_fma_f32 v[32:33], v[170:171], s[2:3], v[32:33] op_sel_hi:[1,0,1]
	v_pk_fma_f32 v[30:31], v[164:165], s[2:3], v[30:31] op_sel_hi:[1,0,1]
	v_pk_fma_f32 v[28:29], v[166:167], s[2:3], v[28:29] op_sel_hi:[1,0,1]
	s_lshl_b32 s0, s5, 3
	v_cmp_gt_u32_e32 vcc, 16, v197
	s_add_i32 s2, s0, 0
	s_and_saveexec_b64 s[0:1], vcc
	s_cbranch_execz .LBB0_1349
	s_lshl_b32 s5, s3, 11
	s_add_i32 s5, s2, s5
	v_lshl_add_u32 v129, v197, 5, s5
	s_waitcnt lgkmcnt(0)
	v_pk_add_f32 v[130:131], v[130:131], v[132:133]
	ds_write_b64 v129, v[130:131]
.LBB0_1349:
	s_or_b64 exec, exec, s[0:1]
	v_mul_f32_e32 v137, v88, v88
	v_mul_f32_e32 v136, v98, v98
	v_add_f32_e32 v130, v88, v89
	s_waitcnt lgkmcnt(1)
	v_add_f32_e32 v132, v90, v91
	v_mul_f32_e32 v139, v89, v89
	v_mul_f32_e32 v141, v90, v90
	v_mul_f32_e32 v143, v91, v91
	v_mul_f32_e32 v131, v96, v96
	s_waitcnt lgkmcnt(0)
	v_mul_f32_e32 v133, v97, v97
	v_pk_fma_f32 v[146:147], v[98:99], v[98:99], v[136:137] op_sel_hi:[1,1,0]
	v_mov_b32_e32 v136, v96
	v_mov_b32_e32 v138, v97
	v_mov_b32_e32 v140, v98
	v_mov_b32_e32 v142, v99
	v_mul_f32_e32 v149, v108, v108
	v_mul_f32_e32 v151, v109, v109
	v_mul_f32_e32 v153, v110, v110
	v_mul_f32_e32 v155, v111, v111
	v_pk_add_f32 v[136:137], v[136:137], v[138:139]
	v_pk_add_f32 v[138:139], v[140:141], v[142:143]
	v_pk_add_f32 v[130:131], v[130:131], v[132:133]
	v_mov_b32_e32 v129, v147
	v_mov_b32_e32 v148, v108
	v_mov_b32_e32 v150, v109
	v_mov_b32_e32 v152, v110
	v_mov_b32_e32 v154, v111
	v_pk_add_f32 v[136:137], v[136:137], v[138:139]
	v_pk_add_f32 v[128:129], v[130:131], v[128:129]
	v_pk_add_f32 v[130:131], v[148:149], v[150:151]
	v_pk_add_f32 v[132:133], v[152:153], v[154:155]
	v_mul_f32_e32 v157, v112, v112
	v_mul_f32_e32 v159, v113, v113
	v_mul_f32_e32 v161, v114, v114
	v_mul_f32_e32 v163, v115, v115
	v_pk_add_f32 v[128:129], v[136:137], v[128:129]
	v_pk_add_f32 v[130:131], v[130:131], v[132:133]
	v_mov_b32_e32 v156, v112
	v_mov_b32_e32 v158, v113
	v_mov_b32_e32 v160, v114
	v_mov_b32_e32 v162, v115
	v_pk_add_f32 v[128:129], v[130:131], v[128:129]
	v_pk_add_f32 v[130:131], v[156:157], v[158:159]
	v_pk_add_f32 v[132:133], v[160:161], v[162:163]
	s_nop 0
	v_pk_add_f32 v[130:131], v[130:131], v[132:133]
	s_nop 0
	v_pk_add_f32 v[128:129], v[130:131], v[128:129]
	v_mov_b32_e32 v130, v128
	v_mov_b32_e32 v131, v129
	s_nop 1
	v_permlane16_swap_b32_e32 v128, v130
	v_permlane16_swap_b32_e32 v129, v131
	s_waitcnt lgkmcnt(0)
	v_pk_add_f32 v[128:129], v[128:129], v[130:131]
	v_mov_b32_e32 v130, v128
	v_mov_b32_e32 v131, v129
	s_nop 1
	v_permlane32_swap_b32_e32 v128, v130
	v_permlane32_swap_b32_e32 v129, v131
	s_and_saveexec_b64 s[0:1], vcc
	v_readlane_b32 s86, v255, 26
	v_readlane_b32 s87, v255, 27
	s_cbranch_execz .LBB0_1351
	s_lshl_b32 s5, s3, 11
	s_add_i32 s5, s2, s5
	v_lshl_add_u32 v132, v197, 5, s5
	s_waitcnt lgkmcnt(0)
	v_pk_add_f32 v[128:129], v[128:129], v[130:131]
	ds_write_b64 v132, v[128:129] offset:512
.LBB0_1351:
	s_or_b64 exec, exec, s[0:1]
	v_mul_f32_e32 v128, v126, v126
	s_waitcnt lgkmcnt(1)
	v_add_f32_e32 v130, v120, v121
	v_add_f32_e32 v132, v122, v123
	v_mul_f32_e32 v137, v120, v120
	v_mul_f32_e32 v139, v121, v121
	v_mul_f32_e32 v141, v122, v122
	v_mul_f32_e32 v143, v123, v123
	s_waitcnt lgkmcnt(0)
	v_mul_f32_e32 v131, v124, v124
	v_mul_f32_e32 v133, v125, v125
	v_pk_fma_f32 v[128:129], v[126:127], v[126:127], v[128:129] op_sel_hi:[1,1,0]
	v_mov_b32_e32 v136, v124
	v_mov_b32_e32 v138, v125
	v_mov_b32_e32 v140, v126
	v_mov_b32_e32 v142, v127
	v_pk_add_f32 v[136:137], v[136:137], v[138:139]
	v_pk_add_f32 v[138:139], v[140:141], v[142:143]
	v_pk_add_f32 v[130:131], v[130:131], v[132:133]
	v_mov_b32_e32 v128, 0
	v_mul_f32_e32 v147, v116, v116
	v_mul_f32_e32 v149, v117, v117
	v_mul_f32_e32 v151, v118, v118
	v_mul_f32_e32 v153, v119, v119
	v_pk_add_f32 v[136:137], v[136:137], v[138:139]
	v_pk_add_f32 v[130:131], v[130:131], v[128:129]
	v_mov_b32_e32 v146, v116
	v_mov_b32_e32 v148, v117
	v_mov_b32_e32 v150, v118
	v_mov_b32_e32 v152, v119
	v_pk_add_f32 v[130:131], v[136:137], v[130:131]
	v_pk_add_f32 v[132:133], v[146:147], v[148:149]
	v_pk_add_f32 v[136:137], v[150:151], v[152:153]
	v_mul_f32_e32 v155, v104, v104
	v_mul_f32_e32 v157, v105, v105
	v_mul_f32_e32 v159, v106, v106
	v_mul_f32_e32 v161, v107, v107
	v_pk_add_f32 v[132:133], v[132:133], v[136:137]
	v_mov_b32_e32 v154, v104
	v_mov_b32_e32 v156, v105
	v_mov_b32_e32 v158, v106
	v_mov_b32_e32 v160, v107
	v_pk_add_f32 v[130:131], v[132:133], v[130:131]
	v_pk_add_f32 v[132:133], v[154:155], v[156:157]
	v_pk_add_f32 v[136:137], v[158:159], v[160:161]
	s_nop 0
	v_pk_add_f32 v[132:133], v[132:133], v[136:137]
	s_nop 0
	v_pk_add_f32 v[130:131], v[132:133], v[130:131]
	v_mov_b32_e32 v132, v130
	v_mov_b32_e32 v133, v131
	s_nop 1
	v_permlane16_swap_b32_e32 v130, v132
	v_permlane16_swap_b32_e32 v131, v133
	s_waitcnt lgkmcnt(0)
	v_pk_add_f32 v[130:131], v[130:131], v[132:133]
	v_mov_b32_e32 v132, v130
	v_mov_b32_e32 v133, v131
	s_nop 1
	v_permlane32_swap_b32_e32 v130, v132
	v_permlane32_swap_b32_e32 v131, v133
	s_and_saveexec_b64 s[0:1], vcc
	s_cbranch_execz .LBB0_1353
	s_lshl_b32 s5, s3, 11
	s_add_i32 s5, s2, s5
	v_lshl_add_u32 v129, v197, 5, s5
	s_waitcnt lgkmcnt(0)
	v_pk_add_f32 v[130:131], v[130:131], v[132:133]
	ds_write_b64 v129, v[130:131] offset:1024
.LBB0_1353:
	s_or_b64 exec, exec, s[0:1]
	v_mul_f32_e32 v137, v100, v100
	v_mul_f32_e32 v136, v94, v94
	v_add_f32_e32 v130, v100, v101
	s_waitcnt lgkmcnt(1)
	v_add_f32_e32 v132, v102, v103
	v_mul_f32_e32 v139, v101, v101
	v_mul_f32_e32 v141, v102, v102
	v_mul_f32_e32 v143, v103, v103
	v_mul_f32_e32 v131, v92, v92
	s_waitcnt lgkmcnt(0)
	v_mul_f32_e32 v133, v93, v93
	v_pk_fma_f32 v[146:147], v[94:95], v[94:95], v[136:137] op_sel_hi:[1,1,0]
	v_mov_b32_e32 v136, v92
	v_mov_b32_e32 v138, v93
	v_mov_b32_e32 v140, v94
	v_mov_b32_e32 v142, v95
	v_mul_f32_e32 v149, v76, v76
	v_mul_f32_e32 v151, v77, v77
	v_mul_f32_e32 v153, v78, v78
	v_mul_f32_e32 v155, v79, v79
	v_pk_add_f32 v[136:137], v[136:137], v[138:139]
	v_pk_add_f32 v[138:139], v[140:141], v[142:143]
	v_pk_add_f32 v[130:131], v[130:131], v[132:133]
	v_mov_b32_e32 v129, v147
	v_mov_b32_e32 v148, v76
	v_mov_b32_e32 v150, v77
	v_mov_b32_e32 v152, v78
	v_mov_b32_e32 v154, v79
	v_pk_add_f32 v[136:137], v[136:137], v[138:139]
	v_pk_add_f32 v[128:129], v[130:131], v[128:129]
	v_pk_add_f32 v[130:131], v[148:149], v[150:151]
	v_pk_add_f32 v[132:133], v[152:153], v[154:155]
	v_mul_f32_e32 v157, v68, v68
	v_mul_f32_e32 v159, v69, v69
	v_mul_f32_e32 v161, v70, v70
	v_mul_f32_e32 v163, v71, v71
	v_pk_add_f32 v[128:129], v[136:137], v[128:129]
	v_pk_add_f32 v[130:131], v[130:131], v[132:133]
	v_mov_b32_e32 v156, v68
	v_mov_b32_e32 v158, v69
	v_mov_b32_e32 v160, v70
	v_mov_b32_e32 v162, v71
	v_pk_add_f32 v[128:129], v[130:131], v[128:129]
	v_pk_add_f32 v[130:131], v[156:157], v[158:159]
	v_pk_add_f32 v[132:133], v[160:161], v[162:163]
	s_nop 0
	v_pk_add_f32 v[130:131], v[130:131], v[132:133]
	s_nop 0
	v_pk_add_f32 v[128:129], v[130:131], v[128:129]
	v_mov_b32_e32 v130, v128
	v_mov_b32_e32 v131, v129
	s_nop 1
	v_permlane16_swap_b32_e32 v128, v130
	v_permlane16_swap_b32_e32 v129, v131
	s_waitcnt lgkmcnt(0)
	v_pk_add_f32 v[128:129], v[128:129], v[130:131]
	v_mov_b32_e32 v130, v128
	v_mov_b32_e32 v131, v129
	s_nop 1
	v_permlane32_swap_b32_e32 v128, v130
	v_permlane32_swap_b32_e32 v129, v131
	s_and_saveexec_b64 s[0:1], vcc
	s_cbranch_execz .LBB0_1355
	s_lshl_b32 s5, s3, 11
	s_add_i32 s5, s2, s5
	v_lshl_add_u32 v132, v197, 5, s5
	s_waitcnt lgkmcnt(0)
	v_pk_add_f32 v[128:129], v[128:129], v[130:131]
	ds_write_b64 v132, v[128:129] offset:1536
.LBB0_1355:
	s_or_b64 exec, exec, s[0:1]
	v_mul_f32_e32 v128, v58, v58
	s_waitcnt lgkmcnt(1)
	v_add_f32_e32 v130, v60, v61
	v_add_f32_e32 v132, v62, v63
	v_mul_f32_e32 v137, v60, v60
	v_mul_f32_e32 v139, v61, v61
	v_mul_f32_e32 v141, v62, v62
	v_mul_f32_e32 v143, v63, v63
	s_waitcnt lgkmcnt(0)
	v_mul_f32_e32 v131, v56, v56
	v_mul_f32_e32 v133, v57, v57
	v_pk_fma_f32 v[128:129], v[58:59], v[58:59], v[128:129] op_sel_hi:[1,1,0]
	v_mov_b32_e32 v136, v56
	v_mov_b32_e32 v138, v57
	v_mov_b32_e32 v140, v58
	v_mov_b32_e32 v142, v59
	v_pk_add_f32 v[136:137], v[136:137], v[138:139]
	v_pk_add_f32 v[138:139], v[140:141], v[142:143]
	v_pk_add_f32 v[130:131], v[130:131], v[132:133]
	v_mov_b32_e32 v128, 0
	v_mul_f32_e32 v147, v52, v52
	v_mul_f32_e32 v149, v53, v53
	v_mul_f32_e32 v151, v54, v54
	v_mul_f32_e32 v153, v55, v55
	v_pk_add_f32 v[136:137], v[136:137], v[138:139]
	v_pk_add_f32 v[130:131], v[130:131], v[128:129]
	v_mov_b32_e32 v146, v52
	v_mov_b32_e32 v148, v53
	v_mov_b32_e32 v150, v54
	v_mov_b32_e32 v152, v55
	v_pk_add_f32 v[130:131], v[136:137], v[130:131]
	v_pk_add_f32 v[132:133], v[146:147], v[148:149]
	v_pk_add_f32 v[136:137], v[150:151], v[152:153]
	v_mul_f32_e32 v155, v48, v48
	v_mul_f32_e32 v157, v49, v49
	v_mul_f32_e32 v159, v50, v50
	v_mul_f32_e32 v161, v51, v51
	v_pk_add_f32 v[132:133], v[132:133], v[136:137]
	v_mov_b32_e32 v154, v48
	v_mov_b32_e32 v156, v49
	v_mov_b32_e32 v158, v50
	v_mov_b32_e32 v160, v51
	v_pk_add_f32 v[130:131], v[132:133], v[130:131]
	v_pk_add_f32 v[132:133], v[154:155], v[156:157]
	v_pk_add_f32 v[136:137], v[158:159], v[160:161]
	s_nop 0
	v_pk_add_f32 v[132:133], v[132:133], v[136:137]
	s_nop 0
	v_pk_add_f32 v[130:131], v[132:133], v[130:131]
	v_mov_b32_e32 v132, v130
	v_mov_b32_e32 v133, v131
	s_nop 1
	v_permlane16_swap_b32_e32 v130, v132
	v_permlane16_swap_b32_e32 v131, v133
	s_waitcnt lgkmcnt(0)
	v_pk_add_f32 v[130:131], v[130:131], v[132:133]
	v_mov_b32_e32 v132, v130
	v_mov_b32_e32 v133, v131
	s_nop 1
	v_permlane32_swap_b32_e32 v130, v132
	v_permlane32_swap_b32_e32 v131, v133
	s_and_saveexec_b64 s[0:1], vcc
	s_cbranch_execz .LBB0_1357
	s_lshl_b32 s5, s3, 11
	s_add_i32 s5, s2, s5
	v_lshl_add_u32 v129, v197, 5, s5
	s_waitcnt lgkmcnt(0)
	v_pk_add_f32 v[130:131], v[130:131], v[132:133]
	ds_write_b64 v129, v[130:131] offset:4096
.LBB0_1357:
	s_or_b64 exec, exec, s[0:1]
	v_mul_f32_e32 v137, v44, v44
	v_mul_f32_e32 v136, v42, v42
	v_add_f32_e32 v130, v44, v45
	s_waitcnt lgkmcnt(1)
	v_add_f32_e32 v132, v46, v47
	v_mul_f32_e32 v139, v45, v45
	v_mul_f32_e32 v141, v46, v46
	v_mul_f32_e32 v143, v47, v47
	v_mul_f32_e32 v131, v40, v40
	s_waitcnt lgkmcnt(0)
	v_mul_f32_e32 v133, v41, v41
	v_pk_fma_f32 v[146:147], v[42:43], v[42:43], v[136:137] op_sel_hi:[1,1,0]
	v_mov_b32_e32 v136, v40
	v_mov_b32_e32 v138, v41
	v_mov_b32_e32 v140, v42
	v_mov_b32_e32 v142, v43
	v_mul_f32_e32 v149, v36, v36
	v_mul_f32_e32 v151, v37, v37
	v_mul_f32_e32 v153, v38, v38
	v_mul_f32_e32 v155, v39, v39
	v_pk_add_f32 v[136:137], v[136:137], v[138:139]
	v_pk_add_f32 v[138:139], v[140:141], v[142:143]
	v_pk_add_f32 v[130:131], v[130:131], v[132:133]
	v_mov_b32_e32 v129, v147
	v_mov_b32_e32 v148, v36
	v_mov_b32_e32 v150, v37
	v_mov_b32_e32 v152, v38
	v_mov_b32_e32 v154, v39
	v_pk_add_f32 v[136:137], v[136:137], v[138:139]
	v_pk_add_f32 v[128:129], v[130:131], v[128:129]
	v_pk_add_f32 v[130:131], v[148:149], v[150:151]
	v_pk_add_f32 v[132:133], v[152:153], v[154:155]
	v_mul_f32_e32 v157, v20, v20
	v_mul_f32_e32 v159, v21, v21
	v_mul_f32_e32 v161, v22, v22
	v_mul_f32_e32 v163, v23, v23
	v_pk_add_f32 v[128:129], v[136:137], v[128:129]
	v_pk_add_f32 v[130:131], v[130:131], v[132:133]
	v_mov_b32_e32 v156, v20
	v_mov_b32_e32 v158, v21
	v_mov_b32_e32 v160, v22
	v_mov_b32_e32 v162, v23
	v_pk_add_f32 v[128:129], v[130:131], v[128:129]
	v_pk_add_f32 v[130:131], v[156:157], v[158:159]
	v_pk_add_f32 v[132:133], v[160:161], v[162:163]
	s_nop 0
	v_pk_add_f32 v[130:131], v[130:131], v[132:133]
	s_nop 0
	v_pk_add_f32 v[128:129], v[130:131], v[128:129]
	v_mov_b32_e32 v130, v128
	v_mov_b32_e32 v131, v129
	s_nop 1
	v_permlane16_swap_b32_e32 v128, v130
	v_permlane16_swap_b32_e32 v129, v131
	s_waitcnt lgkmcnt(0)
	v_pk_add_f32 v[128:129], v[128:129], v[130:131]
	v_mov_b32_e32 v130, v128
	v_mov_b32_e32 v131, v129
	s_nop 1
	v_permlane32_swap_b32_e32 v128, v130
	v_permlane32_swap_b32_e32 v129, v131
	s_and_saveexec_b64 s[0:1], vcc
	s_cbranch_execz .LBB0_1359
	s_lshl_b32 s5, s3, 11
	s_add_i32 s5, s2, s5
	v_lshl_add_u32 v132, v197, 5, s5
	s_waitcnt lgkmcnt(0)
	v_pk_add_f32 v[128:129], v[128:129], v[130:131]
	ds_write_b64 v132, v[128:129] offset:4608
.LBB0_1359:
	s_or_b64 exec, exec, s[0:1]
	v_mul_f32_e32 v128, v18, v18
	s_waitcnt lgkmcnt(1)
	v_add_f32_e32 v130, v24, v25
	v_add_f32_e32 v132, v26, v27
	v_mul_f32_e32 v137, v24, v24
	v_mul_f32_e32 v139, v25, v25
	v_mul_f32_e32 v141, v26, v26
	v_mul_f32_e32 v143, v27, v27
	s_waitcnt lgkmcnt(0)
	v_mul_f32_e32 v131, v16, v16
	v_mul_f32_e32 v133, v17, v17
	v_pk_fma_f32 v[128:129], v[18:19], v[18:19], v[128:129] op_sel_hi:[1,1,0]
	v_mov_b32_e32 v136, v16
	v_mov_b32_e32 v138, v17
	v_mov_b32_e32 v140, v18
	v_mov_b32_e32 v142, v19
	v_pk_add_f32 v[136:137], v[136:137], v[138:139]
	v_pk_add_f32 v[138:139], v[140:141], v[142:143]
	v_pk_add_f32 v[130:131], v[130:131], v[132:133]
	v_mov_b32_e32 v128, 0
	v_mul_f32_e32 v147, v32, v32
	v_mul_f32_e32 v149, v33, v33
	v_mul_f32_e32 v151, v34, v34
	v_mul_f32_e32 v153, v35, v35
	v_pk_add_f32 v[136:137], v[136:137], v[138:139]
	v_pk_add_f32 v[130:131], v[130:131], v[128:129]
	v_mov_b32_e32 v146, v32
	v_mov_b32_e32 v148, v33
	v_mov_b32_e32 v150, v34
	v_mov_b32_e32 v152, v35
	v_pk_add_f32 v[130:131], v[136:137], v[130:131]
	v_pk_add_f32 v[132:133], v[146:147], v[148:149]
	v_pk_add_f32 v[136:137], v[150:151], v[152:153]
	v_mul_f32_e32 v155, v28, v28
	v_mul_f32_e32 v157, v29, v29
	v_mul_f32_e32 v159, v30, v30
	v_mul_f32_e32 v161, v31, v31
	v_pk_add_f32 v[132:133], v[132:133], v[136:137]
	v_mov_b32_e32 v154, v28
	v_mov_b32_e32 v156, v29
	v_mov_b32_e32 v158, v30
	v_mov_b32_e32 v160, v31
	v_pk_add_f32 v[130:131], v[132:133], v[130:131]
	v_pk_add_f32 v[132:133], v[154:155], v[156:157]
	v_pk_add_f32 v[136:137], v[158:159], v[160:161]
	s_nop 0
	v_pk_add_f32 v[132:133], v[132:133], v[136:137]
	s_nop 0
	v_pk_add_f32 v[130:131], v[132:133], v[130:131]
	v_mov_b32_e32 v132, v130
	v_mov_b32_e32 v133, v131
	s_nop 1
	v_permlane16_swap_b32_e32 v130, v132
	v_permlane16_swap_b32_e32 v131, v133
	s_waitcnt lgkmcnt(0)
	v_pk_add_f32 v[130:131], v[130:131], v[132:133]
	v_mov_b32_e32 v132, v130
	v_mov_b32_e32 v133, v131
	s_nop 1
	v_permlane32_swap_b32_e32 v130, v132
	v_permlane32_swap_b32_e32 v131, v133
	s_and_saveexec_b64 s[0:1], vcc
	s_cbranch_execz .LBB0_1361
	s_lshl_b32 s5, s3, 11
	s_add_i32 s5, s2, s5
	v_lshl_add_u32 v129, v197, 5, s5
	s_waitcnt lgkmcnt(0)
	v_pk_add_f32 v[130:131], v[130:131], v[132:133]
	ds_write_b64 v129, v[130:131] offset:5120
.LBB0_1361:
	s_or_b64 exec, exec, s[0:1]
	v_mul_f32_e32 v137, v4, v4
	v_mul_f32_e32 v136, v2, v2
	v_add_f32_e32 v130, v4, v5
	s_waitcnt lgkmcnt(1)
	v_add_f32_e32 v132, v6, v7
	v_mul_f32_e32 v139, v5, v5
	v_mul_f32_e32 v141, v6, v6
	v_mul_f32_e32 v143, v7, v7
	v_mul_f32_e32 v131, v0, v0
	s_waitcnt lgkmcnt(0)
	v_mul_f32_e32 v133, v1, v1
	v_pk_fma_f32 v[146:147], v[2:3], v[2:3], v[136:137] op_sel_hi:[1,1,0]
	v_mov_b32_e32 v136, v0
	v_mov_b32_e32 v138, v1
	v_mov_b32_e32 v140, v2
	v_mov_b32_e32 v142, v3
	v_mul_f32_e32 v149, v12, v12
	v_mul_f32_e32 v151, v13, v13
	v_mul_f32_e32 v153, v14, v14
	v_mul_f32_e32 v155, v15, v15
	v_pk_add_f32 v[136:137], v[136:137], v[138:139]
	v_pk_add_f32 v[138:139], v[140:141], v[142:143]
	v_pk_add_f32 v[130:131], v[130:131], v[132:133]
	v_mov_b32_e32 v129, v147
	v_mov_b32_e32 v148, v12
	v_mov_b32_e32 v150, v13
	v_mov_b32_e32 v152, v14
	v_mov_b32_e32 v154, v15
	v_pk_add_f32 v[136:137], v[136:137], v[138:139]
	v_pk_add_f32 v[128:129], v[130:131], v[128:129]
	v_pk_add_f32 v[130:131], v[148:149], v[150:151]
	v_pk_add_f32 v[132:133], v[152:153], v[154:155]
	v_mul_f32_e32 v157, v8, v8
	v_mul_f32_e32 v159, v9, v9
	v_mul_f32_e32 v161, v10, v10
	v_mul_f32_e32 v163, v11, v11
	v_pk_add_f32 v[128:129], v[136:137], v[128:129]
	v_pk_add_f32 v[130:131], v[130:131], v[132:133]
	v_mov_b32_e32 v156, v8
	v_mov_b32_e32 v158, v9
	v_mov_b32_e32 v160, v10
	v_mov_b32_e32 v162, v11
	v_pk_add_f32 v[128:129], v[130:131], v[128:129]
	v_pk_add_f32 v[130:131], v[156:157], v[158:159]
	v_pk_add_f32 v[132:133], v[160:161], v[162:163]
	s_nop 0
	v_pk_add_f32 v[130:131], v[130:131], v[132:133]
	s_nop 0
	v_pk_add_f32 v[128:129], v[130:131], v[128:129]
	v_mov_b32_e32 v130, v128
	v_mov_b32_e32 v131, v129
	s_nop 1
	v_permlane16_swap_b32_e32 v128, v130
	v_permlane16_swap_b32_e32 v129, v131
	s_waitcnt lgkmcnt(0)
	v_pk_add_f32 v[128:129], v[128:129], v[130:131]
	v_mov_b32_e32 v130, v128
	v_mov_b32_e32 v131, v129
	s_nop 1
	v_permlane32_swap_b32_e32 v128, v130
	v_permlane32_swap_b32_e32 v129, v131
	s_and_saveexec_b64 s[0:1], vcc
	s_cbranch_execz .LBB0_1363
	s_lshl_b32 s3, s3, 11
	s_add_i32 s2, s2, s3
	v_lshl_add_u32 v132, v197, 5, s2
	s_waitcnt lgkmcnt(0)
	v_pk_add_f32 v[128:129], v[128:129], v[130:131]
	ds_write_b64 v132, v[128:129] offset:5632
